# v46 + all 9 GEMM K-loops: K-iteration 0 peeled with first-touch MFMAs taking C=0 (128-VALU accumulator zeroing deleted per unit); G5 next-unit header consumption deferred to after the peeled iteration
# speedup vs baseline: 1.0065x; 1.0031x over previous
; #define PG8_GIDX(G_, PM_) do { if constexpr (Sched::GATHER) { _Pragma("unroll") for (int h_ = 0; h_ < 2; ++h_) _Pragma("unroll") for (int i_ = 0; i_ < 2; ++i_) { int R_, C_; stage_rc(tid * 16 + i_ * 8192, R_, C_); \
;         const int src_ = S.rowsrc[(PM_) * BM + h_ * HALF + R_]; G_[h_][i_] = (unsigned)(src_ * K + C_) * 2u; } } } while (0)
; #define PG8_WAIT_V(n) asm volatile("s_waitcnt vmcnt(" #n ")" ::: "memory")
; template <class Epi, class Sched, bool ALIGN_EPI = false, bool SP2 = false>
; __device__ __forceinline__ void gemm_phase(PG8_LAS unsigned char* lds, const Gemm g, const Sched& S, const Epi& E, const bool skip_epi = false) {
;     ...
;     for (;;) {
;         const bool has_next = S.next(ui + 1, nxt);
;         if (has_next) PG8_GIDX(gN, nxt.pm);
;         const char* nA = has_next ? (const char*)g.A + (size_t)nxt.pm * pmstepA + nxt.ko : cA; const char* nB = has_next ? (const char*)g.Bt + (size_t)nxt.pn * tstep + nxt.ko : cB;
;         for (int t = 0; t < nt; t += 2) {
;             const bool last = (t == nt - 2); last_ = last && has_next;
;             const char* a1 = cA + (size_t)(t + 1) * kstep;
;             const char* a2 = last ? nA : cA + (size_t)(t + 2) * kstep; const char* b2 = last ? nB : cB + (size_t)(t + 2) * kstep;
;             const char* a3 = a2 + kstep; const char* b3 = b2 + kstep;
;             if (last && has_next) S.a_ready(nxt);
;             if constexpr (SP2) {
;             PG8_LDB(B0, 0, 0); PG8_LDB(B1, 0, 1); PG8_SCHED; PG8_LDA(At, 0, 0); PG8_STAGE_A(1, 1, a1, false);
;             PG8_WAIT_V(8); PG8_WAIT_L(0); PG8_BAR; PG8_MMA(0, 0, At, B0); PG8_MMA(0, 1, At, B1); PG8_BAR; PG8_SCHED;
;             PG8_LDA(At, 0, 1); PG8_STAGE(PG8_SB(0, 0), b2, voffB); PG8_STAGE(PG8_SB(0, 1), b2 + hstep, voffB); PG8_STAGE_A(0, 0, a2, true);
;             PG8_WAIT_V(8); PG8_WAIT_L(0); PG8_BAR; PG8_MMA(1, 0, At, B0); PG8_MMA(1, 1, At, B1); PG8_BAR; PG8_SCHED;
;             PG8_LDB(B0, 1, 0); PG8_LDB(B1, 1, 1); PG8_SCHED; PG8_LDA(At, 1, 0); PG8_STAGE_A(0, 1, a2, true);
;             PG8_WAIT_V(8); PG8_WAIT_L(0); PG8_BAR; PG8_MMA(0, 0, At, B0); PG8_MMA(0, 1, At, B1); PG8_BAR; PG8_SCHED;
;             PG8_LDA(At, 1, 1); PG8_STAGE(PG8_SB(1, 0), b3, voffB); PG8_STAGE(PG8_SB(1, 1), b3 + hstep, voffB); PG8_STAGE_A(1, 0, a3, true);
;             PG8_WAIT_V(8); PG8_WAIT_L(0); PG8_BAR; PG8_MMA(1, 0, At, B0); PG8_MMA(1, 1, At, B1); PG8_BAR; PG8_SCHED;
.LBB0_252:
	s_ashr_i32 s17, s16, 31
	s_lshl_b64 s[18:19], s[16:17], 19
	s_add_u32 s18, s86, s18
	s_addc_u32 s19, s87, s19
	s_and_b64 s[20:21], s[4:5], exec
	s_cselect_b32 s17, s19, s25
	s_cselect_b32 s56, s18, s24
	s_ashr_i32 s15, s14, 31
	s_lshl_b64 s[20:21], s[14:15], 19
	v_readlane_b32 s28, v254, 36
	v_readlane_b32 s29, v254, 37
	s_add_u32 s20, s28, s20
	s_addc_u32 s21, s29, s21
	s_and_b64 s[28:29], s[4:5], exec
	s_cselect_b32 s15, s21, s27
	s_cselect_b32 s57, s20, s26
	s_add_u32 s24, s24, 0x40080
	s_addc_u32 s25, s25, 0
	s_add_u32 s58, s26, 0x100
	s_addc_u32 s59, s27, 0
	s_mov_b32 s60, -2
	s_waitcnt vmcnt(0)
	ds_read_b128 v[148:151], v170
	ds_read_b128 v[152:155], v170 offset:1024
	ds_read_b128 v[156:159], v170 offset:2048
	ds_read_b128 v[160:163], v170 offset:3072
	ds_read_b128 v[176:179], v171
	ds_read_b128 v[180:183], v171 offset:1024
	ds_read_b128 v[184:187], v171 offset:2048
	ds_read_b128 v[188:191], v171 offset:3072
	s_add_u32 s26, s24, 0xfffc0080
	s_addc_u32 s27, s25, -1
	s_cmp_eq_u32 s60, 12
	s_cselect_b32 s29, s17, s27
	s_cselect_b32 s28, s56, s26
	s_cselect_b32 s27, s15, s59
	s_cselect_b32 s26, s57, s58
	v_lshl_add_u64 v[164:165], s[24:25], 0, v[140:141]
	s_add_i32 m0, s23, 0xc000
	ds_read_b128 v[192:195], v172
	ds_read_b128 v[196:199], v172 offset:1024
	ds_read_b128 v[200:203], v172 offset:2048
	ds_read_b128 v[204:207], v172 offset:3072
	ds_read_b128 v[208:211], v172 offset:4096
	ds_read_b128 v[212:215], v172 offset:5120
	ds_read_b128 v[216:219], v172 offset:6144
	ds_read_b128 v[220:223], v172 offset:7168
	global_load_lds_dwordx4 v[164:165], off
	v_lshl_add_u64 v[164:165], s[24:25], 0, v[142:143]
	s_add_i32 m0, s23, 0xe000
	s_nop 0
	global_load_lds_dwordx4 v[164:165], off
	s_waitcnt vmcnt(8)
	s_waitcnt lgkmcnt(0)
	s_barrier
	s_setprio 1
	s_waitcnt lgkmcnt(0)
	v_mfma_f32_16x16x32_bf16 v[126:129], v[148:151], v[192:195], 0
	v_mfma_f32_16x16x32_bf16 v[122:125], v[156:159], v[192:195], 0
	v_mfma_f32_16x16x32_bf16 v[114:117], v[148:151], v[200:203], 0
	v_mfma_f32_16x16x32_bf16 v[106:109], v[156:159], v[200:203], 0
	v_mfma_f32_16x16x32_bf16 v[98:101], v[148:151], v[208:211], 0
	v_mfma_f32_16x16x32_bf16 v[90:93], v[156:159], v[208:211], 0
	v_mfma_f32_16x16x32_bf16 v[82:85], v[148:151], v[216:219], 0
	v_mfma_f32_16x16x32_bf16 v[74:77], v[156:159], v[216:219], 0
	v_mfma_f32_16x16x32_bf16 v[126:129], v[152:155], v[196:199], v[126:129]
	v_mfma_f32_16x16x32_bf16 v[122:125], v[160:163], v[196:199], v[122:125]
	v_mfma_f32_16x16x32_bf16 v[114:117], v[152:155], v[204:207], v[114:117]
	v_mfma_f32_16x16x32_bf16 v[106:109], v[160:163], v[204:207], v[106:109]
	v_mfma_f32_16x16x32_bf16 v[98:101], v[152:155], v[212:215], v[98:101]
	v_mfma_f32_16x16x32_bf16 v[90:93], v[160:163], v[212:215], v[90:93]
	v_mfma_f32_16x16x32_bf16 v[82:85], v[152:155], v[220:223], v[82:85]
	v_mfma_f32_16x16x32_bf16 v[74:77], v[160:163], v[220:223], v[74:77]
	s_setprio 0
	s_setprio 1
	v_mfma_f32_16x16x32_bf16 v[118:121], v[176:179], v[192:195], 0
	v_mfma_f32_16x16x32_bf16 v[110:113], v[184:187], v[192:195], 0
	v_mfma_f32_16x16x32_bf16 v[102:105], v[176:179], v[200:203], 0
	v_mfma_f32_16x16x32_bf16 v[94:97], v[184:187], v[200:203], 0
	v_mfma_f32_16x16x32_bf16 v[86:89], v[176:179], v[208:211], 0
	v_mfma_f32_16x16x32_bf16 v[78:81], v[184:187], v[208:211], 0
	v_mfma_f32_16x16x32_bf16 v[70:73], v[176:179], v[216:219], 0
	v_mfma_f32_16x16x32_bf16 v[66:69], v[184:187], v[216:219], 0
	v_mfma_f32_16x16x32_bf16 v[118:121], v[180:183], v[196:199], v[118:121]
	v_mfma_f32_16x16x32_bf16 v[110:113], v[188:191], v[196:199], v[110:113]
	v_mfma_f32_16x16x32_bf16 v[102:105], v[180:183], v[204:207], v[102:105]
	v_mfma_f32_16x16x32_bf16 v[94:97], v[188:191], v[204:207], v[94:97]
	v_mfma_f32_16x16x32_bf16 v[86:89], v[180:183], v[212:215], v[86:89]
	v_mfma_f32_16x16x32_bf16 v[78:81], v[188:191], v[212:215], v[78:81]
	v_mfma_f32_16x16x32_bf16 v[70:73], v[180:183], v[220:223], v[70:73]
	v_mfma_f32_16x16x32_bf16 v[66:69], v[188:191], v[220:223], v[66:69]
	s_setprio 0
	s_barrier
	s_add_i32 s61, s46, s2
	v_lshl_add_u64 v[164:165], s[26:27], 0, v[134:135]
	s_mov_b32 m0, s61
	ds_read_b128 v[192:195], v172 offset:16384
	ds_read_b128 v[196:199], v172 offset:17408
	ds_read_b128 v[200:203], v172 offset:18432
	ds_read_b128 v[204:207], v172 offset:19456
	ds_read_b128 v[208:211], v172 offset:20480
	ds_read_b128 v[212:215], v172 offset:21504
	ds_read_b128 v[216:219], v172 offset:22528
	ds_read_b128 v[220:223], v172 offset:23552
	global_load_lds_dwordx4 v[164:165], off
	s_add_i32 m0, s61, 0x2000
	s_add_u32 s62, s26, 0x40000
	v_lshl_add_u64 v[224:225], s[26:27], 0, v[130:131]
	s_addc_u32 s63, s27, 0
	s_add_i32 s61, s47, s2
	global_load_lds_dwordx4 v[224:225], off
	v_lshl_add_u64 v[226:227], s[62:63], 0, v[134:135]
	s_mov_b32 m0, s61
	v_lshl_add_u64 v[230:231], s[28:29], 0, v[132:133]
	global_load_lds_dwordx4 v[226:227], off
	v_lshl_add_u64 v[226:227], s[62:63], 0, v[130:131]
	s_add_i32 m0, s61, 0x2000
	s_nop 0
	global_load_lds_dwordx4 v[226:227], off
	v_lshl_add_u64 v[226:227], s[28:29], 0, v[136:137]
	s_mov_b32 m0, s23
	s_nop 0
	global_load_lds_dwordx4 v[226:227], off
	s_mov_b32 m0, s31
	s_nop 0
	global_load_lds_dwordx4 v[230:231], off
	s_waitcnt vmcnt(8)
	s_waitcnt lgkmcnt(0)
	s_barrier
; #define PG8_STAGE_A(b, h, ptr, NX) do { if constexpr (Sched::GATHER) { unsigned gs_[2]; gs_[0] = ((NX) && last_) ? gN[h][0] : gA[h][0]; gs_[1] = ((NX) && last_) ? gN[h][1] : gA[h][1]; PG8_STAGE(PG8_SA(b, h), ptr, gs_); } \
;         else PG8_STAGE(PG8_SA(b, h), (ptr) + ((h) ? hstep : (size_t)0), voffA); } while (0)
; #define PG8_STAGE(bufoff, gbase, voff) do { _Pragma("unroll") for (int _i = 0; _i < 2; ++_i) \
;         __builtin_amdgcn_global_load_lds((const unsigned*)((const char*)(gbase) + (voff)[_i]), (PG8_LAS unsigned*)(lds + (bufoff) + ldsw + _i * 8192), 16, 0, 0); } while (0)
; #define PG8_LDA(dst, b, h) do { _Pragma("unroll") for (int m = 0; m < 4; ++m) _Pragma("unroll") for (int k = 0; k < 2; ++k) dst[m][k] = *(const PG8_LAS bf16x8*)(lds + PG8_SA(b, h) + aoff + m * 2048 + k * 1024); } while (0)
; #define PG8_LDB(dst, b, h) do { _Pragma("unroll") for (int n = 0; n < 2; ++n) _Pragma("unroll") for (int k = 0; k < 2; ++k) dst[n][k] = *(const PG8_LAS bf16x8*)(lds + PG8_SB(b, h) + boff + n * 2048 + k * 1024); } while (0)
; #define PG8_MMA(ai, bj, At, Bt) do { __builtin_amdgcn_s_setprio(1); _Pragma("unroll") for (int m = 0; m < 4; ++m) _Pragma("unroll") for (int n = 0; n < 2; ++n) _Pragma("unroll") for (int k = 0; k < 2; ++k) \
;         acc[ai][bj][m][n] = __builtin_amdgcn_mfma_f32_16x16x32_bf16(Bt[n][k], At[m][k], acc[ai][bj][m][n], 0, 0, 0); __builtin_amdgcn_s_setprio(0); } while (0)
; #define PG8_WAIT_V(n) asm volatile("s_waitcnt vmcnt(" #n ")" ::: "memory")
; #define PG8_WAIT_L(n) asm volatile("s_waitcnt lgkmcnt(" #n ")" ::: "memory")
; #define PG8_BAR __builtin_amdgcn_s_barrier()
; #define PG8_SCHED __builtin_amdgcn_sched_barrier(0)
; template <class Epi, class Sched, bool ALIGN_EPI = false, bool SP2 = false>
; __device__ __forceinline__ void gemm_phase(PG8_LAS unsigned char* lds, const Gemm g, const Sched& S, const Epi& E, const bool skip_epi = false) {
;     ...
;             PG8_WAIT_V(8); PG8_WAIT_L(0); PG8_BAR; PG8_MMA(1, 0, At, B0); PG8_MMA(1, 1, At, B1); PG8_BAR; PG8_SCHED;
;             PG8_LDB(B0, 1, 0); PG8_LDB(B1, 1, 1); PG8_SCHED; PG8_LDA(At, 1, 0); PG8_STAGE_A(0, 1, a2, true);
;             PG8_WAIT_V(8); PG8_WAIT_L(0); PG8_BAR; PG8_MMA(0, 0, At, B0); PG8_MMA(0, 1, At, B1); PG8_BAR; PG8_SCHED;
;             PG8_LDA(At, 1, 1); PG8_STAGE(PG8_SB(1, 0), b3, voffB); PG8_STAGE(PG8_SB(1, 1), b3 + hstep, voffB); PG8_STAGE_A(1, 0, a3, true);
	s_setprio 1
	s_waitcnt lgkmcnt(0)
	v_mfma_f32_16x16x32_bf16 v[62:65], v[148:151], v[192:195], 0
	v_mfma_f32_16x16x32_bf16 v[58:61], v[156:159], v[192:195], 0
	v_mfma_f32_16x16x32_bf16 v[50:53], v[148:151], v[200:203], 0
	v_mfma_f32_16x16x32_bf16 v[42:45], v[156:159], v[200:203], 0
	v_mfma_f32_16x16x32_bf16 v[34:37], v[148:151], v[208:211], 0
	v_mfma_f32_16x16x32_bf16 v[26:29], v[156:159], v[208:211], 0
	v_mfma_f32_16x16x32_bf16 v[18:21], v[148:151], v[216:219], 0
	v_mfma_f32_16x16x32_bf16 v[10:13], v[156:159], v[216:219], 0
	v_mfma_f32_16x16x32_bf16 v[62:65], v[152:155], v[196:199], v[62:65]
	v_mfma_f32_16x16x32_bf16 v[58:61], v[160:163], v[196:199], v[58:61]
	v_mfma_f32_16x16x32_bf16 v[50:53], v[152:155], v[204:207], v[50:53]
	v_mfma_f32_16x16x32_bf16 v[42:45], v[160:163], v[204:207], v[42:45]
	v_mfma_f32_16x16x32_bf16 v[34:37], v[152:155], v[212:215], v[34:37]
	v_mfma_f32_16x16x32_bf16 v[26:29], v[160:163], v[212:215], v[26:29]
	v_mfma_f32_16x16x32_bf16 v[18:21], v[152:155], v[220:223], v[18:21]
	v_mfma_f32_16x16x32_bf16 v[10:13], v[160:163], v[220:223], v[10:13]
	s_setprio 0
	s_setprio 1
	v_mfma_f32_16x16x32_bf16 v[54:57], v[176:179], v[192:195], 0
	v_mfma_f32_16x16x32_bf16 v[46:49], v[184:187], v[192:195], 0
	v_mfma_f32_16x16x32_bf16 v[38:41], v[176:179], v[200:203], 0
	v_mfma_f32_16x16x32_bf16 v[30:33], v[184:187], v[200:203], 0
	v_mfma_f32_16x16x32_bf16 v[22:25], v[176:179], v[208:211], 0
	v_mfma_f32_16x16x32_bf16 v[14:17], v[184:187], v[208:211], 0
	v_mfma_f32_16x16x32_bf16 v[6:9], v[176:179], v[216:219], 0
	v_mfma_f32_16x16x32_bf16 v[2:5], v[184:187], v[216:219], 0
	v_mfma_f32_16x16x32_bf16 v[54:57], v[180:183], v[196:199], v[54:57]
	v_mfma_f32_16x16x32_bf16 v[46:49], v[188:191], v[196:199], v[46:49]
	v_mfma_f32_16x16x32_bf16 v[38:41], v[180:183], v[204:207], v[38:41]
	v_mfma_f32_16x16x32_bf16 v[30:33], v[188:191], v[204:207], v[30:33]
	v_mfma_f32_16x16x32_bf16 v[22:25], v[180:183], v[212:215], v[22:25]
	v_mfma_f32_16x16x32_bf16 v[14:17], v[188:191], v[212:215], v[14:17]
	v_mfma_f32_16x16x32_bf16 v[6:9], v[180:183], v[220:223], v[6:9]
	v_mfma_f32_16x16x32_bf16 v[2:5], v[188:191], v[220:223], v[2:5]
	s_setprio 0
	s_barrier
	s_add_i32 s61, 0, 0x18000
	s_add_i32 s62, 0, 0x1c000
	v_add_u32_e32 v160, s61, v1
	v_add_u32_e32 v188, s62, v1
	ds_read_b128 v[148:151], v160
	ds_read_b128 v[152:155], v160 offset:1024
	ds_read_b128 v[156:159], v160 offset:2048
	ds_read_b128 v[160:163], v160 offset:3072
	ds_read_b128 v[176:179], v188
	ds_read_b128 v[180:183], v188 offset:1024
	ds_read_b128 v[184:187], v188 offset:2048
	ds_read_b128 v[188:191], v188 offset:3072
	s_add_u32 s28, s28, 0x40000
	s_addc_u32 s29, s29, 0
	s_mov_b32 m0, s34
	v_lshl_add_u64 v[232:233], s[28:29], 0, v[136:137]
	ds_read_b128 v[192:195], v172 offset:32768
	ds_read_b128 v[196:199], v172 offset:33792
	ds_read_b128 v[200:203], v172 offset:34816
	ds_read_b128 v[204:207], v172 offset:35840
	ds_read_b128 v[208:211], v172 offset:36864
	ds_read_b128 v[212:215], v172 offset:37888
	ds_read_b128 v[216:219], v172 offset:38912
	ds_read_b128 v[220:223], v172 offset:39936
	global_load_lds_dwordx4 v[232:233], off
	v_lshl_add_u64 v[232:233], s[28:29], 0, v[132:133]
	s_mov_b32 m0, s35
	s_nop 0
	global_load_lds_dwordx4 v[232:233], off
	s_waitcnt vmcnt(8)
	s_waitcnt lgkmcnt(0)
	s_barrier
	s_setprio 1
	s_waitcnt lgkmcnt(0)
	v_mfma_f32_16x16x32_bf16 v[126:129], v[148:151], v[192:195], v[126:129]
	v_mfma_f32_16x16x32_bf16 v[122:125], v[156:159], v[192:195], v[122:125]
	v_mfma_f32_16x16x32_bf16 v[114:117], v[148:151], v[200:203], v[114:117]
	v_mfma_f32_16x16x32_bf16 v[106:109], v[156:159], v[200:203], v[106:109]
	v_mfma_f32_16x16x32_bf16 v[98:101], v[148:151], v[208:211], v[98:101]
	v_mfma_f32_16x16x32_bf16 v[90:93], v[156:159], v[208:211], v[90:93]
	v_mfma_f32_16x16x32_bf16 v[82:85], v[148:151], v[216:219], v[82:85]
	v_mfma_f32_16x16x32_bf16 v[74:77], v[156:159], v[216:219], v[74:77]
	v_mfma_f32_16x16x32_bf16 v[126:129], v[152:155], v[196:199], v[126:129]
	v_mfma_f32_16x16x32_bf16 v[122:125], v[160:163], v[196:199], v[122:125]
	v_mfma_f32_16x16x32_bf16 v[114:117], v[152:155], v[204:207], v[114:117]
	v_mfma_f32_16x16x32_bf16 v[106:109], v[160:163], v[204:207], v[106:109]
	v_mfma_f32_16x16x32_bf16 v[98:101], v[152:155], v[212:215], v[98:101]
	v_mfma_f32_16x16x32_bf16 v[90:93], v[160:163], v[212:215], v[90:93]
	v_mfma_f32_16x16x32_bf16 v[82:85], v[152:155], v[220:223], v[82:85]
	v_mfma_f32_16x16x32_bf16 v[74:77], v[160:163], v[220:223], v[74:77]
	s_setprio 0
	s_setprio 1
	v_mfma_f32_16x16x32_bf16 v[118:121], v[176:179], v[192:195], v[118:121]
	v_mfma_f32_16x16x32_bf16 v[110:113], v[184:187], v[192:195], v[110:113]
	v_mfma_f32_16x16x32_bf16 v[102:105], v[176:179], v[200:203], v[102:105]
	v_mfma_f32_16x16x32_bf16 v[94:97], v[184:187], v[200:203], v[94:97]
	v_mfma_f32_16x16x32_bf16 v[86:89], v[176:179], v[208:211], v[86:89]
	v_mfma_f32_16x16x32_bf16 v[78:81], v[184:187], v[208:211], v[78:81]
	v_mfma_f32_16x16x32_bf16 v[70:73], v[176:179], v[216:219], v[70:73]
	v_mfma_f32_16x16x32_bf16 v[66:69], v[184:187], v[216:219], v[66:69]
	v_mfma_f32_16x16x32_bf16 v[118:121], v[180:183], v[196:199], v[118:121]
	v_mfma_f32_16x16x32_bf16 v[110:113], v[188:191], v[196:199], v[110:113]
	v_mfma_f32_16x16x32_bf16 v[102:105], v[180:183], v[204:207], v[102:105]
	v_mfma_f32_16x16x32_bf16 v[94:97], v[188:191], v[204:207], v[94:97]
	v_mfma_f32_16x16x32_bf16 v[86:89], v[180:183], v[212:215], v[86:89]
	v_mfma_f32_16x16x32_bf16 v[78:81], v[188:191], v[212:215], v[78:81]
	v_mfma_f32_16x16x32_bf16 v[70:73], v[180:183], v[220:223], v[70:73]
	v_mfma_f32_16x16x32_bf16 v[66:69], v[188:191], v[220:223], v[66:69]
	s_setprio 0
	s_barrier
; #define PG8_STAGE_A(b, h, ptr, NX) do { if constexpr (Sched::GATHER) { unsigned gs_[2]; gs_[0] = ((NX) && last_) ? gN[h][0] : gA[h][0]; gs_[1] = ((NX) && last_) ? gN[h][1] : gA[h][1]; PG8_STAGE(PG8_SA(b, h), ptr, gs_); } \
;         else PG8_STAGE(PG8_SA(b, h), (ptr) + ((h) ? hstep : (size_t)0), voffA); } while (0)
; #define PG8_STAGE(bufoff, gbase, voff) do { _Pragma("unroll") for (int _i = 0; _i < 2; ++_i) \
;         __builtin_amdgcn_global_load_lds((const unsigned*)((const char*)(gbase) + (voff)[_i]), (PG8_LAS unsigned*)(lds + (bufoff) + ldsw + _i * 8192), 16, 0, 0); } while (0)
; #define PG8_LDA(dst, b, h) do { _Pragma("unroll") for (int m = 0; m < 4; ++m) _Pragma("unroll") for (int k = 0; k < 2; ++k) dst[m][k] = *(const PG8_LAS bf16x8*)(lds + PG8_SA(b, h) + aoff + m * 2048 + k * 1024); } while (0)
; #define PG8_MMA(ai, bj, At, Bt) do { __builtin_amdgcn_s_setprio(1); _Pragma("unroll") for (int m = 0; m < 4; ++m) _Pragma("unroll") for (int n = 0; n < 2; ++n) _Pragma("unroll") for (int k = 0; k < 2; ++k) \
;         acc[ai][bj][m][n] = __builtin_amdgcn_mfma_f32_16x16x32_bf16(Bt[n][k], At[m][k], acc[ai][bj][m][n], 0, 0, 0); __builtin_amdgcn_s_setprio(0); } while (0)
; #define PG8_WAIT_V(n) asm volatile("s_waitcnt vmcnt(" #n ")" ::: "memory")
; #define PG8_WAIT_L(n) asm volatile("s_waitcnt lgkmcnt(" #n ")" ::: "memory")
; #define PG8_BAR __builtin_amdgcn_s_barrier()
; #define PG8_SCHED __builtin_amdgcn_sched_barrier(0)
; template <class Epi, class Sched, bool ALIGN_EPI = false, bool SP2 = false>
; __device__ __forceinline__ void gemm_phase(PG8_LAS unsigned char* lds, const Gemm g, const Sched& S, const Epi& E, const bool skip_epi = false) {
;     ...
;         for (int t = 0; t < nt; t += 2) {
;     ...
;             PG8_LDA(At, 1, 1); PG8_STAGE(PG8_SB(1, 0), b3, voffB); PG8_STAGE(PG8_SB(1, 1), b3 + hstep, voffB); PG8_STAGE_A(1, 0, a3, true);
;             PG8_WAIT_V(8); PG8_WAIT_L(0); PG8_BAR; PG8_MMA(1, 0, At, B0); PG8_MMA(1, 1, At, B1); PG8_BAR; PG8_SCHED;
	s_add_i32 s28, s61, s2
	v_lshl_add_u64 v[164:165], v[164:165], 0, s[10:11]
	s_mov_b32 m0, s28
	ds_read_b128 v[192:195], v172 offset:49152
	ds_read_b128 v[196:199], v172 offset:50176
	ds_read_b128 v[200:203], v172 offset:51200
	ds_read_b128 v[204:207], v172 offset:52224
	ds_read_b128 v[208:211], v172 offset:53248
	ds_read_b128 v[212:215], v172 offset:54272
	ds_read_b128 v[216:219], v172 offset:55296
	ds_read_b128 v[220:223], v172 offset:56320
	global_load_lds_dwordx4 v[164:165], off
	s_add_i32 m0, s28, 0x2000
	s_add_u32 s26, s26, 0x40080
	v_lshl_add_u64 v[164:165], v[224:225], 0, s[10:11]
	s_addc_u32 s27, s27, 0
	s_add_i32 s28, s62, s2
	global_load_lds_dwordx4 v[164:165], off
	v_lshl_add_u64 v[164:165], s[26:27], 0, v[134:135]
	s_mov_b32 m0, s28
	s_nop 0
	global_load_lds_dwordx4 v[164:165], off
	v_lshl_add_u64 v[164:165], s[26:27], 0, v[130:131]
	s_add_i32 m0, s28, 0x2000
	s_nop 0
	global_load_lds_dwordx4 v[164:165], off
	v_lshl_add_u64 v[164:165], v[226:227], 0, s[10:11]
	s_mov_b32 m0, s37
	s_nop 0
	global_load_lds_dwordx4 v[164:165], off
	v_lshl_add_u64 v[164:165], v[230:231], 0, s[10:11]
	s_mov_b32 m0, s38
	s_nop 0
	global_load_lds_dwordx4 v[164:165], off
	s_waitcnt vmcnt(8)
	s_waitcnt lgkmcnt(0)
	s_barrier
	s_setprio 1
	s_waitcnt lgkmcnt(0)
	v_mfma_f32_16x16x32_bf16 v[62:65], v[148:151], v[192:195], v[62:65]
	v_mfma_f32_16x16x32_bf16 v[58:61], v[156:159], v[192:195], v[58:61]
	v_mfma_f32_16x16x32_bf16 v[50:53], v[148:151], v[200:203], v[50:53]
	v_mfma_f32_16x16x32_bf16 v[42:45], v[156:159], v[200:203], v[42:45]
	v_mfma_f32_16x16x32_bf16 v[34:37], v[148:151], v[208:211], v[34:37]
	v_mfma_f32_16x16x32_bf16 v[26:29], v[156:159], v[208:211], v[26:29]
	v_mfma_f32_16x16x32_bf16 v[18:21], v[148:151], v[216:219], v[18:21]
	v_mfma_f32_16x16x32_bf16 v[10:13], v[156:159], v[216:219], v[10:13]
	v_mfma_f32_16x16x32_bf16 v[62:65], v[152:155], v[196:199], v[62:65]
	v_mfma_f32_16x16x32_bf16 v[58:61], v[160:163], v[196:199], v[58:61]
	v_mfma_f32_16x16x32_bf16 v[50:53], v[152:155], v[204:207], v[50:53]
	v_mfma_f32_16x16x32_bf16 v[42:45], v[160:163], v[204:207], v[42:45]
	v_mfma_f32_16x16x32_bf16 v[34:37], v[152:155], v[212:215], v[34:37]
	v_mfma_f32_16x16x32_bf16 v[26:29], v[160:163], v[212:215], v[26:29]
	v_mfma_f32_16x16x32_bf16 v[18:21], v[152:155], v[220:223], v[18:21]
	v_mfma_f32_16x16x32_bf16 v[10:13], v[160:163], v[220:223], v[10:13]
	s_setprio 0
	s_setprio 1
	v_mfma_f32_16x16x32_bf16 v[54:57], v[176:179], v[192:195], v[54:57]
	v_mfma_f32_16x16x32_bf16 v[46:49], v[184:187], v[192:195], v[46:49]
	v_mfma_f32_16x16x32_bf16 v[38:41], v[176:179], v[200:203], v[38:41]
	v_mfma_f32_16x16x32_bf16 v[30:33], v[184:187], v[200:203], v[30:33]
	v_mfma_f32_16x16x32_bf16 v[22:25], v[176:179], v[208:211], v[22:25]
	v_mfma_f32_16x16x32_bf16 v[14:17], v[184:187], v[208:211], v[14:17]
	v_mfma_f32_16x16x32_bf16 v[6:9], v[176:179], v[216:219], v[6:9]
	v_mfma_f32_16x16x32_bf16 v[2:5], v[184:187], v[216:219], v[2:5]
	v_mfma_f32_16x16x32_bf16 v[54:57], v[180:183], v[196:199], v[54:57]
	v_mfma_f32_16x16x32_bf16 v[46:49], v[188:191], v[196:199], v[46:49]
	v_mfma_f32_16x16x32_bf16 v[38:41], v[180:183], v[204:207], v[38:41]
	v_mfma_f32_16x16x32_bf16 v[30:33], v[188:191], v[204:207], v[30:33]
	v_mfma_f32_16x16x32_bf16 v[22:25], v[180:183], v[212:215], v[22:25]
	v_mfma_f32_16x16x32_bf16 v[14:17], v[188:191], v[212:215], v[14:17]
	v_mfma_f32_16x16x32_bf16 v[6:9], v[180:183], v[220:223], v[6:9]
	v_mfma_f32_16x16x32_bf16 v[2:5], v[188:191], v[220:223], v[2:5]
	s_setprio 0
	s_barrier
	s_add_i32 s60, s60, 2
	s_add_u32 s24, s24, 0x100
	s_addc_u32 s25, s25, 0
	s_add_u32 s58, s58, 0x100
	s_addc_u32 s59, s59, 0
	s_cmp_gt_u32 s60, 13

; template <class Epi, class Sched, bool ALIGN_EPI = false, bool SP2 = false>
; __device__ __forceinline__ void gemm_phase(PG8_LAS unsigned char* lds, const Gemm g, const Sched& S, const Epi& E, const bool skip_epi = false) {
;     ...
;     for (;;) {
;         const bool has_next = S.next(ui + 1, nxt);
;         if (has_next) PG8_GIDX(gN, nxt.pm);
;         const char* nA = has_next ? (const char*)g.A + (size_t)nxt.pm * pmstepA + nxt.ko : cA; const char* nB = has_next ? (const char*)g.Bt + (size_t)nxt.pn * tstep + nxt.ko : cB;
;         for (int t = 0; t < nt; t += 2) {
;             const bool last = (t == nt - 2); last_ = last && has_next;
;             const char* a1 = cA + (size_t)(t + 1) * kstep;
;             const char* a2 = last ? nA : cA + (size_t)(t + 2) * kstep; const char* b2 = last ? nB : cB + (size_t)(t + 2) * kstep;
;             const char* a3 = a2 + kstep; const char* b3 = b2 + kstep;
;             if (last && has_next) S.a_ready(nxt);
;             if constexpr (SP2) {
;             PG8_LDB(B0, 0, 0); PG8_LDB(B1, 0, 1); PG8_SCHED; PG8_LDA(At, 0, 0); PG8_STAGE_A(1, 1, a1, false);
;             PG8_WAIT_V(8); PG8_WAIT_L(0); PG8_BAR; PG8_MMA(0, 0, At, B0); PG8_MMA(0, 1, At, B1); PG8_BAR; PG8_SCHED;
;             PG8_LDA(At, 0, 1); PG8_STAGE(PG8_SB(0, 0), b2, voffB); PG8_STAGE(PG8_SB(0, 1), b2 + hstep, voffB); PG8_STAGE_A(0, 0, a2, true);
;             PG8_WAIT_V(8); PG8_WAIT_L(0); PG8_BAR; PG8_MMA(1, 0, At, B0); PG8_MMA(1, 1, At, B1); PG8_BAR; PG8_SCHED;
;             PG8_LDB(B0, 1, 0); PG8_LDB(B1, 1, 1); PG8_SCHED; PG8_LDA(At, 1, 0); PG8_STAGE_A(0, 1, a2, true);
;             PG8_WAIT_V(8); PG8_WAIT_L(0); PG8_BAR; PG8_MMA(0, 0, At, B0); PG8_MMA(0, 1, At, B1); PG8_BAR; PG8_SCHED;
;             PG8_LDA(At, 1, 1); PG8_STAGE(PG8_SB(1, 0), b3, voffB); PG8_STAGE(PG8_SB(1, 1), b3 + hstep, voffB); PG8_STAGE_A(1, 0, a3, true);
;             PG8_WAIT_V(8); PG8_WAIT_L(0); PG8_BAR; PG8_MMA(1, 0, At, B0); PG8_MMA(1, 1, At, B1); PG8_BAR; PG8_SCHED;
; template <int layer> __device__ __forceinline__ void layer_phases(const Ctx& c, unsigned char* lds) {
;     ...
;             pg8::Gemm g{MIX, (const bf16*)(ws + WS_WOUT) + (size_t)layer * D * D, M, D, D, D}; pg8::StaticOrder S; S.init(M, D, G, bx);
;             { pg8::EpiRes<false> E{XB, XBD, SSD}; pg8::gemm_phase<pg8::EpiRes<false>, pg8::StaticOrder, true, true>(ldsl, g, S, E, noepi); }
.LBB0_633:
	s_ashr_i32 s19, s18, 31
	s_lshl_b64 s[20:21], s[18:19], 19
	s_add_u32 s20, s46, s20
	s_addc_u32 s21, s47, s21
	s_and_b64 s[22:23], s[6:7], exec
	s_cselect_b32 s19, s21, s27
	s_cselect_b32 s25, s20, s26
	s_ashr_i32 s17, s16, 31
	s_lshl_b64 s[22:23], s[16:17], 19
	v_readlane_b32 s17, v254, 40
	s_add_u32 s22, s17, s22
	v_readlane_b32 s17, v254, 41
	s_addc_u32 s23, s17, s23
	s_and_b64 s[30:31], s[6:7], exec
	s_cselect_b32 s17, s23, s29
	s_cselect_b32 s60, s22, s28
	s_add_u32 s26, s26, 0x40080
	s_addc_u32 s27, s27, 0
	s_add_u32 s61, s28, 0x100
	s_addc_u32 s62, s29, 0
	s_mov_b32 s63, -2
	s_waitcnt lgkmcnt(0)
	ds_read_b128 v[98:101], v234
	ds_read_b128 v[110:113], v234 offset:1024
	ds_read_b128 v[122:125], v234 offset:2048
	ds_read_b128 v[126:129], v234 offset:3072
	ds_read_b128 v[138:141], v235
	ds_read_b128 v[142:145], v235 offset:1024
	ds_read_b128 v[146:149], v235 offset:2048
	ds_read_b128 v[150:153], v235 offset:3072
	s_add_u32 s28, s26, 0xfffc0080
	s_addc_u32 s29, s27, -1
	s_cmp_eq_u32 s63, 12
	s_cselect_b32 s31, s19, s29
	s_cselect_b32 s30, s25, s28
	s_cselect_b32 s29, s17, s62
	s_cselect_b32 s28, s60, s61
	v_lshl_add_u64 v[210:211], s[26:27], 0, v[198:199]
	s_add_i32 m0, s3, 0xc000
	ds_read_b128 v[154:157], v236
	ds_read_b128 v[166:169], v236 offset:1024
	ds_read_b128 v[170:173], v236 offset:2048
	ds_read_b128 v[174:177], v236 offset:3072
	ds_read_b128 v[178:181], v236 offset:4096
	ds_read_b128 v[182:185], v236 offset:5120
	ds_read_b128 v[186:189], v236 offset:6144
	ds_read_b128 v[206:209], v236 offset:7168
	global_load_lds_dwordx4 v[210:211], off
	v_lshl_add_u64 v[210:211], s[26:27], 0, v[200:201]
	s_add_i32 m0, s3, 0xe000
	s_nop 0
	global_load_lds_dwordx4 v[210:211], off
	s_waitcnt vmcnt(8)
	s_waitcnt lgkmcnt(0)
	s_barrier
	s_setprio 1
	s_waitcnt lgkmcnt(0)
	v_mfma_f32_16x16x32_bf16 v[162:165], v[98:101], v[154:157], 0
	v_mfma_f32_16x16x32_bf16 v[158:161], v[122:125], v[154:157], 0
	v_mfma_f32_16x16x32_bf16 v[118:121], v[98:101], v[170:173], 0
	v_mfma_f32_16x16x32_bf16 v[114:117], v[122:125], v[170:173], 0
	v_mfma_f32_16x16x32_bf16 v[94:97], v[98:101], v[178:181], 0
	v_mfma_f32_16x16x32_bf16 v[90:93], v[122:125], v[178:181], 0
	v_mfma_f32_16x16x32_bf16 v[78:81], v[98:101], v[186:189], 0
	v_mfma_f32_16x16x32_bf16 v[74:77], v[122:125], v[186:189], 0
	v_mfma_f32_16x16x32_bf16 v[162:165], v[110:113], v[166:169], v[162:165]
	v_mfma_f32_16x16x32_bf16 v[158:161], v[126:129], v[166:169], v[158:161]
	v_mfma_f32_16x16x32_bf16 v[118:121], v[110:113], v[174:177], v[118:121]
	v_mfma_f32_16x16x32_bf16 v[114:117], v[126:129], v[174:177], v[114:117]
	v_mfma_f32_16x16x32_bf16 v[94:97], v[110:113], v[182:185], v[94:97]
	v_mfma_f32_16x16x32_bf16 v[90:93], v[126:129], v[182:185], v[90:93]
	v_mfma_f32_16x16x32_bf16 v[78:81], v[110:113], v[206:209], v[78:81]
	v_mfma_f32_16x16x32_bf16 v[74:77], v[126:129], v[206:209], v[74:77]
	s_setprio 0
	s_setprio 1
	v_mfma_f32_16x16x32_bf16 v[134:137], v[138:141], v[154:157], 0
	v_mfma_f32_16x16x32_bf16 v[130:133], v[146:149], v[154:157], 0
	v_mfma_f32_16x16x32_bf16 v[106:109], v[138:141], v[170:173], 0
	v_mfma_f32_16x16x32_bf16 v[102:105], v[146:149], v[170:173], 0
	v_mfma_f32_16x16x32_bf16 v[86:89], v[138:141], v[178:181], 0
	v_mfma_f32_16x16x32_bf16 v[82:85], v[146:149], v[178:181], 0
	v_mfma_f32_16x16x32_bf16 v[70:73], v[138:141], v[186:189], 0
	v_mfma_f32_16x16x32_bf16 v[66:69], v[146:149], v[186:189], 0
	v_mfma_f32_16x16x32_bf16 v[134:137], v[142:145], v[166:169], v[134:137]
	v_mfma_f32_16x16x32_bf16 v[130:133], v[150:153], v[166:169], v[130:133]
	v_mfma_f32_16x16x32_bf16 v[106:109], v[142:145], v[174:177], v[106:109]
	v_mfma_f32_16x16x32_bf16 v[102:105], v[150:153], v[174:177], v[102:105]
	v_mfma_f32_16x16x32_bf16 v[86:89], v[142:145], v[182:185], v[86:89]
	v_mfma_f32_16x16x32_bf16 v[82:85], v[150:153], v[182:185], v[82:85]
	v_mfma_f32_16x16x32_bf16 v[70:73], v[142:145], v[206:209], v[70:73]
	v_mfma_f32_16x16x32_bf16 v[66:69], v[150:153], v[206:209], v[66:69]
	s_setprio 0
	s_barrier
	s_add_i32 s64, s57, s2
	v_lshl_add_u64 v[210:211], s[28:29], 0, v[192:193]
	s_mov_b32 m0, s64
	ds_read_b128 v[154:157], v236 offset:16384
	ds_read_b128 v[166:169], v236 offset:17408
	ds_read_b128 v[170:173], v236 offset:18432
	ds_read_b128 v[174:177], v236 offset:19456
	ds_read_b128 v[178:181], v236 offset:20480
	ds_read_b128 v[182:185], v236 offset:21504
	ds_read_b128 v[186:189], v236 offset:22528
	ds_read_b128 v[206:209], v236 offset:23552
	global_load_lds_dwordx4 v[210:211], off
	s_add_i32 m0, s64, 0x2000
	s_add_u32 s64, s28, 0x40000
	v_lshl_add_u64 v[212:213], s[28:29], 0, v[196:197]
	s_addc_u32 s65, s29, 0
	s_add_i32 s66, s58, s2
	global_load_lds_dwordx4 v[212:213], off
	v_lshl_add_u64 v[214:215], s[64:65], 0, v[192:193]
	s_mov_b32 m0, s66
	v_lshl_add_u64 v[216:217], s[30:31], 0, v[194:195]
	global_load_lds_dwordx4 v[214:215], off
	v_lshl_add_u64 v[214:215], s[64:65], 0, v[196:197]
	s_add_i32 m0, s66, 0x2000
	s_nop 0
	global_load_lds_dwordx4 v[214:215], off
	v_lshl_add_u64 v[214:215], s[30:31], 0, v[190:191]
	s_mov_b32 m0, s3
	s_nop 0
	global_load_lds_dwordx4 v[214:215], off
	s_mov_b32 m0, s34
	s_nop 0
	global_load_lds_dwordx4 v[216:217], off
	s_waitcnt vmcnt(8)
	s_waitcnt lgkmcnt(0)
	s_barrier
; #define PG8_STAGE_A(b, h, ptr, NX) do { if constexpr (Sched::GATHER) { unsigned gs_[2]; gs_[0] = ((NX) && last_) ? gN[h][0] : gA[h][0]; gs_[1] = ((NX) && last_) ? gN[h][1] : gA[h][1]; PG8_STAGE(PG8_SA(b, h), ptr, gs_); } \
;         else PG8_STAGE(PG8_SA(b, h), (ptr) + ((h) ? hstep : (size_t)0), voffA); } while (0)
; #define PG8_STAGE(bufoff, gbase, voff) do { _Pragma("unroll") for (int _i = 0; _i < 2; ++_i) \
;         __builtin_amdgcn_global_load_lds((const unsigned*)((const char*)(gbase) + (voff)[_i]), (PG8_LAS unsigned*)(lds + (bufoff) + ldsw + _i * 8192), 16, 0, 0); } while (0)
; #define PG8_LDA(dst, b, h) do { _Pragma("unroll") for (int m = 0; m < 4; ++m) _Pragma("unroll") for (int k = 0; k < 2; ++k) dst[m][k] = *(const PG8_LAS bf16x8*)(lds + PG8_SA(b, h) + aoff + m * 2048 + k * 1024); } while (0)
; #define PG8_LDB(dst, b, h) do { _Pragma("unroll") for (int n = 0; n < 2; ++n) _Pragma("unroll") for (int k = 0; k < 2; ++k) dst[n][k] = *(const PG8_LAS bf16x8*)(lds + PG8_SB(b, h) + boff + n * 2048 + k * 1024); } while (0)
; #define PG8_MMA(ai, bj, At, Bt) do { __builtin_amdgcn_s_setprio(1); _Pragma("unroll") for (int m = 0; m < 4; ++m) _Pragma("unroll") for (int n = 0; n < 2; ++n) _Pragma("unroll") for (int k = 0; k < 2; ++k) \
;         acc[ai][bj][m][n] = __builtin_amdgcn_mfma_f32_16x16x32_bf16(Bt[n][k], At[m][k], acc[ai][bj][m][n], 0, 0, 0); __builtin_amdgcn_s_setprio(0); } while (0)
; #define PG8_WAIT_V(n) asm volatile("s_waitcnt vmcnt(" #n ")" ::: "memory")
; #define PG8_WAIT_L(n) asm volatile("s_waitcnt lgkmcnt(" #n ")" ::: "memory")
; #define PG8_BAR __builtin_amdgcn_s_barrier()
; #define PG8_SCHED __builtin_amdgcn_sched_barrier(0)
; template <class Epi, class Sched, bool ALIGN_EPI = false, bool SP2 = false>
; __device__ __forceinline__ void gemm_phase(PG8_LAS unsigned char* lds, const Gemm g, const Sched& S, const Epi& E, const bool skip_epi = false) {
;     ...
;             PG8_WAIT_V(8); PG8_WAIT_L(0); PG8_BAR; PG8_MMA(1, 0, At, B0); PG8_MMA(1, 1, At, B1); PG8_BAR; PG8_SCHED;
;             PG8_LDB(B0, 1, 0); PG8_LDB(B1, 1, 1); PG8_SCHED; PG8_LDA(At, 1, 0); PG8_STAGE_A(0, 1, a2, true);
;             PG8_WAIT_V(8); PG8_WAIT_L(0); PG8_BAR; PG8_MMA(0, 0, At, B0); PG8_MMA(0, 1, At, B1); PG8_BAR; PG8_SCHED;
;             PG8_LDA(At, 1, 1); PG8_STAGE(PG8_SB(1, 0), b3, voffB); PG8_STAGE(PG8_SB(1, 1), b3 + hstep, voffB); PG8_STAGE_A(1, 0, a3, true);
	s_setprio 1
	s_waitcnt lgkmcnt(0)
	v_mfma_f32_16x16x32_bf16 v[62:65], v[98:101], v[154:157], 0
	v_mfma_f32_16x16x32_bf16 v[58:61], v[122:125], v[154:157], 0
	v_mfma_f32_16x16x32_bf16 v[46:49], v[98:101], v[170:173], 0
	v_mfma_f32_16x16x32_bf16 v[42:45], v[122:125], v[170:173], 0
	v_mfma_f32_16x16x32_bf16 v[30:33], v[98:101], v[178:181], 0
	v_mfma_f32_16x16x32_bf16 v[26:29], v[122:125], v[178:181], 0
	v_mfma_f32_16x16x32_bf16 v[14:17], v[98:101], v[186:189], 0
	v_mfma_f32_16x16x32_bf16 v[10:13], v[122:125], v[186:189], 0
	v_mfma_f32_16x16x32_bf16 v[62:65], v[110:113], v[166:169], v[62:65]
	v_mfma_f32_16x16x32_bf16 v[58:61], v[126:129], v[166:169], v[58:61]
	v_mfma_f32_16x16x32_bf16 v[46:49], v[110:113], v[174:177], v[46:49]
	v_mfma_f32_16x16x32_bf16 v[42:45], v[126:129], v[174:177], v[42:45]
	v_mfma_f32_16x16x32_bf16 v[30:33], v[110:113], v[182:185], v[30:33]
	v_mfma_f32_16x16x32_bf16 v[26:29], v[126:129], v[182:185], v[26:29]
	v_mfma_f32_16x16x32_bf16 v[14:17], v[110:113], v[206:209], v[14:17]
	v_mfma_f32_16x16x32_bf16 v[10:13], v[126:129], v[206:209], v[10:13]
	s_setprio 0
	s_setprio 1
	v_mfma_f32_16x16x32_bf16 v[54:57], v[138:141], v[154:157], 0
	v_mfma_f32_16x16x32_bf16 v[50:53], v[146:149], v[154:157], 0
	v_mfma_f32_16x16x32_bf16 v[38:41], v[138:141], v[170:173], 0
	v_mfma_f32_16x16x32_bf16 v[34:37], v[146:149], v[170:173], 0
	v_mfma_f32_16x16x32_bf16 v[22:25], v[138:141], v[178:181], 0
	v_mfma_f32_16x16x32_bf16 v[18:21], v[146:149], v[178:181], 0
	v_mfma_f32_16x16x32_bf16 v[6:9], v[138:141], v[186:189], 0
	v_mfma_f32_16x16x32_bf16 v[2:5], v[146:149], v[186:189], 0
	v_mfma_f32_16x16x32_bf16 v[54:57], v[142:145], v[166:169], v[54:57]
	v_mfma_f32_16x16x32_bf16 v[50:53], v[150:153], v[166:169], v[50:53]
	v_mfma_f32_16x16x32_bf16 v[38:41], v[142:145], v[174:177], v[38:41]
	v_mfma_f32_16x16x32_bf16 v[34:37], v[150:153], v[174:177], v[34:37]
	v_mfma_f32_16x16x32_bf16 v[22:25], v[142:145], v[182:185], v[22:25]
	v_mfma_f32_16x16x32_bf16 v[18:21], v[150:153], v[182:185], v[18:21]
	v_mfma_f32_16x16x32_bf16 v[6:9], v[142:145], v[206:209], v[6:9]
	v_mfma_f32_16x16x32_bf16 v[2:5], v[150:153], v[206:209], v[2:5]
	s_setprio 0
	s_barrier
	s_add_i32 s64, 0, 0x18000
	s_add_i32 s65, 0, 0x1c000
	v_add_u32_e32 v126, s64, v229
	v_add_u32_e32 v150, s65, v229
	ds_read_b128 v[98:101], v126
	ds_read_b128 v[110:113], v126 offset:1024
	ds_read_b128 v[122:125], v126 offset:2048
	ds_read_b128 v[126:129], v126 offset:3072
	ds_read_b128 v[138:141], v150
	ds_read_b128 v[142:145], v150 offset:1024
	ds_read_b128 v[146:149], v150 offset:2048
	ds_read_b128 v[150:153], v150 offset:3072
	s_add_u32 s30, s30, 0x40000
	s_addc_u32 s31, s31, 0
	s_mov_b32 m0, s35
	v_lshl_add_u64 v[218:219], s[30:31], 0, v[190:191]
	ds_read_b128 v[154:157], v236 offset:32768
	ds_read_b128 v[166:169], v236 offset:33792
	ds_read_b128 v[170:173], v236 offset:34816
	ds_read_b128 v[174:177], v236 offset:35840
	ds_read_b128 v[178:181], v236 offset:36864
	ds_read_b128 v[182:185], v236 offset:37888
	ds_read_b128 v[186:189], v236 offset:38912
	ds_read_b128 v[206:209], v236 offset:39936
	global_load_lds_dwordx4 v[218:219], off
	v_lshl_add_u64 v[218:219], s[30:31], 0, v[194:195]
	s_mov_b32 m0, s36
	s_nop 0
	global_load_lds_dwordx4 v[218:219], off
	s_waitcnt vmcnt(8)
	s_waitcnt lgkmcnt(0)
	s_barrier
	s_setprio 1
	s_waitcnt lgkmcnt(0)
	v_mfma_f32_16x16x32_bf16 v[162:165], v[98:101], v[154:157], v[162:165]
	v_mfma_f32_16x16x32_bf16 v[158:161], v[122:125], v[154:157], v[158:161]
	v_mfma_f32_16x16x32_bf16 v[118:121], v[98:101], v[170:173], v[118:121]
	v_mfma_f32_16x16x32_bf16 v[114:117], v[122:125], v[170:173], v[114:117]
	v_mfma_f32_16x16x32_bf16 v[94:97], v[98:101], v[178:181], v[94:97]
	v_mfma_f32_16x16x32_bf16 v[90:93], v[122:125], v[178:181], v[90:93]
	v_mfma_f32_16x16x32_bf16 v[78:81], v[98:101], v[186:189], v[78:81]
	v_mfma_f32_16x16x32_bf16 v[74:77], v[122:125], v[186:189], v[74:77]
	v_mfma_f32_16x16x32_bf16 v[162:165], v[110:113], v[166:169], v[162:165]
	v_mfma_f32_16x16x32_bf16 v[158:161], v[126:129], v[166:169], v[158:161]
	v_mfma_f32_16x16x32_bf16 v[118:121], v[110:113], v[174:177], v[118:121]
	v_mfma_f32_16x16x32_bf16 v[114:117], v[126:129], v[174:177], v[114:117]
	v_mfma_f32_16x16x32_bf16 v[94:97], v[110:113], v[182:185], v[94:97]
	v_mfma_f32_16x16x32_bf16 v[90:93], v[126:129], v[182:185], v[90:93]
	v_mfma_f32_16x16x32_bf16 v[78:81], v[110:113], v[206:209], v[78:81]
	v_mfma_f32_16x16x32_bf16 v[74:77], v[126:129], v[206:209], v[74:77]
	s_setprio 0
	s_setprio 1
	v_mfma_f32_16x16x32_bf16 v[134:137], v[138:141], v[154:157], v[134:137]
	v_mfma_f32_16x16x32_bf16 v[130:133], v[146:149], v[154:157], v[130:133]
	v_mfma_f32_16x16x32_bf16 v[106:109], v[138:141], v[170:173], v[106:109]
	v_mfma_f32_16x16x32_bf16 v[102:105], v[146:149], v[170:173], v[102:105]
	v_mfma_f32_16x16x32_bf16 v[86:89], v[138:141], v[178:181], v[86:89]
	v_mfma_f32_16x16x32_bf16 v[82:85], v[146:149], v[178:181], v[82:85]
	v_mfma_f32_16x16x32_bf16 v[70:73], v[138:141], v[186:189], v[70:73]
	v_mfma_f32_16x16x32_bf16 v[66:69], v[146:149], v[186:189], v[66:69]
	v_mfma_f32_16x16x32_bf16 v[134:137], v[142:145], v[166:169], v[134:137]
	v_mfma_f32_16x16x32_bf16 v[130:133], v[150:153], v[166:169], v[130:133]
	v_mfma_f32_16x16x32_bf16 v[106:109], v[142:145], v[174:177], v[106:109]
	v_mfma_f32_16x16x32_bf16 v[102:105], v[150:153], v[174:177], v[102:105]
	v_mfma_f32_16x16x32_bf16 v[86:89], v[142:145], v[182:185], v[86:89]
	v_mfma_f32_16x16x32_bf16 v[82:85], v[150:153], v[182:185], v[82:85]
	v_mfma_f32_16x16x32_bf16 v[70:73], v[142:145], v[206:209], v[70:73]
	v_mfma_f32_16x16x32_bf16 v[66:69], v[150:153], v[206:209], v[66:69]
	s_setprio 0
	s_barrier
; #define PG8_STAGE_A(b, h, ptr, NX) do { if constexpr (Sched::GATHER) { unsigned gs_[2]; gs_[0] = ((NX) && last_) ? gN[h][0] : gA[h][0]; gs_[1] = ((NX) && last_) ? gN[h][1] : gA[h][1]; PG8_STAGE(PG8_SA(b, h), ptr, gs_); } \
;         else PG8_STAGE(PG8_SA(b, h), (ptr) + ((h) ? hstep : (size_t)0), voffA); } while (0)
; #define PG8_STAGE(bufoff, gbase, voff) do { _Pragma("unroll") for (int _i = 0; _i < 2; ++_i) \
;         __builtin_amdgcn_global_load_lds((const unsigned*)((const char*)(gbase) + (voff)[_i]), (PG8_LAS unsigned*)(lds + (bufoff) + ldsw + _i * 8192), 16, 0, 0); } while (0)
; #define PG8_LDA(dst, b, h) do { _Pragma("unroll") for (int m = 0; m < 4; ++m) _Pragma("unroll") for (int k = 0; k < 2; ++k) dst[m][k] = *(const PG8_LAS bf16x8*)(lds + PG8_SA(b, h) + aoff + m * 2048 + k * 1024); } while (0)
; #define PG8_MMA(ai, bj, At, Bt) do { __builtin_amdgcn_s_setprio(1); _Pragma("unroll") for (int m = 0; m < 4; ++m) _Pragma("unroll") for (int n = 0; n < 2; ++n) _Pragma("unroll") for (int k = 0; k < 2; ++k) \
;         acc[ai][bj][m][n] = __builtin_amdgcn_mfma_f32_16x16x32_bf16(Bt[n][k], At[m][k], acc[ai][bj][m][n], 0, 0, 0); __builtin_amdgcn_s_setprio(0); } while (0)
; #define PG8_WAIT_V(n) asm volatile("s_waitcnt vmcnt(" #n ")" ::: "memory")
; #define PG8_WAIT_L(n) asm volatile("s_waitcnt lgkmcnt(" #n ")" ::: "memory")
; #define PG8_BAR __builtin_amdgcn_s_barrier()
; #define PG8_SCHED __builtin_amdgcn_sched_barrier(0)
; template <class Epi, class Sched, bool ALIGN_EPI = false, bool SP2 = false>
; __device__ __forceinline__ void gemm_phase(PG8_LAS unsigned char* lds, const Gemm g, const Sched& S, const Epi& E, const bool skip_epi = false) {
;     ...
;         for (int t = 0; t < nt; t += 2) {
;     ...
;             PG8_LDA(At, 1, 1); PG8_STAGE(PG8_SB(1, 0), b3, voffB); PG8_STAGE(PG8_SB(1, 1), b3 + hstep, voffB); PG8_STAGE_A(1, 0, a3, true);
;             PG8_WAIT_V(8); PG8_WAIT_L(0); PG8_BAR; PG8_MMA(1, 0, At, B0); PG8_MMA(1, 1, At, B1); PG8_BAR; PG8_SCHED;
	s_add_i32 s30, s64, s2
	v_lshl_add_u64 v[210:211], v[210:211], 0, s[12:13]
	s_mov_b32 m0, s30
	ds_read_b128 v[154:157], v236 offset:49152
	ds_read_b128 v[166:169], v236 offset:50176
	ds_read_b128 v[170:173], v236 offset:51200
	ds_read_b128 v[174:177], v236 offset:52224
	ds_read_b128 v[178:181], v236 offset:53248
	ds_read_b128 v[182:185], v236 offset:54272
	ds_read_b128 v[186:189], v236 offset:55296
	ds_read_b128 v[206:209], v236 offset:56320
	global_load_lds_dwordx4 v[210:211], off
	s_add_i32 m0, s30, 0x2000
	s_add_u32 s28, s28, 0x40080
	v_lshl_add_u64 v[210:211], v[212:213], 0, s[12:13]
	s_addc_u32 s29, s29, 0
	s_add_i32 s30, s65, s2
	global_load_lds_dwordx4 v[210:211], off
	v_lshl_add_u64 v[210:211], s[28:29], 0, v[192:193]
	s_mov_b32 m0, s30
	s_nop 0
	global_load_lds_dwordx4 v[210:211], off
	v_lshl_add_u64 v[210:211], s[28:29], 0, v[196:197]
	s_add_i32 m0, s30, 0x2000
	s_nop 0
	global_load_lds_dwordx4 v[210:211], off
	v_lshl_add_u64 v[210:211], v[214:215], 0, s[12:13]
	s_mov_b32 m0, s39
	s_nop 0
	global_load_lds_dwordx4 v[210:211], off
	v_lshl_add_u64 v[210:211], v[216:217], 0, s[12:13]
	s_mov_b32 m0, s48
	s_nop 0
	global_load_lds_dwordx4 v[210:211], off
	s_waitcnt vmcnt(8)
	s_waitcnt lgkmcnt(0)
	s_barrier
	s_setprio 1
	s_waitcnt lgkmcnt(0)
	v_mfma_f32_16x16x32_bf16 v[62:65], v[98:101], v[154:157], v[62:65]
	v_mfma_f32_16x16x32_bf16 v[58:61], v[122:125], v[154:157], v[58:61]
	v_mfma_f32_16x16x32_bf16 v[46:49], v[98:101], v[170:173], v[46:49]
	v_mfma_f32_16x16x32_bf16 v[42:45], v[122:125], v[170:173], v[42:45]
	v_mfma_f32_16x16x32_bf16 v[30:33], v[98:101], v[178:181], v[30:33]
	v_mfma_f32_16x16x32_bf16 v[26:29], v[122:125], v[178:181], v[26:29]
	v_mfma_f32_16x16x32_bf16 v[14:17], v[98:101], v[186:189], v[14:17]
	v_mfma_f32_16x16x32_bf16 v[10:13], v[122:125], v[186:189], v[10:13]
	v_mfma_f32_16x16x32_bf16 v[62:65], v[110:113], v[166:169], v[62:65]
	v_mfma_f32_16x16x32_bf16 v[58:61], v[126:129], v[166:169], v[58:61]
	v_mfma_f32_16x16x32_bf16 v[46:49], v[110:113], v[174:177], v[46:49]
	v_mfma_f32_16x16x32_bf16 v[42:45], v[126:129], v[174:177], v[42:45]
	v_mfma_f32_16x16x32_bf16 v[30:33], v[110:113], v[182:185], v[30:33]
	v_mfma_f32_16x16x32_bf16 v[26:29], v[126:129], v[182:185], v[26:29]
	v_mfma_f32_16x16x32_bf16 v[14:17], v[110:113], v[206:209], v[14:17]
	v_mfma_f32_16x16x32_bf16 v[10:13], v[126:129], v[206:209], v[10:13]
	s_setprio 0
	s_setprio 1
	v_mfma_f32_16x16x32_bf16 v[54:57], v[138:141], v[154:157], v[54:57]
	v_mfma_f32_16x16x32_bf16 v[50:53], v[146:149], v[154:157], v[50:53]
	v_mfma_f32_16x16x32_bf16 v[38:41], v[138:141], v[170:173], v[38:41]
	v_mfma_f32_16x16x32_bf16 v[34:37], v[146:149], v[170:173], v[34:37]
	v_mfma_f32_16x16x32_bf16 v[22:25], v[138:141], v[178:181], v[22:25]
	v_mfma_f32_16x16x32_bf16 v[18:21], v[146:149], v[178:181], v[18:21]
	v_mfma_f32_16x16x32_bf16 v[6:9], v[138:141], v[186:189], v[6:9]
	v_mfma_f32_16x16x32_bf16 v[2:5], v[146:149], v[186:189], v[2:5]
	v_mfma_f32_16x16x32_bf16 v[54:57], v[142:145], v[166:169], v[54:57]
	v_mfma_f32_16x16x32_bf16 v[50:53], v[150:153], v[166:169], v[50:53]
	v_mfma_f32_16x16x32_bf16 v[38:41], v[142:145], v[174:177], v[38:41]
	v_mfma_f32_16x16x32_bf16 v[34:37], v[150:153], v[174:177], v[34:37]
	v_mfma_f32_16x16x32_bf16 v[22:25], v[142:145], v[182:185], v[22:25]
	v_mfma_f32_16x16x32_bf16 v[18:21], v[150:153], v[182:185], v[18:21]
	v_mfma_f32_16x16x32_bf16 v[6:9], v[142:145], v[206:209], v[6:9]
	v_mfma_f32_16x16x32_bf16 v[2:5], v[150:153], v[206:209], v[2:5]
	s_setprio 0
	s_barrier
	s_add_i32 s63, s63, 2
	s_add_u32 s26, s26, 0x100
	s_addc_u32 s27, s27, 0
	s_add_u32 s61, s61, 0x100
	s_addc_u32 s62, s62, 0
	s_cmp_gt_u32 s63, 13

; #define PG8_BAR __builtin_amdgcn_s_barrier()
; template <class Epi, class Sched, bool ALIGN_EPI = false, bool SP2 = false>
; __device__ __forceinline__ void gemm_phase(PG8_LAS unsigned char* lds, const Gemm g, const Sched& S, const Epi& E, const bool skip_epi = false) {
;     ...
;     for (;;) {
;         const bool has_next = S.next(ui + 1, nxt);
;         if (has_next) PG8_GIDX(gN, nxt.pm);
;         const char* nA = has_next ? (const char*)g.A + (size_t)nxt.pm * pmstepA + nxt.ko : cA; const char* nB = has_next ? (const char*)g.Bt + (size_t)nxt.pn * tstep + nxt.ko : cB;
;         for (int t = 0; t < nt; t += 2) {
;             const bool last = (t == nt - 2); last_ = last && has_next;
;             const char* a1 = cA + (size_t)(t + 1) * kstep;
;             const char* a2 = last ? nA : cA + (size_t)(t + 2) * kstep; const char* b2 = last ? nB : cB + (size_t)(t + 2) * kstep;
;             const char* a3 = a2 + kstep; const char* b3 = b2 + kstep;
;             if (last && has_next) S.a_ready(nxt);
;             if constexpr (SP2) {
;             PG8_LDB(B0, 0, 0); PG8_LDB(B1, 0, 1); PG8_SCHED; PG8_LDA(At, 0, 0); PG8_STAGE_A(1, 1, a1, false);
;             PG8_WAIT_V(8); PG8_WAIT_L(0); PG8_BAR; PG8_MMA(0, 0, At, B0); PG8_MMA(0, 1, At, B1); PG8_BAR; PG8_SCHED;
;             PG8_LDA(At, 0, 1); PG8_STAGE(PG8_SB(0, 0), b2, voffB); PG8_STAGE(PG8_SB(0, 1), b2 + hstep, voffB); PG8_STAGE_A(0, 0, a2, true);
;             PG8_WAIT_V(8); PG8_WAIT_L(0); PG8_BAR; PG8_MMA(1, 0, At, B0); PG8_MMA(1, 1, At, B1); PG8_BAR; PG8_SCHED;
;             PG8_LDB(B0, 1, 0); PG8_LDB(B1, 1, 1); PG8_SCHED; PG8_LDA(At, 1, 0); PG8_STAGE_A(0, 1, a2, true);
;             PG8_WAIT_V(8); PG8_WAIT_L(0); PG8_BAR; PG8_MMA(0, 0, At, B0); PG8_MMA(0, 1, At, B1); PG8_BAR; PG8_SCHED;
;             PG8_LDA(At, 1, 1); PG8_STAGE(PG8_SB(1, 0), b3, voffB); PG8_STAGE(PG8_SB(1, 1), b3 + hstep, voffB); PG8_STAGE_A(1, 0, a3, true);
;             PG8_WAIT_V(8); PG8_WAIT_L(0); PG8_BAR; PG8_MMA(1, 0, At, B0); PG8_MMA(1, 1, At, B1); PG8_BAR; PG8_SCHED;
; template <int layer> __device__ __forceinline__ void layer_phases(const Ctx& c, unsigned char* lds) {
;     ...
;                 pg8::Gemm g{XB, W13, M, 2 * FF, D, D}; pg8::StaticOrder S; S.init(M, 2 * FF, G, bx);
;                 pg8::EpiGlu<false> E{H, FF, SS};
;                 pg8::gemm_phase<pg8::EpiGlu<false>, pg8::StaticOrder, true, true>(ldsl, g, S, E, noepi);
.LBB0_720:
	s_ashr_i32 s15, s14, 31
	s_lshl_b64 s[16:17], s[14:15], 19
	s_add_u32 s16, s86, s16
	s_addc_u32 s17, s87, s17
	s_and_b64 s[18:19], s[4:5], exec
	s_cselect_b32 s15, s17, s23
	s_cselect_b32 s56, s16, s22
	s_ashr_i32 s13, s12, 31
	s_lshl_b64 s[18:19], s[12:13], 19
	v_readlane_b32 s26, v254, 15
	v_readlane_b32 s27, v254, 16
	s_add_u32 s18, s26, s18
	s_addc_u32 s19, s27, s19
	s_and_b64 s[26:27], s[4:5], exec
	s_cselect_b32 s13, s19, s25
	s_cselect_b32 s57, s18, s24
	s_add_u32 s22, s22, 0x40080
	s_addc_u32 s23, s23, 0
	s_add_u32 s58, s24, 0x100
	s_addc_u32 s59, s25, 0
	s_mov_b32 s60, -2
	s_waitcnt vmcnt(0)
	ds_read_b128 v[130:133], v187
	ds_read_b128 v[134:137], v187 offset:1024
	ds_read_b128 v[138:141], v187 offset:2048
	ds_read_b128 v[160:163], v187 offset:3072
	ds_read_b128 v[164:167], v188
	ds_read_b128 v[182:185], v188 offset:1024
	ds_read_b128 v[192:195], v188 offset:2048
	ds_read_b128 v[196:199], v188 offset:3072
	s_add_u32 s24, s22, 0xfffc0080
	s_addc_u32 s25, s23, -1
	s_cmp_eq_u32 s60, 12
	s_cselect_b32 s27, s15, s25
	s_cselect_b32 s26, s56, s24
	s_cselect_b32 s25, s13, s59
	s_cselect_b32 s24, s57, s58
	v_lshl_add_u64 v[168:169], s[22:23], 0, v[152:153]
	s_add_i32 m0, s29, 0xc000
	ds_read_b128 v[200:203], v189
	ds_read_b128 v[204:207], v189 offset:1024
	ds_read_b128 v[208:211], v189 offset:2048
	ds_read_b128 v[212:215], v189 offset:3072
	ds_read_b128 v[216:219], v189 offset:4096
	ds_read_b128 v[220:223], v189 offset:5120
	ds_read_b128 v[224:227], v189 offset:6144
	ds_read_b128 v[230:233], v189 offset:7168
	global_load_lds_dwordx4 v[168:169], off
	v_lshl_add_u64 v[168:169], s[22:23], 0, v[154:155]
	s_add_i32 m0, s29, 0xe000
	s_nop 0
	global_load_lds_dwordx4 v[168:169], off
	s_waitcnt vmcnt(8)
	s_waitcnt lgkmcnt(0)
	s_barrier
	s_setprio 1
	s_waitcnt lgkmcnt(0)
	v_mfma_f32_16x16x32_bf16 v[126:129], v[130:133], v[200:203], 0
	v_mfma_f32_16x16x32_bf16 v[122:125], v[138:141], v[200:203], 0
	v_mfma_f32_16x16x32_bf16 v[110:113], v[130:133], v[208:211], 0
	v_mfma_f32_16x16x32_bf16 v[106:109], v[138:141], v[208:211], 0
	v_mfma_f32_16x16x32_bf16 v[94:97], v[130:133], v[216:219], 0
	v_mfma_f32_16x16x32_bf16 v[90:93], v[138:141], v[216:219], 0
	v_mfma_f32_16x16x32_bf16 v[78:81], v[130:133], v[224:227], 0
	v_mfma_f32_16x16x32_bf16 v[74:77], v[138:141], v[224:227], 0
	v_mfma_f32_16x16x32_bf16 v[126:129], v[134:137], v[204:207], v[126:129]
	v_mfma_f32_16x16x32_bf16 v[122:125], v[160:163], v[204:207], v[122:125]
	v_mfma_f32_16x16x32_bf16 v[110:113], v[134:137], v[212:215], v[110:113]
	v_mfma_f32_16x16x32_bf16 v[106:109], v[160:163], v[212:215], v[106:109]
	v_mfma_f32_16x16x32_bf16 v[94:97], v[134:137], v[220:223], v[94:97]
	v_mfma_f32_16x16x32_bf16 v[90:93], v[160:163], v[220:223], v[90:93]
	v_mfma_f32_16x16x32_bf16 v[78:81], v[134:137], v[230:233], v[78:81]
	v_mfma_f32_16x16x32_bf16 v[74:77], v[160:163], v[230:233], v[74:77]
	s_setprio 0
	s_setprio 1
	v_mfma_f32_16x16x32_bf16 v[118:121], v[164:167], v[200:203], 0
	v_mfma_f32_16x16x32_bf16 v[114:117], v[192:195], v[200:203], 0
	v_mfma_f32_16x16x32_bf16 v[102:105], v[164:167], v[208:211], 0
	v_mfma_f32_16x16x32_bf16 v[98:101], v[192:195], v[208:211], 0
	v_mfma_f32_16x16x32_bf16 v[86:89], v[164:167], v[216:219], 0
	v_mfma_f32_16x16x32_bf16 v[82:85], v[192:195], v[216:219], 0
	v_mfma_f32_16x16x32_bf16 v[70:73], v[164:167], v[224:227], 0
	v_mfma_f32_16x16x32_bf16 v[66:69], v[192:195], v[224:227], 0
	v_mfma_f32_16x16x32_bf16 v[118:121], v[182:185], v[204:207], v[118:121]
	v_mfma_f32_16x16x32_bf16 v[114:117], v[196:199], v[204:207], v[114:117]
	v_mfma_f32_16x16x32_bf16 v[102:105], v[182:185], v[212:215], v[102:105]
	v_mfma_f32_16x16x32_bf16 v[98:101], v[196:199], v[212:215], v[98:101]
	v_mfma_f32_16x16x32_bf16 v[86:89], v[182:185], v[220:223], v[86:89]
	v_mfma_f32_16x16x32_bf16 v[82:85], v[196:199], v[220:223], v[82:85]
	v_mfma_f32_16x16x32_bf16 v[70:73], v[182:185], v[230:233], v[70:73]
	v_mfma_f32_16x16x32_bf16 v[66:69], v[196:199], v[230:233], v[66:69]
	s_setprio 0
	s_barrier
	s_add_i32 s61, s39, s2
	v_lshl_add_u64 v[168:169], s[24:25], 0, v[146:147]
	s_mov_b32 m0, s61
	ds_read_b128 v[200:203], v189 offset:16384
	ds_read_b128 v[204:207], v189 offset:17408
	ds_read_b128 v[208:211], v189 offset:18432
	ds_read_b128 v[212:215], v189 offset:19456
	ds_read_b128 v[216:219], v189 offset:20480
	ds_read_b128 v[220:223], v189 offset:21504
	ds_read_b128 v[224:227], v189 offset:22528
	ds_read_b128 v[230:233], v189 offset:23552
	global_load_lds_dwordx4 v[168:169], off
	s_add_i32 m0, s61, 0x2000
	s_add_u32 s62, s24, 0x40000
	v_lshl_add_u64 v[172:173], s[24:25], 0, v[142:143]
	s_addc_u32 s63, s25, 0
	s_add_i32 s61, s48, s2
	global_load_lds_dwordx4 v[172:173], off
	v_lshl_add_u64 v[176:177], s[62:63], 0, v[146:147]
	s_mov_b32 m0, s61
	v_lshl_add_u64 v[234:235], s[26:27], 0, v[144:145]
	global_load_lds_dwordx4 v[176:177], off
	v_lshl_add_u64 v[176:177], s[62:63], 0, v[142:143]
	s_add_i32 m0, s61, 0x2000
	s_nop 0
	global_load_lds_dwordx4 v[176:177], off
	v_lshl_add_u64 v[176:177], s[26:27], 0, v[148:149]
	s_mov_b32 m0, s29
	s_nop 0
	global_load_lds_dwordx4 v[176:177], off
	s_mov_b32 m0, s30
	s_nop 0
	global_load_lds_dwordx4 v[234:235], off
	s_waitcnt vmcnt(8)
	s_waitcnt lgkmcnt(0)
	s_barrier
; #define PG8_STAGE_A(b, h, ptr, NX) do { if constexpr (Sched::GATHER) { unsigned gs_[2]; gs_[0] = ((NX) && last_) ? gN[h][0] : gA[h][0]; gs_[1] = ((NX) && last_) ? gN[h][1] : gA[h][1]; PG8_STAGE(PG8_SA(b, h), ptr, gs_); } \
;         else PG8_STAGE(PG8_SA(b, h), (ptr) + ((h) ? hstep : (size_t)0), voffA); } while (0)
; #define PG8_STAGE(bufoff, gbase, voff) do { _Pragma("unroll") for (int _i = 0; _i < 2; ++_i) \
;         __builtin_amdgcn_global_load_lds((const unsigned*)((const char*)(gbase) + (voff)[_i]), (PG8_LAS unsigned*)(lds + (bufoff) + ldsw + _i * 8192), 16, 0, 0); } while (0)
; #define PG8_LDA(dst, b, h) do { _Pragma("unroll") for (int m = 0; m < 4; ++m) _Pragma("unroll") for (int k = 0; k < 2; ++k) dst[m][k] = *(const PG8_LAS bf16x8*)(lds + PG8_SA(b, h) + aoff + m * 2048 + k * 1024); } while (0)
; #define PG8_LDB(dst, b, h) do { _Pragma("unroll") for (int n = 0; n < 2; ++n) _Pragma("unroll") for (int k = 0; k < 2; ++k) dst[n][k] = *(const PG8_LAS bf16x8*)(lds + PG8_SB(b, h) + boff + n * 2048 + k * 1024); } while (0)
; #define PG8_MMA(ai, bj, At, Bt) do { __builtin_amdgcn_s_setprio(1); _Pragma("unroll") for (int m = 0; m < 4; ++m) _Pragma("unroll") for (int n = 0; n < 2; ++n) _Pragma("unroll") for (int k = 0; k < 2; ++k) \
;         acc[ai][bj][m][n] = __builtin_amdgcn_mfma_f32_16x16x32_bf16(Bt[n][k], At[m][k], acc[ai][bj][m][n], 0, 0, 0); __builtin_amdgcn_s_setprio(0); } while (0)
; #define PG8_WAIT_V(n) asm volatile("s_waitcnt vmcnt(" #n ")" ::: "memory")
; #define PG8_WAIT_L(n) asm volatile("s_waitcnt lgkmcnt(" #n ")" ::: "memory")
; #define PG8_BAR __builtin_amdgcn_s_barrier()
; #define PG8_SCHED __builtin_amdgcn_sched_barrier(0)
; template <class Epi, class Sched, bool ALIGN_EPI = false, bool SP2 = false>
; __device__ __forceinline__ void gemm_phase(PG8_LAS unsigned char* lds, const Gemm g, const Sched& S, const Epi& E, const bool skip_epi = false) {
;     ...
;             PG8_WAIT_V(8); PG8_WAIT_L(0); PG8_BAR; PG8_MMA(1, 0, At, B0); PG8_MMA(1, 1, At, B1); PG8_BAR; PG8_SCHED;
;             PG8_LDB(B0, 1, 0); PG8_LDB(B1, 1, 1); PG8_SCHED; PG8_LDA(At, 1, 0); PG8_STAGE_A(0, 1, a2, true);
;             PG8_WAIT_V(8); PG8_WAIT_L(0); PG8_BAR; PG8_MMA(0, 0, At, B0); PG8_MMA(0, 1, At, B1); PG8_BAR; PG8_SCHED;
;             PG8_LDA(At, 1, 1); PG8_STAGE(PG8_SB(1, 0), b3, voffB); PG8_STAGE(PG8_SB(1, 1), b3 + hstep, voffB); PG8_STAGE_A(1, 0, a3, true);
	s_setprio 1
	s_waitcnt lgkmcnt(0)
	v_mfma_f32_16x16x32_bf16 v[62:65], v[130:133], v[200:203], 0
	v_mfma_f32_16x16x32_bf16 v[58:61], v[138:141], v[200:203], 0
	v_mfma_f32_16x16x32_bf16 v[46:49], v[130:133], v[208:211], 0
	v_mfma_f32_16x16x32_bf16 v[42:45], v[138:141], v[208:211], 0
	v_mfma_f32_16x16x32_bf16 v[30:33], v[130:133], v[216:219], 0
	v_mfma_f32_16x16x32_bf16 v[26:29], v[138:141], v[216:219], 0
	v_mfma_f32_16x16x32_bf16 v[14:17], v[130:133], v[224:227], 0
	v_mfma_f32_16x16x32_bf16 v[10:13], v[138:141], v[224:227], 0
	v_mfma_f32_16x16x32_bf16 v[62:65], v[134:137], v[204:207], v[62:65]
	v_mfma_f32_16x16x32_bf16 v[58:61], v[160:163], v[204:207], v[58:61]
	v_mfma_f32_16x16x32_bf16 v[46:49], v[134:137], v[212:215], v[46:49]
	v_mfma_f32_16x16x32_bf16 v[42:45], v[160:163], v[212:215], v[42:45]
	v_mfma_f32_16x16x32_bf16 v[30:33], v[134:137], v[220:223], v[30:33]
	v_mfma_f32_16x16x32_bf16 v[26:29], v[160:163], v[220:223], v[26:29]
	v_mfma_f32_16x16x32_bf16 v[14:17], v[134:137], v[230:233], v[14:17]
	v_mfma_f32_16x16x32_bf16 v[10:13], v[160:163], v[230:233], v[10:13]
	s_setprio 0
	s_setprio 1
	v_mfma_f32_16x16x32_bf16 v[54:57], v[164:167], v[200:203], 0
	v_mfma_f32_16x16x32_bf16 v[50:53], v[192:195], v[200:203], 0
	v_mfma_f32_16x16x32_bf16 v[38:41], v[164:167], v[208:211], 0
	v_mfma_f32_16x16x32_bf16 v[34:37], v[192:195], v[208:211], 0
	v_mfma_f32_16x16x32_bf16 v[22:25], v[164:167], v[216:219], 0
	v_mfma_f32_16x16x32_bf16 v[18:21], v[192:195], v[216:219], 0
	v_mfma_f32_16x16x32_bf16 v[6:9], v[164:167], v[224:227], 0
	v_mfma_f32_16x16x32_bf16 v[2:5], v[192:195], v[224:227], 0
	v_mfma_f32_16x16x32_bf16 v[54:57], v[182:185], v[204:207], v[54:57]
	v_mfma_f32_16x16x32_bf16 v[50:53], v[196:199], v[204:207], v[50:53]
	v_mfma_f32_16x16x32_bf16 v[38:41], v[182:185], v[212:215], v[38:41]
	v_mfma_f32_16x16x32_bf16 v[34:37], v[196:199], v[212:215], v[34:37]
	v_mfma_f32_16x16x32_bf16 v[22:25], v[182:185], v[220:223], v[22:25]
	v_mfma_f32_16x16x32_bf16 v[18:21], v[196:199], v[220:223], v[18:21]
	v_mfma_f32_16x16x32_bf16 v[6:9], v[182:185], v[230:233], v[6:9]
	v_mfma_f32_16x16x32_bf16 v[2:5], v[196:199], v[230:233], v[2:5]
	s_setprio 0
	s_barrier
	s_add_i32 s61, 0, 0x18000
	s_add_i32 s62, 0, 0x1c000
	v_add_u32_e32 v160, s61, v1
	v_add_u32_e32 v170, s62, v1
	ds_read_b128 v[130:133], v160
	ds_read_b128 v[134:137], v160 offset:1024
	ds_read_b128 v[138:141], v160 offset:2048
	ds_read_b128 v[160:163], v160 offset:3072
	ds_read_b128 v[164:167], v170
	ds_read_b128 v[182:185], v170 offset:1024
	ds_read_b128 v[192:195], v170 offset:2048
	ds_read_b128 v[196:199], v170 offset:3072
	s_add_u32 s26, s26, 0x40000
	s_addc_u32 s27, s27, 0
	s_mov_b32 m0, s31
	v_lshl_add_u64 v[236:237], s[26:27], 0, v[148:149]
	ds_read_b128 v[200:203], v189 offset:32768
	ds_read_b128 v[204:207], v189 offset:33792
	ds_read_b128 v[208:211], v189 offset:34816
	ds_read_b128 v[212:215], v189 offset:35840
	ds_read_b128 v[216:219], v189 offset:36864
	ds_read_b128 v[220:223], v189 offset:37888
	ds_read_b128 v[224:227], v189 offset:38912
	ds_read_b128 v[230:233], v189 offset:39936
	global_load_lds_dwordx4 v[236:237], off
	v_lshl_add_u64 v[236:237], s[26:27], 0, v[144:145]
	s_mov_b32 m0, s34
	s_nop 0
	global_load_lds_dwordx4 v[236:237], off
	s_waitcnt vmcnt(8)
	s_waitcnt lgkmcnt(0)
	s_barrier
	s_setprio 1
	s_waitcnt lgkmcnt(0)
	v_mfma_f32_16x16x32_bf16 v[126:129], v[130:133], v[200:203], v[126:129]
	v_mfma_f32_16x16x32_bf16 v[122:125], v[138:141], v[200:203], v[122:125]
	v_mfma_f32_16x16x32_bf16 v[110:113], v[130:133], v[208:211], v[110:113]
	v_mfma_f32_16x16x32_bf16 v[106:109], v[138:141], v[208:211], v[106:109]
	v_mfma_f32_16x16x32_bf16 v[94:97], v[130:133], v[216:219], v[94:97]
	v_mfma_f32_16x16x32_bf16 v[90:93], v[138:141], v[216:219], v[90:93]
	v_mfma_f32_16x16x32_bf16 v[78:81], v[130:133], v[224:227], v[78:81]
	v_mfma_f32_16x16x32_bf16 v[74:77], v[138:141], v[224:227], v[74:77]
	v_mfma_f32_16x16x32_bf16 v[126:129], v[134:137], v[204:207], v[126:129]
	v_mfma_f32_16x16x32_bf16 v[122:125], v[160:163], v[204:207], v[122:125]
	v_mfma_f32_16x16x32_bf16 v[110:113], v[134:137], v[212:215], v[110:113]
	v_mfma_f32_16x16x32_bf16 v[106:109], v[160:163], v[212:215], v[106:109]
	v_mfma_f32_16x16x32_bf16 v[94:97], v[134:137], v[220:223], v[94:97]
	v_mfma_f32_16x16x32_bf16 v[90:93], v[160:163], v[220:223], v[90:93]
	v_mfma_f32_16x16x32_bf16 v[78:81], v[134:137], v[230:233], v[78:81]
	v_mfma_f32_16x16x32_bf16 v[74:77], v[160:163], v[230:233], v[74:77]
	s_setprio 0
	s_setprio 1
	v_mfma_f32_16x16x32_bf16 v[118:121], v[164:167], v[200:203], v[118:121]
	v_mfma_f32_16x16x32_bf16 v[114:117], v[192:195], v[200:203], v[114:117]
	v_mfma_f32_16x16x32_bf16 v[102:105], v[164:167], v[208:211], v[102:105]
	v_mfma_f32_16x16x32_bf16 v[98:101], v[192:195], v[208:211], v[98:101]
	v_mfma_f32_16x16x32_bf16 v[86:89], v[164:167], v[216:219], v[86:89]
	v_mfma_f32_16x16x32_bf16 v[82:85], v[192:195], v[216:219], v[82:85]
	v_mfma_f32_16x16x32_bf16 v[70:73], v[164:167], v[224:227], v[70:73]
	v_mfma_f32_16x16x32_bf16 v[66:69], v[192:195], v[224:227], v[66:69]
	v_mfma_f32_16x16x32_bf16 v[118:121], v[182:185], v[204:207], v[118:121]
	v_mfma_f32_16x16x32_bf16 v[114:117], v[196:199], v[204:207], v[114:117]
	v_mfma_f32_16x16x32_bf16 v[102:105], v[182:185], v[212:215], v[102:105]
	v_mfma_f32_16x16x32_bf16 v[98:101], v[196:199], v[212:215], v[98:101]
	v_mfma_f32_16x16x32_bf16 v[86:89], v[182:185], v[220:223], v[86:89]
	v_mfma_f32_16x16x32_bf16 v[82:85], v[196:199], v[220:223], v[82:85]
	v_mfma_f32_16x16x32_bf16 v[70:73], v[182:185], v[230:233], v[70:73]
	v_mfma_f32_16x16x32_bf16 v[66:69], v[196:199], v[230:233], v[66:69]
	s_setprio 0
	s_barrier
; #define PG8_STAGE_A(b, h, ptr, NX) do { if constexpr (Sched::GATHER) { unsigned gs_[2]; gs_[0] = ((NX) && last_) ? gN[h][0] : gA[h][0]; gs_[1] = ((NX) && last_) ? gN[h][1] : gA[h][1]; PG8_STAGE(PG8_SA(b, h), ptr, gs_); } \
;         else PG8_STAGE(PG8_SA(b, h), (ptr) + ((h) ? hstep : (size_t)0), voffA); } while (0)
; #define PG8_STAGE(bufoff, gbase, voff) do { _Pragma("unroll") for (int _i = 0; _i < 2; ++_i) \
;         __builtin_amdgcn_global_load_lds((const unsigned*)((const char*)(gbase) + (voff)[_i]), (PG8_LAS unsigned*)(lds + (bufoff) + ldsw + _i * 8192), 16, 0, 0); } while (0)
; #define PG8_LDA(dst, b, h) do { _Pragma("unroll") for (int m = 0; m < 4; ++m) _Pragma("unroll") for (int k = 0; k < 2; ++k) dst[m][k] = *(const PG8_LAS bf16x8*)(lds + PG8_SA(b, h) + aoff + m * 2048 + k * 1024); } while (0)
; #define PG8_MMA(ai, bj, At, Bt) do { __builtin_amdgcn_s_setprio(1); _Pragma("unroll") for (int m = 0; m < 4; ++m) _Pragma("unroll") for (int n = 0; n < 2; ++n) _Pragma("unroll") for (int k = 0; k < 2; ++k) \
;         acc[ai][bj][m][n] = __builtin_amdgcn_mfma_f32_16x16x32_bf16(Bt[n][k], At[m][k], acc[ai][bj][m][n], 0, 0, 0); __builtin_amdgcn_s_setprio(0); } while (0)
; #define PG8_WAIT_V(n) asm volatile("s_waitcnt vmcnt(" #n ")" ::: "memory")
; #define PG8_WAIT_L(n) asm volatile("s_waitcnt lgkmcnt(" #n ")" ::: "memory")
; #define PG8_BAR __builtin_amdgcn_s_barrier()
; #define PG8_SCHED __builtin_amdgcn_sched_barrier(0)
; template <class Epi, class Sched, bool ALIGN_EPI = false, bool SP2 = false>
; __device__ __forceinline__ void gemm_phase(PG8_LAS unsigned char* lds, const Gemm g, const Sched& S, const Epi& E, const bool skip_epi = false) {
;     ...
;         for (int t = 0; t < nt; t += 2) {
;     ...
;             PG8_LDA(At, 1, 1); PG8_STAGE(PG8_SB(1, 0), b3, voffB); PG8_STAGE(PG8_SB(1, 1), b3 + hstep, voffB); PG8_STAGE_A(1, 0, a3, true);
;             PG8_WAIT_V(8); PG8_WAIT_L(0); PG8_BAR; PG8_MMA(1, 0, At, B0); PG8_MMA(1, 1, At, B1); PG8_BAR; PG8_SCHED;
	s_add_i32 s26, s61, s2
	v_lshl_add_u64 v[168:169], v[168:169], 0, s[8:9]
	s_mov_b32 m0, s26
	ds_read_b128 v[200:203], v189 offset:49152
	ds_read_b128 v[204:207], v189 offset:50176
	ds_read_b128 v[208:211], v189 offset:51200
	ds_read_b128 v[212:215], v189 offset:52224
	ds_read_b128 v[216:219], v189 offset:53248
	ds_read_b128 v[220:223], v189 offset:54272
	ds_read_b128 v[224:227], v189 offset:55296
	ds_read_b128 v[230:233], v189 offset:56320
	global_load_lds_dwordx4 v[168:169], off
	s_add_i32 m0, s26, 0x2000
	s_add_u32 s24, s24, 0x40080
	v_lshl_add_u64 v[168:169], v[172:173], 0, s[8:9]
	s_addc_u32 s25, s25, 0
	s_add_i32 s26, s62, s2
	global_load_lds_dwordx4 v[168:169], off
	v_lshl_add_u64 v[168:169], s[24:25], 0, v[146:147]
	s_mov_b32 m0, s26
	s_nop 0
	global_load_lds_dwordx4 v[168:169], off
	v_lshl_add_u64 v[168:169], s[24:25], 0, v[142:143]
	s_add_i32 m0, s26, 0x2000
	s_nop 0
	global_load_lds_dwordx4 v[168:169], off
	v_lshl_add_u64 v[168:169], v[176:177], 0, s[8:9]
	s_mov_b32 m0, s36
	s_nop 0
	global_load_lds_dwordx4 v[168:169], off
	v_lshl_add_u64 v[168:169], v[234:235], 0, s[8:9]
	s_mov_b32 m0, s37
	s_nop 0
	global_load_lds_dwordx4 v[168:169], off
	s_waitcnt vmcnt(8)
	s_waitcnt lgkmcnt(0)
	s_barrier
	s_setprio 1
	s_waitcnt lgkmcnt(0)
	v_mfma_f32_16x16x32_bf16 v[62:65], v[130:133], v[200:203], v[62:65]
	v_mfma_f32_16x16x32_bf16 v[58:61], v[138:141], v[200:203], v[58:61]
	v_mfma_f32_16x16x32_bf16 v[46:49], v[130:133], v[208:211], v[46:49]
	v_mfma_f32_16x16x32_bf16 v[42:45], v[138:141], v[208:211], v[42:45]
	v_mfma_f32_16x16x32_bf16 v[30:33], v[130:133], v[216:219], v[30:33]
	v_mfma_f32_16x16x32_bf16 v[26:29], v[138:141], v[216:219], v[26:29]
	v_mfma_f32_16x16x32_bf16 v[14:17], v[130:133], v[224:227], v[14:17]
	v_mfma_f32_16x16x32_bf16 v[10:13], v[138:141], v[224:227], v[10:13]
	v_mfma_f32_16x16x32_bf16 v[62:65], v[134:137], v[204:207], v[62:65]
	v_mfma_f32_16x16x32_bf16 v[58:61], v[160:163], v[204:207], v[58:61]
	v_mfma_f32_16x16x32_bf16 v[46:49], v[134:137], v[212:215], v[46:49]
	v_mfma_f32_16x16x32_bf16 v[42:45], v[160:163], v[212:215], v[42:45]
	v_mfma_f32_16x16x32_bf16 v[30:33], v[134:137], v[220:223], v[30:33]
	v_mfma_f32_16x16x32_bf16 v[26:29], v[160:163], v[220:223], v[26:29]
	v_mfma_f32_16x16x32_bf16 v[14:17], v[134:137], v[230:233], v[14:17]
	v_mfma_f32_16x16x32_bf16 v[10:13], v[160:163], v[230:233], v[10:13]
	s_setprio 0
	s_setprio 1
	v_mfma_f32_16x16x32_bf16 v[54:57], v[164:167], v[200:203], v[54:57]
	v_mfma_f32_16x16x32_bf16 v[50:53], v[192:195], v[200:203], v[50:53]
	v_mfma_f32_16x16x32_bf16 v[38:41], v[164:167], v[208:211], v[38:41]
	v_mfma_f32_16x16x32_bf16 v[34:37], v[192:195], v[208:211], v[34:37]
	v_mfma_f32_16x16x32_bf16 v[22:25], v[164:167], v[216:219], v[22:25]
	v_mfma_f32_16x16x32_bf16 v[18:21], v[192:195], v[216:219], v[18:21]
	v_mfma_f32_16x16x32_bf16 v[6:9], v[164:167], v[224:227], v[6:9]
	v_mfma_f32_16x16x32_bf16 v[2:5], v[192:195], v[224:227], v[2:5]
	v_mfma_f32_16x16x32_bf16 v[54:57], v[182:185], v[204:207], v[54:57]
	v_mfma_f32_16x16x32_bf16 v[50:53], v[196:199], v[204:207], v[50:53]
	v_mfma_f32_16x16x32_bf16 v[38:41], v[182:185], v[212:215], v[38:41]
	v_mfma_f32_16x16x32_bf16 v[34:37], v[196:199], v[212:215], v[34:37]
	v_mfma_f32_16x16x32_bf16 v[22:25], v[182:185], v[220:223], v[22:25]
	v_mfma_f32_16x16x32_bf16 v[18:21], v[196:199], v[220:223], v[18:21]
	v_mfma_f32_16x16x32_bf16 v[6:9], v[182:185], v[230:233], v[6:9]
	v_mfma_f32_16x16x32_bf16 v[2:5], v[196:199], v[230:233], v[2:5]
	s_setprio 0
	s_barrier
	s_add_i32 s60, s60, 2
	s_add_u32 s22, s22, 0x100
	s_addc_u32 s23, s23, 0
	s_add_u32 s58, s58, 0x100
	s_addc_u32 s59, s59, 0
	s_cmp_gt_u32 s60, 13

; template <class Epi, class Sched, bool ALIGN_EPI = false, bool SP2 = false>
; __device__ __forceinline__ void gemm_phase(PG8_LAS unsigned char* lds, const Gemm g, const Sched& S, const Epi& E, const bool skip_epi = false) {
;     ...
;     for (;;) {
;         const bool has_next = S.next(ui + 1, nxt);
;         if (has_next) PG8_GIDX(gN, nxt.pm);
;         const char* nA = has_next ? (const char*)g.A + (size_t)nxt.pm * pmstepA + nxt.ko : cA; const char* nB = has_next ? (const char*)g.Bt + (size_t)nxt.pn * tstep + nxt.ko : cB;
;         for (int t = 0; t < nt; t += 2) {
;             const bool last = (t == nt - 2); last_ = last && has_next;
;             const char* a1 = cA + (size_t)(t + 1) * kstep;
;             const char* a2 = last ? nA : cA + (size_t)(t + 2) * kstep; const char* b2 = last ? nB : cB + (size_t)(t + 2) * kstep;
;             const char* a3 = a2 + kstep; const char* b3 = b2 + kstep;
;             if (last && has_next) S.a_ready(nxt);
;             if constexpr (SP2) {
;             PG8_LDB(B0, 0, 0); PG8_LDB(B1, 0, 1); PG8_SCHED; PG8_LDA(At, 0, 0); PG8_STAGE_A(1, 1, a1, false);
;             PG8_WAIT_V(8); PG8_WAIT_L(0); PG8_BAR; PG8_MMA(0, 0, At, B0); PG8_MMA(0, 1, At, B1); PG8_BAR; PG8_SCHED;
;             PG8_LDA(At, 0, 1); PG8_STAGE(PG8_SB(0, 0), b2, voffB); PG8_STAGE(PG8_SB(0, 1), b2 + hstep, voffB); PG8_STAGE_A(0, 0, a2, true);
;             PG8_WAIT_V(8); PG8_WAIT_L(0); PG8_BAR; PG8_MMA(1, 0, At, B0); PG8_MMA(1, 1, At, B1); PG8_BAR; PG8_SCHED;
;             PG8_LDB(B0, 1, 0); PG8_LDB(B1, 1, 1); PG8_SCHED; PG8_LDA(At, 1, 0); PG8_STAGE_A(0, 1, a2, true);
;             PG8_WAIT_V(8); PG8_WAIT_L(0); PG8_BAR; PG8_MMA(0, 0, At, B0); PG8_MMA(0, 1, At, B1); PG8_BAR; PG8_SCHED;
;             PG8_LDA(At, 1, 1); PG8_STAGE(PG8_SB(1, 0), b3, voffB); PG8_STAGE(PG8_SB(1, 1), b3 + hstep, voffB); PG8_STAGE_A(1, 0, a3, true);
;             PG8_WAIT_V(8); PG8_WAIT_L(0); PG8_BAR; PG8_MMA(1, 0, At, B0); PG8_MMA(1, 1, At, B1); PG8_BAR; PG8_SCHED;
; template <int layer> __device__ __forceinline__ void layer_phases(const Ctx& c, unsigned char* lds) {
;     ...
;                 pg8::Gemm g{H, W2, M, D, FF, FF}; pg8::StaticOrder S; S.init(M, D, G, bx);
;     ...
;                 if (dry) { pg8::EpiRes<false, PROBE_EPI> E{XB, XBD, SSD}; pg8::gemm_phase<pg8::EpiRes<false, PROBE_EPI>, pg8::StaticOrder, true, true>(ldsl, g, S, E, noepi); } else
.LBB0_856:
	s_add_u32 s55, s22, 0x100
	s_addc_u32 s56, s23, 0
	s_mov_b32 s57, -2
	s_waitcnt vmcnt(0)
	s_waitcnt lgkmcnt(0)
	ds_read_b128 v[98:101], v234
	ds_read_b128 v[110:113], v234 offset:1024
	ds_read_b128 v[122:125], v234 offset:2048
	ds_read_b128 v[126:129], v234 offset:3072
	ds_read_b128 v[138:141], v235
	ds_read_b128 v[142:145], v235 offset:1024
	ds_read_b128 v[146:149], v235 offset:2048
	ds_read_b128 v[150:153], v235 offset:3072
	s_add_u32 s22, s20, 0x100
	s_addc_u32 s23, s21, 0
	s_cmp_eq_u32 s57, 40
	s_cselect_b32 s27, s9, s23
	s_cselect_b32 s26, s8, s22
	s_cselect_b32 s25, s19, s56
	s_cselect_b32 s24, s18, s55
	v_lshl_add_u64 v[210:211], s[20:21], 0, v[198:199]
	s_add_i32 m0, s3, 0xc000
	ds_read_b128 v[154:157], v236
	ds_read_b128 v[166:169], v236 offset:1024
	ds_read_b128 v[170:173], v236 offset:2048
	ds_read_b128 v[174:177], v236 offset:3072
	ds_read_b128 v[178:181], v236 offset:4096
	ds_read_b128 v[182:185], v236 offset:5120
	ds_read_b128 v[186:189], v236 offset:6144
	ds_read_b128 v[206:209], v236 offset:7168
	global_load_lds_dwordx4 v[210:211], off
	v_lshl_add_u64 v[210:211], s[20:21], 0, v[200:201]
	s_add_i32 m0, s3, 0xe000
	s_nop 0
	global_load_lds_dwordx4 v[210:211], off
	s_waitcnt vmcnt(8)
	s_waitcnt lgkmcnt(0)
	s_barrier
	s_setprio 1
	s_waitcnt lgkmcnt(0)
	v_mfma_f32_16x16x32_bf16 v[162:165], v[98:101], v[154:157], 0
	v_mfma_f32_16x16x32_bf16 v[158:161], v[122:125], v[154:157], 0
	v_mfma_f32_16x16x32_bf16 v[118:121], v[98:101], v[170:173], 0
	v_mfma_f32_16x16x32_bf16 v[114:117], v[122:125], v[170:173], 0
	v_mfma_f32_16x16x32_bf16 v[94:97], v[98:101], v[178:181], 0
	v_mfma_f32_16x16x32_bf16 v[90:93], v[122:125], v[178:181], 0
	v_mfma_f32_16x16x32_bf16 v[78:81], v[98:101], v[186:189], 0
	v_mfma_f32_16x16x32_bf16 v[74:77], v[122:125], v[186:189], 0
	v_mfma_f32_16x16x32_bf16 v[162:165], v[110:113], v[166:169], v[162:165]
	v_mfma_f32_16x16x32_bf16 v[158:161], v[126:129], v[166:169], v[158:161]
	v_mfma_f32_16x16x32_bf16 v[118:121], v[110:113], v[174:177], v[118:121]
	v_mfma_f32_16x16x32_bf16 v[114:117], v[126:129], v[174:177], v[114:117]
	v_mfma_f32_16x16x32_bf16 v[94:97], v[110:113], v[182:185], v[94:97]
	v_mfma_f32_16x16x32_bf16 v[90:93], v[126:129], v[182:185], v[90:93]
	v_mfma_f32_16x16x32_bf16 v[78:81], v[110:113], v[206:209], v[78:81]
	v_mfma_f32_16x16x32_bf16 v[74:77], v[126:129], v[206:209], v[74:77]
	s_setprio 0
	s_setprio 1
	v_mfma_f32_16x16x32_bf16 v[134:137], v[138:141], v[154:157], 0
	v_mfma_f32_16x16x32_bf16 v[130:133], v[146:149], v[154:157], 0
	v_mfma_f32_16x16x32_bf16 v[106:109], v[138:141], v[170:173], 0
	v_mfma_f32_16x16x32_bf16 v[102:105], v[146:149], v[170:173], 0
	v_mfma_f32_16x16x32_bf16 v[86:89], v[138:141], v[178:181], 0
	v_mfma_f32_16x16x32_bf16 v[82:85], v[146:149], v[178:181], 0
	v_mfma_f32_16x16x32_bf16 v[70:73], v[138:141], v[186:189], 0
	v_mfma_f32_16x16x32_bf16 v[66:69], v[146:149], v[186:189], 0
	v_mfma_f32_16x16x32_bf16 v[134:137], v[142:145], v[166:169], v[134:137]
	v_mfma_f32_16x16x32_bf16 v[130:133], v[150:153], v[166:169], v[130:133]
	v_mfma_f32_16x16x32_bf16 v[106:109], v[142:145], v[174:177], v[106:109]
	v_mfma_f32_16x16x32_bf16 v[102:105], v[150:153], v[174:177], v[102:105]
	v_mfma_f32_16x16x32_bf16 v[86:89], v[142:145], v[182:185], v[86:89]
	v_mfma_f32_16x16x32_bf16 v[82:85], v[150:153], v[182:185], v[82:85]
	v_mfma_f32_16x16x32_bf16 v[70:73], v[142:145], v[206:209], v[70:73]
	v_mfma_f32_16x16x32_bf16 v[66:69], v[150:153], v[206:209], v[66:69]
	s_setprio 0
	s_barrier
	s_add_i32 s20, s39, s2
	v_lshl_add_u64 v[210:211], s[24:25], 0, v[192:193]
	s_mov_b32 m0, s20
	ds_read_b128 v[154:157], v236 offset:16384
	ds_read_b128 v[166:169], v236 offset:17408
	ds_read_b128 v[170:173], v236 offset:18432
	ds_read_b128 v[174:177], v236 offset:19456
	ds_read_b128 v[178:181], v236 offset:20480
	ds_read_b128 v[182:185], v236 offset:21504
	ds_read_b128 v[186:189], v236 offset:22528
	ds_read_b128 v[206:209], v236 offset:23552
	global_load_lds_dwordx4 v[210:211], off
	s_add_i32 m0, s20, 0x2000
	s_add_u32 s20, s24, 0xb0000
	v_lshl_add_u64 v[212:213], s[24:25], 0, v[196:197]
	s_addc_u32 s21, s25, 0
	s_add_i32 s58, s48, s2
	global_load_lds_dwordx4 v[212:213], off
	v_lshl_add_u64 v[214:215], s[20:21], 0, v[192:193]
	s_mov_b32 m0, s58
	v_lshl_add_u64 v[216:217], s[26:27], 0, v[194:195]
	global_load_lds_dwordx4 v[214:215], off
	v_lshl_add_u64 v[214:215], s[20:21], 0, v[196:197]
	s_add_i32 m0, s58, 0x2000
	s_nop 0
	global_load_lds_dwordx4 v[214:215], off
	v_lshl_add_u64 v[214:215], s[26:27], 0, v[190:191]
	s_mov_b32 m0, s3
	s_nop 0
	global_load_lds_dwordx4 v[214:215], off
	s_mov_b32 m0, s28
	s_nop 0
	global_load_lds_dwordx4 v[216:217], off
	s_waitcnt vmcnt(8)
	s_waitcnt lgkmcnt(0)
	s_barrier
; #define PG8_STAGE_A(b, h, ptr, NX) do { if constexpr (Sched::GATHER) { unsigned gs_[2]; gs_[0] = ((NX) && last_) ? gN[h][0] : gA[h][0]; gs_[1] = ((NX) && last_) ? gN[h][1] : gA[h][1]; PG8_STAGE(PG8_SA(b, h), ptr, gs_); } \
;         else PG8_STAGE(PG8_SA(b, h), (ptr) + ((h) ? hstep : (size_t)0), voffA); } while (0)
; #define PG8_STAGE(bufoff, gbase, voff) do { _Pragma("unroll") for (int _i = 0; _i < 2; ++_i) \
;         __builtin_amdgcn_global_load_lds((const unsigned*)((const char*)(gbase) + (voff)[_i]), (PG8_LAS unsigned*)(lds + (bufoff) + ldsw + _i * 8192), 16, 0, 0); } while (0)
; #define PG8_LDA(dst, b, h) do { _Pragma("unroll") for (int m = 0; m < 4; ++m) _Pragma("unroll") for (int k = 0; k < 2; ++k) dst[m][k] = *(const PG8_LAS bf16x8*)(lds + PG8_SA(b, h) + aoff + m * 2048 + k * 1024); } while (0)
; #define PG8_LDB(dst, b, h) do { _Pragma("unroll") for (int n = 0; n < 2; ++n) _Pragma("unroll") for (int k = 0; k < 2; ++k) dst[n][k] = *(const PG8_LAS bf16x8*)(lds + PG8_SB(b, h) + boff + n * 2048 + k * 1024); } while (0)
; #define PG8_MMA(ai, bj, At, Bt) do { __builtin_amdgcn_s_setprio(1); _Pragma("unroll") for (int m = 0; m < 4; ++m) _Pragma("unroll") for (int n = 0; n < 2; ++n) _Pragma("unroll") for (int k = 0; k < 2; ++k) \
;         acc[ai][bj][m][n] = __builtin_amdgcn_mfma_f32_16x16x32_bf16(Bt[n][k], At[m][k], acc[ai][bj][m][n], 0, 0, 0); __builtin_amdgcn_s_setprio(0); } while (0)
; #define PG8_WAIT_V(n) asm volatile("s_waitcnt vmcnt(" #n ")" ::: "memory")
; #define PG8_WAIT_L(n) asm volatile("s_waitcnt lgkmcnt(" #n ")" ::: "memory")
; #define PG8_BAR __builtin_amdgcn_s_barrier()
; #define PG8_SCHED __builtin_amdgcn_sched_barrier(0)
; template <class Epi, class Sched, bool ALIGN_EPI = false, bool SP2 = false>
; __device__ __forceinline__ void gemm_phase(PG8_LAS unsigned char* lds, const Gemm g, const Sched& S, const Epi& E, const bool skip_epi = false) {
;     ...
;             PG8_WAIT_V(8); PG8_WAIT_L(0); PG8_BAR; PG8_MMA(1, 0, At, B0); PG8_MMA(1, 1, At, B1); PG8_BAR; PG8_SCHED;
;             PG8_LDB(B0, 1, 0); PG8_LDB(B1, 1, 1); PG8_SCHED; PG8_LDA(At, 1, 0); PG8_STAGE_A(0, 1, a2, true);
;             PG8_WAIT_V(8); PG8_WAIT_L(0); PG8_BAR; PG8_MMA(0, 0, At, B0); PG8_MMA(0, 1, At, B1); PG8_BAR; PG8_SCHED;
;             PG8_LDA(At, 1, 1); PG8_STAGE(PG8_SB(1, 0), b3, voffB); PG8_STAGE(PG8_SB(1, 1), b3 + hstep, voffB); PG8_STAGE_A(1, 0, a3, true);
	s_setprio 1
	s_waitcnt lgkmcnt(0)
	v_mfma_f32_16x16x32_bf16 v[62:65], v[98:101], v[154:157], 0
	v_mfma_f32_16x16x32_bf16 v[58:61], v[122:125], v[154:157], 0
	v_mfma_f32_16x16x32_bf16 v[46:49], v[98:101], v[170:173], 0
	v_mfma_f32_16x16x32_bf16 v[42:45], v[122:125], v[170:173], 0
	v_mfma_f32_16x16x32_bf16 v[30:33], v[98:101], v[178:181], 0
	v_mfma_f32_16x16x32_bf16 v[26:29], v[122:125], v[178:181], 0
	v_mfma_f32_16x16x32_bf16 v[14:17], v[98:101], v[186:189], 0
	v_mfma_f32_16x16x32_bf16 v[10:13], v[122:125], v[186:189], 0
	v_mfma_f32_16x16x32_bf16 v[62:65], v[110:113], v[166:169], v[62:65]
	v_mfma_f32_16x16x32_bf16 v[58:61], v[126:129], v[166:169], v[58:61]
	v_mfma_f32_16x16x32_bf16 v[46:49], v[110:113], v[174:177], v[46:49]
	v_mfma_f32_16x16x32_bf16 v[42:45], v[126:129], v[174:177], v[42:45]
	v_mfma_f32_16x16x32_bf16 v[30:33], v[110:113], v[182:185], v[30:33]
	v_mfma_f32_16x16x32_bf16 v[26:29], v[126:129], v[182:185], v[26:29]
	v_mfma_f32_16x16x32_bf16 v[14:17], v[110:113], v[206:209], v[14:17]
	v_mfma_f32_16x16x32_bf16 v[10:13], v[126:129], v[206:209], v[10:13]
	s_setprio 0
	s_setprio 1
	v_mfma_f32_16x16x32_bf16 v[54:57], v[138:141], v[154:157], 0
	v_mfma_f32_16x16x32_bf16 v[50:53], v[146:149], v[154:157], 0
	v_mfma_f32_16x16x32_bf16 v[38:41], v[138:141], v[170:173], 0
	v_mfma_f32_16x16x32_bf16 v[34:37], v[146:149], v[170:173], 0
	v_mfma_f32_16x16x32_bf16 v[22:25], v[138:141], v[178:181], 0
	v_mfma_f32_16x16x32_bf16 v[18:21], v[146:149], v[178:181], 0
	v_mfma_f32_16x16x32_bf16 v[6:9], v[138:141], v[186:189], 0
	v_mfma_f32_16x16x32_bf16 v[2:5], v[146:149], v[186:189], 0
	v_mfma_f32_16x16x32_bf16 v[54:57], v[142:145], v[166:169], v[54:57]
	v_mfma_f32_16x16x32_bf16 v[50:53], v[150:153], v[166:169], v[50:53]
	v_mfma_f32_16x16x32_bf16 v[38:41], v[142:145], v[174:177], v[38:41]
	v_mfma_f32_16x16x32_bf16 v[34:37], v[150:153], v[174:177], v[34:37]
	v_mfma_f32_16x16x32_bf16 v[22:25], v[142:145], v[182:185], v[22:25]
	v_mfma_f32_16x16x32_bf16 v[18:21], v[150:153], v[182:185], v[18:21]
	v_mfma_f32_16x16x32_bf16 v[6:9], v[142:145], v[206:209], v[6:9]
	v_mfma_f32_16x16x32_bf16 v[2:5], v[150:153], v[206:209], v[2:5]
	s_setprio 0
	s_barrier
	s_add_i32 s58, 0, 0x18000
	s_add_i32 s59, 0, 0x1c000
	v_add_u32_e32 v126, s58, v229
	v_add_u32_e32 v150, s59, v229
	ds_read_b128 v[98:101], v126
	ds_read_b128 v[110:113], v126 offset:1024
	ds_read_b128 v[122:125], v126 offset:2048
	ds_read_b128 v[126:129], v126 offset:3072
	ds_read_b128 v[138:141], v150
	ds_read_b128 v[142:145], v150 offset:1024
	ds_read_b128 v[146:149], v150 offset:2048
	ds_read_b128 v[150:153], v150 offset:3072
	s_add_u32 s20, s26, 0xb0000
	s_addc_u32 s21, s27, 0
	s_mov_b32 m0, s29
	v_lshl_add_u64 v[218:219], s[20:21], 0, v[190:191]
	ds_read_b128 v[154:157], v236 offset:32768
	ds_read_b128 v[166:169], v236 offset:33792
	ds_read_b128 v[170:173], v236 offset:34816
	ds_read_b128 v[174:177], v236 offset:35840
	ds_read_b128 v[178:181], v236 offset:36864
	ds_read_b128 v[182:185], v236 offset:37888
	ds_read_b128 v[186:189], v236 offset:38912
	ds_read_b128 v[206:209], v236 offset:39936
	global_load_lds_dwordx4 v[218:219], off
	v_lshl_add_u64 v[218:219], s[20:21], 0, v[194:195]
	s_mov_b32 m0, s30
	s_nop 0
	global_load_lds_dwordx4 v[218:219], off
	s_waitcnt vmcnt(8)
	s_waitcnt lgkmcnt(0)
	s_barrier
	s_setprio 1
	s_waitcnt lgkmcnt(0)
	v_mfma_f32_16x16x32_bf16 v[162:165], v[98:101], v[154:157], v[162:165]
	v_mfma_f32_16x16x32_bf16 v[158:161], v[122:125], v[154:157], v[158:161]
	v_mfma_f32_16x16x32_bf16 v[118:121], v[98:101], v[170:173], v[118:121]
	v_mfma_f32_16x16x32_bf16 v[114:117], v[122:125], v[170:173], v[114:117]
	v_mfma_f32_16x16x32_bf16 v[94:97], v[98:101], v[178:181], v[94:97]
	v_mfma_f32_16x16x32_bf16 v[90:93], v[122:125], v[178:181], v[90:93]
	v_mfma_f32_16x16x32_bf16 v[78:81], v[98:101], v[186:189], v[78:81]
	v_mfma_f32_16x16x32_bf16 v[74:77], v[122:125], v[186:189], v[74:77]
	v_mfma_f32_16x16x32_bf16 v[162:165], v[110:113], v[166:169], v[162:165]
	v_mfma_f32_16x16x32_bf16 v[158:161], v[126:129], v[166:169], v[158:161]
	v_mfma_f32_16x16x32_bf16 v[118:121], v[110:113], v[174:177], v[118:121]
	v_mfma_f32_16x16x32_bf16 v[114:117], v[126:129], v[174:177], v[114:117]
	v_mfma_f32_16x16x32_bf16 v[94:97], v[110:113], v[182:185], v[94:97]
	v_mfma_f32_16x16x32_bf16 v[90:93], v[126:129], v[182:185], v[90:93]
	v_mfma_f32_16x16x32_bf16 v[78:81], v[110:113], v[206:209], v[78:81]
	v_mfma_f32_16x16x32_bf16 v[74:77], v[126:129], v[206:209], v[74:77]
	s_setprio 0
	s_setprio 1
	v_mfma_f32_16x16x32_bf16 v[134:137], v[138:141], v[154:157], v[134:137]
	v_mfma_f32_16x16x32_bf16 v[130:133], v[146:149], v[154:157], v[130:133]
	v_mfma_f32_16x16x32_bf16 v[106:109], v[138:141], v[170:173], v[106:109]
	v_mfma_f32_16x16x32_bf16 v[102:105], v[146:149], v[170:173], v[102:105]
	v_mfma_f32_16x16x32_bf16 v[86:89], v[138:141], v[178:181], v[86:89]
	v_mfma_f32_16x16x32_bf16 v[82:85], v[146:149], v[178:181], v[82:85]
	v_mfma_f32_16x16x32_bf16 v[70:73], v[138:141], v[186:189], v[70:73]
	v_mfma_f32_16x16x32_bf16 v[66:69], v[146:149], v[186:189], v[66:69]
	v_mfma_f32_16x16x32_bf16 v[134:137], v[142:145], v[166:169], v[134:137]
	v_mfma_f32_16x16x32_bf16 v[130:133], v[150:153], v[166:169], v[130:133]
	v_mfma_f32_16x16x32_bf16 v[106:109], v[142:145], v[174:177], v[106:109]
	v_mfma_f32_16x16x32_bf16 v[102:105], v[150:153], v[174:177], v[102:105]
	v_mfma_f32_16x16x32_bf16 v[86:89], v[142:145], v[182:185], v[86:89]
	v_mfma_f32_16x16x32_bf16 v[82:85], v[150:153], v[182:185], v[82:85]
	v_mfma_f32_16x16x32_bf16 v[70:73], v[142:145], v[206:209], v[70:73]
	v_mfma_f32_16x16x32_bf16 v[66:69], v[150:153], v[206:209], v[66:69]
	s_setprio 0
	s_barrier
; #define PG8_STAGE_A(b, h, ptr, NX) do { if constexpr (Sched::GATHER) { unsigned gs_[2]; gs_[0] = ((NX) && last_) ? gN[h][0] : gA[h][0]; gs_[1] = ((NX) && last_) ? gN[h][1] : gA[h][1]; PG8_STAGE(PG8_SA(b, h), ptr, gs_); } \
;         else PG8_STAGE(PG8_SA(b, h), (ptr) + ((h) ? hstep : (size_t)0), voffA); } while (0)
; #define PG8_STAGE(bufoff, gbase, voff) do { _Pragma("unroll") for (int _i = 0; _i < 2; ++_i) \
;         __builtin_amdgcn_global_load_lds((const unsigned*)((const char*)(gbase) + (voff)[_i]), (PG8_LAS unsigned*)(lds + (bufoff) + ldsw + _i * 8192), 16, 0, 0); } while (0)
; #define PG8_LDA(dst, b, h) do { _Pragma("unroll") for (int m = 0; m < 4; ++m) _Pragma("unroll") for (int k = 0; k < 2; ++k) dst[m][k] = *(const PG8_LAS bf16x8*)(lds + PG8_SA(b, h) + aoff + m * 2048 + k * 1024); } while (0)
; #define PG8_MMA(ai, bj, At, Bt) do { __builtin_amdgcn_s_setprio(1); _Pragma("unroll") for (int m = 0; m < 4; ++m) _Pragma("unroll") for (int n = 0; n < 2; ++n) _Pragma("unroll") for (int k = 0; k < 2; ++k) \
;         acc[ai][bj][m][n] = __builtin_amdgcn_mfma_f32_16x16x32_bf16(Bt[n][k], At[m][k], acc[ai][bj][m][n], 0, 0, 0); __builtin_amdgcn_s_setprio(0); } while (0)
; #define PG8_WAIT_V(n) asm volatile("s_waitcnt vmcnt(" #n ")" ::: "memory")
; #define PG8_WAIT_L(n) asm volatile("s_waitcnt lgkmcnt(" #n ")" ::: "memory")
; #define PG8_BAR __builtin_amdgcn_s_barrier()
; #define PG8_SCHED __builtin_amdgcn_sched_barrier(0)
; template <class Epi, class Sched, bool ALIGN_EPI = false, bool SP2 = false>
; __device__ __forceinline__ void gemm_phase(PG8_LAS unsigned char* lds, const Gemm g, const Sched& S, const Epi& E, const bool skip_epi = false) {
;     ...
;         for (int t = 0; t < nt; t += 2) {
;     ...
;             PG8_LDA(At, 1, 1); PG8_STAGE(PG8_SB(1, 0), b3, voffB); PG8_STAGE(PG8_SB(1, 1), b3 + hstep, voffB); PG8_STAGE_A(1, 0, a3, true);
;             PG8_WAIT_V(8); PG8_WAIT_L(0); PG8_BAR; PG8_MMA(1, 0, At, B0); PG8_MMA(1, 1, At, B1); PG8_BAR; PG8_SCHED;
	s_add_i32 s20, s58, s2
	v_lshl_add_u64 v[210:211], v[210:211], 0, s[14:15]
	s_mov_b32 m0, s20
	ds_read_b128 v[154:157], v236 offset:49152
	ds_read_b128 v[166:169], v236 offset:50176
	ds_read_b128 v[170:173], v236 offset:51200
	ds_read_b128 v[174:177], v236 offset:52224
	ds_read_b128 v[178:181], v236 offset:53248
	ds_read_b128 v[182:185], v236 offset:54272
	ds_read_b128 v[186:189], v236 offset:55296
	ds_read_b128 v[206:209], v236 offset:56320
	global_load_lds_dwordx4 v[210:211], off
	s_add_i32 m0, s20, 0x2000
	s_add_u32 s20, s24, 0xb0080
	v_lshl_add_u64 v[210:211], v[212:213], 0, s[14:15]
	s_addc_u32 s21, s25, 0
	s_add_i32 s24, s59, s2
	global_load_lds_dwordx4 v[210:211], off
	v_lshl_add_u64 v[210:211], s[20:21], 0, v[192:193]
	s_mov_b32 m0, s24
	s_nop 0
	global_load_lds_dwordx4 v[210:211], off
	v_lshl_add_u64 v[210:211], s[20:21], 0, v[196:197]
	s_add_i32 m0, s24, 0x2000
	s_nop 0
	global_load_lds_dwordx4 v[210:211], off
	v_lshl_add_u64 v[210:211], v[214:215], 0, s[14:15]
	s_mov_b32 m0, s35
	s_nop 0
	global_load_lds_dwordx4 v[210:211], off
	v_lshl_add_u64 v[210:211], v[216:217], 0, s[14:15]
	s_mov_b32 m0, s36
	s_nop 0
	global_load_lds_dwordx4 v[210:211], off
	s_waitcnt vmcnt(8)
	s_waitcnt lgkmcnt(0)
	s_barrier
	s_setprio 1
	s_waitcnt lgkmcnt(0)
	v_mfma_f32_16x16x32_bf16 v[62:65], v[98:101], v[154:157], v[62:65]
	v_mfma_f32_16x16x32_bf16 v[58:61], v[122:125], v[154:157], v[58:61]
	v_mfma_f32_16x16x32_bf16 v[46:49], v[98:101], v[170:173], v[46:49]
	v_mfma_f32_16x16x32_bf16 v[42:45], v[122:125], v[170:173], v[42:45]
	v_mfma_f32_16x16x32_bf16 v[30:33], v[98:101], v[178:181], v[30:33]
	v_mfma_f32_16x16x32_bf16 v[26:29], v[122:125], v[178:181], v[26:29]
	v_mfma_f32_16x16x32_bf16 v[14:17], v[98:101], v[186:189], v[14:17]
	v_mfma_f32_16x16x32_bf16 v[10:13], v[122:125], v[186:189], v[10:13]
	v_mfma_f32_16x16x32_bf16 v[62:65], v[110:113], v[166:169], v[62:65]
	v_mfma_f32_16x16x32_bf16 v[58:61], v[126:129], v[166:169], v[58:61]
	v_mfma_f32_16x16x32_bf16 v[46:49], v[110:113], v[174:177], v[46:49]
	v_mfma_f32_16x16x32_bf16 v[42:45], v[126:129], v[174:177], v[42:45]
	v_mfma_f32_16x16x32_bf16 v[30:33], v[110:113], v[182:185], v[30:33]
	v_mfma_f32_16x16x32_bf16 v[26:29], v[126:129], v[182:185], v[26:29]
	v_mfma_f32_16x16x32_bf16 v[14:17], v[110:113], v[206:209], v[14:17]
	v_mfma_f32_16x16x32_bf16 v[10:13], v[126:129], v[206:209], v[10:13]
	s_setprio 0
	s_setprio 1
	v_mfma_f32_16x16x32_bf16 v[54:57], v[138:141], v[154:157], v[54:57]
	v_mfma_f32_16x16x32_bf16 v[50:53], v[146:149], v[154:157], v[50:53]
	v_mfma_f32_16x16x32_bf16 v[38:41], v[138:141], v[170:173], v[38:41]
	v_mfma_f32_16x16x32_bf16 v[34:37], v[146:149], v[170:173], v[34:37]
	v_mfma_f32_16x16x32_bf16 v[22:25], v[138:141], v[178:181], v[22:25]
	v_mfma_f32_16x16x32_bf16 v[18:21], v[146:149], v[178:181], v[18:21]
	v_mfma_f32_16x16x32_bf16 v[6:9], v[138:141], v[186:189], v[6:9]
	v_mfma_f32_16x16x32_bf16 v[2:5], v[146:149], v[186:189], v[2:5]
	v_mfma_f32_16x16x32_bf16 v[54:57], v[142:145], v[166:169], v[54:57]
	v_mfma_f32_16x16x32_bf16 v[50:53], v[150:153], v[166:169], v[50:53]
	v_mfma_f32_16x16x32_bf16 v[38:41], v[142:145], v[174:177], v[38:41]
	v_mfma_f32_16x16x32_bf16 v[34:37], v[150:153], v[174:177], v[34:37]
	v_mfma_f32_16x16x32_bf16 v[22:25], v[142:145], v[182:185], v[22:25]
	v_mfma_f32_16x16x32_bf16 v[18:21], v[150:153], v[182:185], v[18:21]
	v_mfma_f32_16x16x32_bf16 v[6:9], v[142:145], v[206:209], v[6:9]
	v_mfma_f32_16x16x32_bf16 v[2:5], v[150:153], v[206:209], v[2:5]
	s_setprio 0
	s_barrier
	s_add_i32 s57, s57, 2
	s_add_u32 s55, s55, 0x100
	s_addc_u32 s56, s56, 0
	s_cmp_gt_u32 s57, 41
	s_mov_b64 s[20:21], s[22:23]

; #define PG8_GIDX(G_, PM_) do { if constexpr (Sched::GATHER) { _Pragma("unroll") for (int h_ = 0; h_ < 2; ++h_) _Pragma("unroll") for (int i_ = 0; i_ < 2; ++i_) { int R_, C_; stage_rc(tid * 16 + i_ * 8192, R_, C_); \
;         const int src_ = S.rowsrc[(PM_) * BM + h_ * HALF + R_]; G_[h_][i_] = (unsigned)(src_ * K + C_) * 2u; } } } while (0)
; #define PG8_WAIT_V(n) asm volatile("s_waitcnt vmcnt(" #n ")" ::: "memory")
; template <class Epi, class Sched, bool ALIGN_EPI = false, bool SP2 = false>
; __device__ __forceinline__ void gemm_phase(PG8_LAS unsigned char* lds, const Gemm g, const Sched& S, const Epi& E, const bool skip_epi = false) {
;     ...
;     for (;;) {
;         const bool has_next = S.next(ui + 1, nxt);
;         if (has_next) PG8_GIDX(gN, nxt.pm);
;         const char* nA = has_next ? (const char*)g.A + (size_t)nxt.pm * pmstepA + nxt.ko : cA; const char* nB = has_next ? (const char*)g.Bt + (size_t)nxt.pn * tstep + nxt.ko : cB;
;         for (int t = 0; t < nt; t += 2) {
;             const bool last = (t == nt - 2); last_ = last && has_next;
;             const char* a1 = cA + (size_t)(t + 1) * kstep;
;             const char* a2 = last ? nA : cA + (size_t)(t + 2) * kstep; const char* b2 = last ? nB : cB + (size_t)(t + 2) * kstep;
;             const char* a3 = a2 + kstep; const char* b3 = b2 + kstep;
;             if (last && has_next) S.a_ready(nxt);
;             if constexpr (SP2) {
;             PG8_LDB(B0, 0, 0); PG8_LDB(B1, 0, 1); PG8_SCHED; PG8_LDA(At, 0, 0); PG8_STAGE_A(1, 1, a1, false);
;             PG8_WAIT_V(8); PG8_WAIT_L(0); PG8_BAR; PG8_MMA(0, 0, At, B0); PG8_MMA(0, 1, At, B1); PG8_BAR; PG8_SCHED;
;             PG8_LDA(At, 0, 1); PG8_STAGE(PG8_SB(0, 0), b2, voffB); PG8_STAGE(PG8_SB(0, 1), b2 + hstep, voffB); PG8_STAGE_A(0, 0, a2, true);
;             PG8_WAIT_V(8); PG8_WAIT_L(0); PG8_BAR; PG8_MMA(1, 0, At, B0); PG8_MMA(1, 1, At, B1); PG8_BAR; PG8_SCHED;
;             PG8_LDB(B0, 1, 0); PG8_LDB(B1, 1, 1); PG8_SCHED; PG8_LDA(At, 1, 0); PG8_STAGE_A(0, 1, a2, true);
;             PG8_WAIT_V(8); PG8_WAIT_L(0); PG8_BAR; PG8_MMA(0, 0, At, B0); PG8_MMA(0, 1, At, B1); PG8_BAR; PG8_SCHED;
;             PG8_LDA(At, 1, 1); PG8_STAGE(PG8_SB(1, 0), b3, voffB); PG8_STAGE(PG8_SB(1, 1), b3 + hstep, voffB); PG8_STAGE_A(1, 0, a3, true);
;             PG8_WAIT_V(8); PG8_WAIT_L(0); PG8_BAR; PG8_MMA(1, 0, At, B0); PG8_MMA(1, 1, At, B1); PG8_BAR; PG8_SCHED;
.LBB0_943:
	s_ashr_i32 s15, s14, 31
	s_lshl_b64 s[16:17], s[14:15], 19
	s_add_u32 s16, s86, s16
	s_addc_u32 s17, s87, s17
	s_and_b64 s[18:19], s[4:5], exec
	s_cselect_b32 s15, s17, s23
	s_cselect_b32 s54, s16, s22
	s_ashr_i32 s13, s12, 31
	s_lshl_b64 s[18:19], s[12:13], 19
	s_add_u32 s18, s2, s18
	s_addc_u32 s19, s3, s19
	s_and_b64 s[26:27], s[4:5], exec
	s_cselect_b32 s13, s19, s25
	s_cselect_b32 s55, s18, s24
	s_add_u32 s22, s22, 0x40080
	s_addc_u32 s23, s23, 0
	s_add_u32 s56, s24, 0x100
	s_addc_u32 s57, s25, 0
	s_mov_b32 s58, -2
	s_waitcnt vmcnt(0)
	ds_read_b128 v[148:151], v170
	ds_read_b128 v[152:155], v170 offset:1024
	ds_read_b128 v[156:159], v170 offset:2048
	ds_read_b128 v[160:163], v170 offset:3072
	ds_read_b128 v[176:179], v171
	ds_read_b128 v[180:183], v171 offset:1024
	ds_read_b128 v[184:187], v171 offset:2048
	ds_read_b128 v[188:191], v171 offset:3072
	s_add_u32 s24, s22, 0xfffc0080
	s_addc_u32 s25, s23, -1
	s_cmp_eq_u32 s58, 12
	s_cselect_b32 s27, s15, s25
	s_cselect_b32 s26, s54, s24
	s_cselect_b32 s25, s13, s57
	s_cselect_b32 s24, s55, s56
	v_lshl_add_u64 v[164:165], s[22:23], 0, v[140:141]
	s_add_i32 m0, s21, 0xc000
	ds_read_b128 v[192:195], v172
	ds_read_b128 v[196:199], v172 offset:1024
	ds_read_b128 v[200:203], v172 offset:2048
	ds_read_b128 v[204:207], v172 offset:3072
	ds_read_b128 v[208:211], v172 offset:4096
	ds_read_b128 v[212:215], v172 offset:5120
	ds_read_b128 v[216:219], v172 offset:6144
	ds_read_b128 v[220:223], v172 offset:7168
	global_load_lds_dwordx4 v[164:165], off
	v_lshl_add_u64 v[164:165], s[22:23], 0, v[142:143]
	s_add_i32 m0, s21, 0xe000
	s_nop 0
	global_load_lds_dwordx4 v[164:165], off
	s_waitcnt vmcnt(8)
	s_waitcnt lgkmcnt(0)
	s_barrier
	s_setprio 1
	s_waitcnt lgkmcnt(0)
	v_mfma_f32_16x16x32_bf16 v[126:129], v[148:151], v[192:195], 0
	v_mfma_f32_16x16x32_bf16 v[122:125], v[156:159], v[192:195], 0
	v_mfma_f32_16x16x32_bf16 v[114:117], v[148:151], v[200:203], 0
	v_mfma_f32_16x16x32_bf16 v[106:109], v[156:159], v[200:203], 0
	v_mfma_f32_16x16x32_bf16 v[98:101], v[148:151], v[208:211], 0
	v_mfma_f32_16x16x32_bf16 v[90:93], v[156:159], v[208:211], 0
	v_mfma_f32_16x16x32_bf16 v[82:85], v[148:151], v[216:219], 0
	v_mfma_f32_16x16x32_bf16 v[74:77], v[156:159], v[216:219], 0
	v_mfma_f32_16x16x32_bf16 v[126:129], v[152:155], v[196:199], v[126:129]
	v_mfma_f32_16x16x32_bf16 v[122:125], v[160:163], v[196:199], v[122:125]
	v_mfma_f32_16x16x32_bf16 v[114:117], v[152:155], v[204:207], v[114:117]
	v_mfma_f32_16x16x32_bf16 v[106:109], v[160:163], v[204:207], v[106:109]
	v_mfma_f32_16x16x32_bf16 v[98:101], v[152:155], v[212:215], v[98:101]
	v_mfma_f32_16x16x32_bf16 v[90:93], v[160:163], v[212:215], v[90:93]
	v_mfma_f32_16x16x32_bf16 v[82:85], v[152:155], v[220:223], v[82:85]
	v_mfma_f32_16x16x32_bf16 v[74:77], v[160:163], v[220:223], v[74:77]
	s_setprio 0
	s_setprio 1
	v_mfma_f32_16x16x32_bf16 v[118:121], v[176:179], v[192:195], 0
	v_mfma_f32_16x16x32_bf16 v[110:113], v[184:187], v[192:195], 0
	v_mfma_f32_16x16x32_bf16 v[102:105], v[176:179], v[200:203], 0
	v_mfma_f32_16x16x32_bf16 v[94:97], v[184:187], v[200:203], 0
	v_mfma_f32_16x16x32_bf16 v[86:89], v[176:179], v[208:211], 0
	v_mfma_f32_16x16x32_bf16 v[78:81], v[184:187], v[208:211], 0
	v_mfma_f32_16x16x32_bf16 v[70:73], v[176:179], v[216:219], 0
	v_mfma_f32_16x16x32_bf16 v[66:69], v[184:187], v[216:219], 0
	v_mfma_f32_16x16x32_bf16 v[118:121], v[180:183], v[196:199], v[118:121]
	v_mfma_f32_16x16x32_bf16 v[110:113], v[188:191], v[196:199], v[110:113]
	v_mfma_f32_16x16x32_bf16 v[102:105], v[180:183], v[204:207], v[102:105]
	v_mfma_f32_16x16x32_bf16 v[94:97], v[188:191], v[204:207], v[94:97]
	v_mfma_f32_16x16x32_bf16 v[86:89], v[180:183], v[212:215], v[86:89]
	v_mfma_f32_16x16x32_bf16 v[78:81], v[188:191], v[212:215], v[78:81]
	v_mfma_f32_16x16x32_bf16 v[70:73], v[180:183], v[220:223], v[70:73]
	v_mfma_f32_16x16x32_bf16 v[66:69], v[188:191], v[220:223], v[66:69]
	s_setprio 0
	s_barrier
	s_add_i32 s59, s48, s28
	v_lshl_add_u64 v[164:165], s[24:25], 0, v[134:135]
	s_mov_b32 m0, s59
	ds_read_b128 v[192:195], v172 offset:16384
	ds_read_b128 v[196:199], v172 offset:17408
	ds_read_b128 v[200:203], v172 offset:18432
	ds_read_b128 v[204:207], v172 offset:19456
	ds_read_b128 v[208:211], v172 offset:20480
	ds_read_b128 v[212:215], v172 offset:21504
	ds_read_b128 v[216:219], v172 offset:22528
	ds_read_b128 v[220:223], v172 offset:23552
	global_load_lds_dwordx4 v[164:165], off
	s_add_i32 m0, s59, 0x2000
	s_add_u32 s60, s24, 0x40000
	v_lshl_add_u64 v[224:225], s[24:25], 0, v[130:131]
	s_addc_u32 s61, s25, 0
	s_add_i32 s59, s49, s28
	global_load_lds_dwordx4 v[224:225], off
	v_lshl_add_u64 v[226:227], s[60:61], 0, v[134:135]
	s_mov_b32 m0, s59
	v_lshl_add_u64 v[230:231], s[26:27], 0, v[132:133]
	global_load_lds_dwordx4 v[226:227], off
	v_lshl_add_u64 v[226:227], s[60:61], 0, v[130:131]
	s_add_i32 m0, s59, 0x2000
	s_nop 0
	global_load_lds_dwordx4 v[226:227], off
	v_lshl_add_u64 v[226:227], s[26:27], 0, v[136:137]
	s_mov_b32 m0, s21
	s_nop 0
	global_load_lds_dwordx4 v[226:227], off
	s_mov_b32 m0, s31
	s_nop 0
	global_load_lds_dwordx4 v[230:231], off
	s_waitcnt vmcnt(8)
	s_waitcnt lgkmcnt(0)
	s_barrier
; #define PG8_STAGE_A(b, h, ptr, NX) do { if constexpr (Sched::GATHER) { unsigned gs_[2]; gs_[0] = ((NX) && last_) ? gN[h][0] : gA[h][0]; gs_[1] = ((NX) && last_) ? gN[h][1] : gA[h][1]; PG8_STAGE(PG8_SA(b, h), ptr, gs_); } \
;         else PG8_STAGE(PG8_SA(b, h), (ptr) + ((h) ? hstep : (size_t)0), voffA); } while (0)
; #define PG8_STAGE(bufoff, gbase, voff) do { _Pragma("unroll") for (int _i = 0; _i < 2; ++_i) \
;         __builtin_amdgcn_global_load_lds((const unsigned*)((const char*)(gbase) + (voff)[_i]), (PG8_LAS unsigned*)(lds + (bufoff) + ldsw + _i * 8192), 16, 0, 0); } while (0)
; #define PG8_LDA(dst, b, h) do { _Pragma("unroll") for (int m = 0; m < 4; ++m) _Pragma("unroll") for (int k = 0; k < 2; ++k) dst[m][k] = *(const PG8_LAS bf16x8*)(lds + PG8_SA(b, h) + aoff + m * 2048 + k * 1024); } while (0)
; #define PG8_LDB(dst, b, h) do { _Pragma("unroll") for (int n = 0; n < 2; ++n) _Pragma("unroll") for (int k = 0; k < 2; ++k) dst[n][k] = *(const PG8_LAS bf16x8*)(lds + PG8_SB(b, h) + boff + n * 2048 + k * 1024); } while (0)
; #define PG8_MMA(ai, bj, At, Bt) do { __builtin_amdgcn_s_setprio(1); _Pragma("unroll") for (int m = 0; m < 4; ++m) _Pragma("unroll") for (int n = 0; n < 2; ++n) _Pragma("unroll") for (int k = 0; k < 2; ++k) \
;         acc[ai][bj][m][n] = __builtin_amdgcn_mfma_f32_16x16x32_bf16(Bt[n][k], At[m][k], acc[ai][bj][m][n], 0, 0, 0); __builtin_amdgcn_s_setprio(0); } while (0)
; #define PG8_WAIT_V(n) asm volatile("s_waitcnt vmcnt(" #n ")" ::: "memory")
; #define PG8_WAIT_L(n) asm volatile("s_waitcnt lgkmcnt(" #n ")" ::: "memory")
; #define PG8_BAR __builtin_amdgcn_s_barrier()
; #define PG8_SCHED __builtin_amdgcn_sched_barrier(0)
; template <class Epi, class Sched, bool ALIGN_EPI = false, bool SP2 = false>
; __device__ __forceinline__ void gemm_phase(PG8_LAS unsigned char* lds, const Gemm g, const Sched& S, const Epi& E, const bool skip_epi = false) {
;     ...
;             PG8_WAIT_V(8); PG8_WAIT_L(0); PG8_BAR; PG8_MMA(1, 0, At, B0); PG8_MMA(1, 1, At, B1); PG8_BAR; PG8_SCHED;
;             PG8_LDB(B0, 1, 0); PG8_LDB(B1, 1, 1); PG8_SCHED; PG8_LDA(At, 1, 0); PG8_STAGE_A(0, 1, a2, true);
;             PG8_WAIT_V(8); PG8_WAIT_L(0); PG8_BAR; PG8_MMA(0, 0, At, B0); PG8_MMA(0, 1, At, B1); PG8_BAR; PG8_SCHED;
;             PG8_LDA(At, 1, 1); PG8_STAGE(PG8_SB(1, 0), b3, voffB); PG8_STAGE(PG8_SB(1, 1), b3 + hstep, voffB); PG8_STAGE_A(1, 0, a3, true);
	s_setprio 1
	s_waitcnt lgkmcnt(0)
	v_mfma_f32_16x16x32_bf16 v[62:65], v[148:151], v[192:195], 0
	v_mfma_f32_16x16x32_bf16 v[58:61], v[156:159], v[192:195], 0
	v_mfma_f32_16x16x32_bf16 v[50:53], v[148:151], v[200:203], 0
	v_mfma_f32_16x16x32_bf16 v[42:45], v[156:159], v[200:203], 0
	v_mfma_f32_16x16x32_bf16 v[34:37], v[148:151], v[208:211], 0
	v_mfma_f32_16x16x32_bf16 v[26:29], v[156:159], v[208:211], 0
	v_mfma_f32_16x16x32_bf16 v[18:21], v[148:151], v[216:219], 0
	v_mfma_f32_16x16x32_bf16 v[10:13], v[156:159], v[216:219], 0
	v_mfma_f32_16x16x32_bf16 v[62:65], v[152:155], v[196:199], v[62:65]
	v_mfma_f32_16x16x32_bf16 v[58:61], v[160:163], v[196:199], v[58:61]
	v_mfma_f32_16x16x32_bf16 v[50:53], v[152:155], v[204:207], v[50:53]
	v_mfma_f32_16x16x32_bf16 v[42:45], v[160:163], v[204:207], v[42:45]
	v_mfma_f32_16x16x32_bf16 v[34:37], v[152:155], v[212:215], v[34:37]
	v_mfma_f32_16x16x32_bf16 v[26:29], v[160:163], v[212:215], v[26:29]
	v_mfma_f32_16x16x32_bf16 v[18:21], v[152:155], v[220:223], v[18:21]
	v_mfma_f32_16x16x32_bf16 v[10:13], v[160:163], v[220:223], v[10:13]
	s_setprio 0
	s_setprio 1
	v_mfma_f32_16x16x32_bf16 v[54:57], v[176:179], v[192:195], 0
	v_mfma_f32_16x16x32_bf16 v[46:49], v[184:187], v[192:195], 0
	v_mfma_f32_16x16x32_bf16 v[38:41], v[176:179], v[200:203], 0
	v_mfma_f32_16x16x32_bf16 v[30:33], v[184:187], v[200:203], 0
	v_mfma_f32_16x16x32_bf16 v[22:25], v[176:179], v[208:211], 0
	v_mfma_f32_16x16x32_bf16 v[14:17], v[184:187], v[208:211], 0
	v_mfma_f32_16x16x32_bf16 v[6:9], v[176:179], v[216:219], 0
	v_mfma_f32_16x16x32_bf16 v[2:5], v[184:187], v[216:219], 0
	v_mfma_f32_16x16x32_bf16 v[54:57], v[180:183], v[196:199], v[54:57]
	v_mfma_f32_16x16x32_bf16 v[46:49], v[188:191], v[196:199], v[46:49]
	v_mfma_f32_16x16x32_bf16 v[38:41], v[180:183], v[204:207], v[38:41]
	v_mfma_f32_16x16x32_bf16 v[30:33], v[188:191], v[204:207], v[30:33]
	v_mfma_f32_16x16x32_bf16 v[22:25], v[180:183], v[212:215], v[22:25]
	v_mfma_f32_16x16x32_bf16 v[14:17], v[188:191], v[212:215], v[14:17]
	v_mfma_f32_16x16x32_bf16 v[6:9], v[180:183], v[220:223], v[6:9]
	v_mfma_f32_16x16x32_bf16 v[2:5], v[188:191], v[220:223], v[2:5]
	s_setprio 0
	s_barrier
	s_add_i32 s59, 0, 0x18000
	s_add_i32 s60, 0, 0x1c000
	v_add_u32_e32 v160, s59, v1
	v_add_u32_e32 v188, s60, v1
	ds_read_b128 v[148:151], v160
	ds_read_b128 v[152:155], v160 offset:1024
	ds_read_b128 v[156:159], v160 offset:2048
	ds_read_b128 v[160:163], v160 offset:3072
	ds_read_b128 v[176:179], v188
	ds_read_b128 v[180:183], v188 offset:1024
	ds_read_b128 v[184:187], v188 offset:2048
	ds_read_b128 v[188:191], v188 offset:3072
	s_add_u32 s26, s26, 0x40000
	s_addc_u32 s27, s27, 0
	s_mov_b32 m0, s34
	v_lshl_add_u64 v[232:233], s[26:27], 0, v[136:137]
	ds_read_b128 v[192:195], v172 offset:32768
	ds_read_b128 v[196:199], v172 offset:33792
	ds_read_b128 v[200:203], v172 offset:34816
	ds_read_b128 v[204:207], v172 offset:35840
	ds_read_b128 v[208:211], v172 offset:36864
	ds_read_b128 v[212:215], v172 offset:37888
	ds_read_b128 v[216:219], v172 offset:38912
	ds_read_b128 v[220:223], v172 offset:39936
	global_load_lds_dwordx4 v[232:233], off
	v_lshl_add_u64 v[232:233], s[26:27], 0, v[132:133]
	s_mov_b32 m0, s35
	s_nop 0
	global_load_lds_dwordx4 v[232:233], off
	s_waitcnt vmcnt(8)
	s_waitcnt lgkmcnt(0)
	s_barrier
	s_setprio 1
	s_waitcnt lgkmcnt(0)
	v_mfma_f32_16x16x32_bf16 v[126:129], v[148:151], v[192:195], v[126:129]
	v_mfma_f32_16x16x32_bf16 v[122:125], v[156:159], v[192:195], v[122:125]
	v_mfma_f32_16x16x32_bf16 v[114:117], v[148:151], v[200:203], v[114:117]
	v_mfma_f32_16x16x32_bf16 v[106:109], v[156:159], v[200:203], v[106:109]
	v_mfma_f32_16x16x32_bf16 v[98:101], v[148:151], v[208:211], v[98:101]
	v_mfma_f32_16x16x32_bf16 v[90:93], v[156:159], v[208:211], v[90:93]
	v_mfma_f32_16x16x32_bf16 v[82:85], v[148:151], v[216:219], v[82:85]
	v_mfma_f32_16x16x32_bf16 v[74:77], v[156:159], v[216:219], v[74:77]
	v_mfma_f32_16x16x32_bf16 v[126:129], v[152:155], v[196:199], v[126:129]
	v_mfma_f32_16x16x32_bf16 v[122:125], v[160:163], v[196:199], v[122:125]
	v_mfma_f32_16x16x32_bf16 v[114:117], v[152:155], v[204:207], v[114:117]
	v_mfma_f32_16x16x32_bf16 v[106:109], v[160:163], v[204:207], v[106:109]
	v_mfma_f32_16x16x32_bf16 v[98:101], v[152:155], v[212:215], v[98:101]
	v_mfma_f32_16x16x32_bf16 v[90:93], v[160:163], v[212:215], v[90:93]
	v_mfma_f32_16x16x32_bf16 v[82:85], v[152:155], v[220:223], v[82:85]
	v_mfma_f32_16x16x32_bf16 v[74:77], v[160:163], v[220:223], v[74:77]
	s_setprio 0
	s_setprio 1
	v_mfma_f32_16x16x32_bf16 v[118:121], v[176:179], v[192:195], v[118:121]
	v_mfma_f32_16x16x32_bf16 v[110:113], v[184:187], v[192:195], v[110:113]
	v_mfma_f32_16x16x32_bf16 v[102:105], v[176:179], v[200:203], v[102:105]
	v_mfma_f32_16x16x32_bf16 v[94:97], v[184:187], v[200:203], v[94:97]
	v_mfma_f32_16x16x32_bf16 v[86:89], v[176:179], v[208:211], v[86:89]
	v_mfma_f32_16x16x32_bf16 v[78:81], v[184:187], v[208:211], v[78:81]
	v_mfma_f32_16x16x32_bf16 v[70:73], v[176:179], v[216:219], v[70:73]
	v_mfma_f32_16x16x32_bf16 v[66:69], v[184:187], v[216:219], v[66:69]
	v_mfma_f32_16x16x32_bf16 v[118:121], v[180:183], v[196:199], v[118:121]
	v_mfma_f32_16x16x32_bf16 v[110:113], v[188:191], v[196:199], v[110:113]
	v_mfma_f32_16x16x32_bf16 v[102:105], v[180:183], v[204:207], v[102:105]
	v_mfma_f32_16x16x32_bf16 v[94:97], v[188:191], v[204:207], v[94:97]
	v_mfma_f32_16x16x32_bf16 v[86:89], v[180:183], v[212:215], v[86:89]
	v_mfma_f32_16x16x32_bf16 v[78:81], v[188:191], v[212:215], v[78:81]
	v_mfma_f32_16x16x32_bf16 v[70:73], v[180:183], v[220:223], v[70:73]
	v_mfma_f32_16x16x32_bf16 v[66:69], v[188:191], v[220:223], v[66:69]
	s_setprio 0
	s_barrier
; #define PG8_STAGE_A(b, h, ptr, NX) do { if constexpr (Sched::GATHER) { unsigned gs_[2]; gs_[0] = ((NX) && last_) ? gN[h][0] : gA[h][0]; gs_[1] = ((NX) && last_) ? gN[h][1] : gA[h][1]; PG8_STAGE(PG8_SA(b, h), ptr, gs_); } \
;         else PG8_STAGE(PG8_SA(b, h), (ptr) + ((h) ? hstep : (size_t)0), voffA); } while (0)
; #define PG8_STAGE(bufoff, gbase, voff) do { _Pragma("unroll") for (int _i = 0; _i < 2; ++_i) \
;         __builtin_amdgcn_global_load_lds((const unsigned*)((const char*)(gbase) + (voff)[_i]), (PG8_LAS unsigned*)(lds + (bufoff) + ldsw + _i * 8192), 16, 0, 0); } while (0)
; #define PG8_LDA(dst, b, h) do { _Pragma("unroll") for (int m = 0; m < 4; ++m) _Pragma("unroll") for (int k = 0; k < 2; ++k) dst[m][k] = *(const PG8_LAS bf16x8*)(lds + PG8_SA(b, h) + aoff + m * 2048 + k * 1024); } while (0)
; #define PG8_MMA(ai, bj, At, Bt) do { __builtin_amdgcn_s_setprio(1); _Pragma("unroll") for (int m = 0; m < 4; ++m) _Pragma("unroll") for (int n = 0; n < 2; ++n) _Pragma("unroll") for (int k = 0; k < 2; ++k) \
;         acc[ai][bj][m][n] = __builtin_amdgcn_mfma_f32_16x16x32_bf16(Bt[n][k], At[m][k], acc[ai][bj][m][n], 0, 0, 0); __builtin_amdgcn_s_setprio(0); } while (0)
; #define PG8_WAIT_V(n) asm volatile("s_waitcnt vmcnt(" #n ")" ::: "memory")
; #define PG8_WAIT_L(n) asm volatile("s_waitcnt lgkmcnt(" #n ")" ::: "memory")
; #define PG8_BAR __builtin_amdgcn_s_barrier()
; #define PG8_SCHED __builtin_amdgcn_sched_barrier(0)
; template <class Epi, class Sched, bool ALIGN_EPI = false, bool SP2 = false>
; __device__ __forceinline__ void gemm_phase(PG8_LAS unsigned char* lds, const Gemm g, const Sched& S, const Epi& E, const bool skip_epi = false) {
;     ...
;         for (int t = 0; t < nt; t += 2) {
;     ...
;             PG8_LDA(At, 1, 1); PG8_STAGE(PG8_SB(1, 0), b3, voffB); PG8_STAGE(PG8_SB(1, 1), b3 + hstep, voffB); PG8_STAGE_A(1, 0, a3, true);
;             PG8_WAIT_V(8); PG8_WAIT_L(0); PG8_BAR; PG8_MMA(1, 0, At, B0); PG8_MMA(1, 1, At, B1); PG8_BAR; PG8_SCHED;
	s_add_i32 s26, s59, s28
	v_lshl_add_u64 v[164:165], v[164:165], 0, s[8:9]
	s_mov_b32 m0, s26
	ds_read_b128 v[192:195], v172 offset:49152
	ds_read_b128 v[196:199], v172 offset:50176
	ds_read_b128 v[200:203], v172 offset:51200
	ds_read_b128 v[204:207], v172 offset:52224
	ds_read_b128 v[208:211], v172 offset:53248
	ds_read_b128 v[212:215], v172 offset:54272
	ds_read_b128 v[216:219], v172 offset:55296
	ds_read_b128 v[220:223], v172 offset:56320
	global_load_lds_dwordx4 v[164:165], off
	s_add_i32 m0, s26, 0x2000
	s_add_u32 s24, s24, 0x40080
	v_lshl_add_u64 v[164:165], v[224:225], 0, s[8:9]
	s_addc_u32 s25, s25, 0
	s_add_i32 s26, s60, s28
	global_load_lds_dwordx4 v[164:165], off
	v_lshl_add_u64 v[164:165], s[24:25], 0, v[134:135]
	s_mov_b32 m0, s26
	s_nop 0
	global_load_lds_dwordx4 v[164:165], off
	v_lshl_add_u64 v[164:165], s[24:25], 0, v[130:131]
	s_add_i32 m0, s26, 0x2000
	s_nop 0
	global_load_lds_dwordx4 v[164:165], off
	v_lshl_add_u64 v[164:165], v[226:227], 0, s[8:9]
	s_mov_b32 m0, s37
	s_nop 0
	global_load_lds_dwordx4 v[164:165], off
	v_lshl_add_u64 v[164:165], v[230:231], 0, s[8:9]
	s_mov_b32 m0, s38
	s_nop 0
	global_load_lds_dwordx4 v[164:165], off
	s_waitcnt vmcnt(8)
	s_waitcnt lgkmcnt(0)
	s_barrier
	s_setprio 1
	s_waitcnt lgkmcnt(0)
	v_mfma_f32_16x16x32_bf16 v[62:65], v[148:151], v[192:195], v[62:65]
	v_mfma_f32_16x16x32_bf16 v[58:61], v[156:159], v[192:195], v[58:61]
	v_mfma_f32_16x16x32_bf16 v[50:53], v[148:151], v[200:203], v[50:53]
	v_mfma_f32_16x16x32_bf16 v[42:45], v[156:159], v[200:203], v[42:45]
	v_mfma_f32_16x16x32_bf16 v[34:37], v[148:151], v[208:211], v[34:37]
	v_mfma_f32_16x16x32_bf16 v[26:29], v[156:159], v[208:211], v[26:29]
	v_mfma_f32_16x16x32_bf16 v[18:21], v[148:151], v[216:219], v[18:21]
	v_mfma_f32_16x16x32_bf16 v[10:13], v[156:159], v[216:219], v[10:13]
	v_mfma_f32_16x16x32_bf16 v[62:65], v[152:155], v[196:199], v[62:65]
	v_mfma_f32_16x16x32_bf16 v[58:61], v[160:163], v[196:199], v[58:61]
	v_mfma_f32_16x16x32_bf16 v[50:53], v[152:155], v[204:207], v[50:53]
	v_mfma_f32_16x16x32_bf16 v[42:45], v[160:163], v[204:207], v[42:45]
	v_mfma_f32_16x16x32_bf16 v[34:37], v[152:155], v[212:215], v[34:37]
	v_mfma_f32_16x16x32_bf16 v[26:29], v[160:163], v[212:215], v[26:29]
	v_mfma_f32_16x16x32_bf16 v[18:21], v[152:155], v[220:223], v[18:21]
	v_mfma_f32_16x16x32_bf16 v[10:13], v[160:163], v[220:223], v[10:13]
	s_setprio 0
	s_setprio 1
	v_mfma_f32_16x16x32_bf16 v[54:57], v[176:179], v[192:195], v[54:57]
	v_mfma_f32_16x16x32_bf16 v[46:49], v[184:187], v[192:195], v[46:49]
	v_mfma_f32_16x16x32_bf16 v[38:41], v[176:179], v[200:203], v[38:41]
	v_mfma_f32_16x16x32_bf16 v[30:33], v[184:187], v[200:203], v[30:33]
	v_mfma_f32_16x16x32_bf16 v[22:25], v[176:179], v[208:211], v[22:25]
	v_mfma_f32_16x16x32_bf16 v[14:17], v[184:187], v[208:211], v[14:17]
	v_mfma_f32_16x16x32_bf16 v[6:9], v[176:179], v[216:219], v[6:9]
	v_mfma_f32_16x16x32_bf16 v[2:5], v[184:187], v[216:219], v[2:5]
	v_mfma_f32_16x16x32_bf16 v[54:57], v[180:183], v[196:199], v[54:57]
	v_mfma_f32_16x16x32_bf16 v[46:49], v[188:191], v[196:199], v[46:49]
	v_mfma_f32_16x16x32_bf16 v[38:41], v[180:183], v[204:207], v[38:41]
	v_mfma_f32_16x16x32_bf16 v[30:33], v[188:191], v[204:207], v[30:33]
	v_mfma_f32_16x16x32_bf16 v[22:25], v[180:183], v[212:215], v[22:25]
	v_mfma_f32_16x16x32_bf16 v[14:17], v[188:191], v[212:215], v[14:17]
	v_mfma_f32_16x16x32_bf16 v[6:9], v[180:183], v[220:223], v[6:9]
	v_mfma_f32_16x16x32_bf16 v[2:5], v[188:191], v[220:223], v[2:5]
	s_setprio 0
	s_barrier
	s_add_i32 s58, s58, 2
	s_add_u32 s22, s22, 0x100
	s_addc_u32 s23, s23, 0
	s_add_u32 s56, s56, 0x100
	s_addc_u32 s57, s57, 0
	s_cmp_gt_u32 s58, 13

; template <class Epi, class Sched, bool ALIGN_EPI = false, bool SP2 = false>
; __device__ __forceinline__ void gemm_phase(PG8_LAS unsigned char* lds, const Gemm g, const Sched& S, const Epi& E, const bool skip_epi = false) {
;     ...
;     for (;;) {
;         const bool has_next = S.next(ui + 1, nxt);
;         if (has_next) PG8_GIDX(gN, nxt.pm);
;         const char* nA = has_next ? (const char*)g.A + (size_t)nxt.pm * pmstepA + nxt.ko : cA; const char* nB = has_next ? (const char*)g.Bt + (size_t)nxt.pn * tstep + nxt.ko : cB;
;         for (int t = 0; t < nt; t += 2) {
;             const bool last = (t == nt - 2); last_ = last && has_next;
;             const char* a1 = cA + (size_t)(t + 1) * kstep;
;             const char* a2 = last ? nA : cA + (size_t)(t + 2) * kstep; const char* b2 = last ? nB : cB + (size_t)(t + 2) * kstep;
;             const char* a3 = a2 + kstep; const char* b3 = b2 + kstep;
;             if (last && has_next) S.a_ready(nxt);
;             if constexpr (SP2) {
;             PG8_LDB(B0, 0, 0); PG8_LDB(B1, 0, 1); PG8_SCHED; PG8_LDA(At, 0, 0); PG8_STAGE_A(1, 1, a1, false);
;             PG8_WAIT_V(8); PG8_WAIT_L(0); PG8_BAR; PG8_MMA(0, 0, At, B0); PG8_MMA(0, 1, At, B1); PG8_BAR; PG8_SCHED;
;             PG8_LDA(At, 0, 1); PG8_STAGE(PG8_SB(0, 0), b2, voffB); PG8_STAGE(PG8_SB(0, 1), b2 + hstep, voffB); PG8_STAGE_A(0, 0, a2, true);
;             PG8_WAIT_V(8); PG8_WAIT_L(0); PG8_BAR; PG8_MMA(1, 0, At, B0); PG8_MMA(1, 1, At, B1); PG8_BAR; PG8_SCHED;
;             PG8_LDB(B0, 1, 0); PG8_LDB(B1, 1, 1); PG8_SCHED; PG8_LDA(At, 1, 0); PG8_STAGE_A(0, 1, a2, true);
;             PG8_WAIT_V(8); PG8_WAIT_L(0); PG8_BAR; PG8_MMA(0, 0, At, B0); PG8_MMA(0, 1, At, B1); PG8_BAR; PG8_SCHED;
;             PG8_LDA(At, 1, 1); PG8_STAGE(PG8_SB(1, 0), b3, voffB); PG8_STAGE(PG8_SB(1, 1), b3 + hstep, voffB); PG8_STAGE_A(1, 0, a3, true);
;             PG8_WAIT_V(8); PG8_WAIT_L(0); PG8_BAR; PG8_MMA(1, 0, At, B0); PG8_MMA(1, 1, At, B1); PG8_BAR; PG8_SCHED;
; template <int layer> __device__ __forceinline__ void layer_phases(const Ctx& c, unsigned char* lds) {
;     ...
;             pg8::Gemm g{MIX, (const bf16*)(ws + WS_WOUT) + (size_t)layer * D * D, M, D, D, D}; pg8::StaticOrder S; S.init(M, D, G, bx);
;             { pg8::EpiRes<false> E{XB, XBD, SSD}; pg8::gemm_phase<pg8::EpiRes<false>, pg8::StaticOrder, true, true>(ldsl, g, S, E, noepi); }
.LBB0_1323:
	s_ashr_i32 s25, s24, 31
	s_lshl_b64 s[26:27], s[24:25], 19
	s_add_u32 s26, s46, s26
	s_addc_u32 s27, s47, s27
	s_and_b64 s[28:29], s[6:7], exec
	s_cselect_b32 s25, s27, s35
	s_cselect_b32 s31, s26, s34
	s_ashr_i32 s23, s22, 31
	s_lshl_b64 s[28:29], s[22:23], 19
	s_add_u32 s28, s2, s28
	s_addc_u32 s29, s3, s29
	s_and_b64 s[38:39], s[6:7], exec
	s_cselect_b32 s23, s29, s37
	s_cselect_b32 s60, s28, s36
	s_add_u32 s34, s34, 0x40080
	s_addc_u32 s35, s35, 0
	s_add_u32 s61, s36, 0x100
	s_addc_u32 s62, s37, 0
	s_mov_b32 s63, -2
	s_waitcnt vmcnt(0)
	s_waitcnt lgkmcnt(0)
	ds_read_b128 v[98:101], v225
	ds_read_b128 v[110:113], v225 offset:1024
	ds_read_b128 v[122:125], v225 offset:2048
	ds_read_b128 v[130:133], v225 offset:3072
	ds_read_b128 v[146:149], v226
	ds_read_b128 v[150:153], v226 offset:1024
	ds_read_b128 v[154:157], v226 offset:2048
	ds_read_b128 v[158:161], v226 offset:3072
	s_add_u32 s36, s34, 0xfffc0080
	s_addc_u32 s37, s35, -1
	s_cmp_eq_u32 s63, 12
	s_cselect_b32 s39, s25, s37
	s_cselect_b32 s38, s31, s36
	s_cselect_b32 s37, s23, s62
	s_cselect_b32 s36, s60, s61
	v_lshl_add_u64 v[210:211], s[34:35], 0, v[194:195]
	s_add_i32 m0, s41, 0xc000
	ds_read_b128 v[162:165], v227
	ds_read_b128 v[166:169], v227 offset:1024
	ds_read_b128 v[170:173], v227 offset:2048
	ds_read_b128 v[174:177], v227 offset:3072
	ds_read_b128 v[178:181], v227 offset:4096
	ds_read_b128 v[182:185], v227 offset:5120
	ds_read_b128 v[202:205], v227 offset:6144
	ds_read_b128 v[206:209], v227 offset:7168
	global_load_lds_dwordx4 v[210:211], off
	v_lshl_add_u64 v[210:211], s[34:35], 0, v[196:197]
	s_add_i32 m0, s41, 0xe000
	s_nop 0
	global_load_lds_dwordx4 v[210:211], off
	s_waitcnt vmcnt(8)
	s_waitcnt lgkmcnt(0)
	s_barrier
	s_setprio 1
	s_waitcnt lgkmcnt(0)
	v_mfma_f32_16x16x32_bf16 v[142:145], v[98:101], v[162:165], 0
	v_mfma_f32_16x16x32_bf16 v[138:141], v[122:125], v[162:165], 0
	v_mfma_f32_16x16x32_bf16 v[118:121], v[98:101], v[170:173], 0
	v_mfma_f32_16x16x32_bf16 v[114:117], v[122:125], v[170:173], 0
	v_mfma_f32_16x16x32_bf16 v[94:97], v[98:101], v[178:181], 0
	v_mfma_f32_16x16x32_bf16 v[90:93], v[122:125], v[178:181], 0
	v_mfma_f32_16x16x32_bf16 v[78:81], v[98:101], v[202:205], 0
	v_mfma_f32_16x16x32_bf16 v[74:77], v[122:125], v[202:205], 0
	v_mfma_f32_16x16x32_bf16 v[142:145], v[110:113], v[166:169], v[142:145]
	v_mfma_f32_16x16x32_bf16 v[138:141], v[130:133], v[166:169], v[138:141]
	v_mfma_f32_16x16x32_bf16 v[118:121], v[110:113], v[174:177], v[118:121]
	v_mfma_f32_16x16x32_bf16 v[114:117], v[130:133], v[174:177], v[114:117]
	v_mfma_f32_16x16x32_bf16 v[94:97], v[110:113], v[182:185], v[94:97]
	v_mfma_f32_16x16x32_bf16 v[90:93], v[130:133], v[182:185], v[90:93]
	v_mfma_f32_16x16x32_bf16 v[78:81], v[110:113], v[206:209], v[78:81]
	v_mfma_f32_16x16x32_bf16 v[74:77], v[130:133], v[206:209], v[74:77]
	s_setprio 0
	s_setprio 1
	v_mfma_f32_16x16x32_bf16 v[134:137], v[146:149], v[162:165], 0
	v_mfma_f32_16x16x32_bf16 v[126:129], v[154:157], v[162:165], 0
	v_mfma_f32_16x16x32_bf16 v[106:109], v[146:149], v[170:173], 0
	v_mfma_f32_16x16x32_bf16 v[102:105], v[154:157], v[170:173], 0
	v_mfma_f32_16x16x32_bf16 v[86:89], v[146:149], v[178:181], 0
	v_mfma_f32_16x16x32_bf16 v[82:85], v[154:157], v[178:181], 0
	v_mfma_f32_16x16x32_bf16 v[70:73], v[146:149], v[202:205], 0
	v_mfma_f32_16x16x32_bf16 v[66:69], v[154:157], v[202:205], 0
	v_mfma_f32_16x16x32_bf16 v[134:137], v[150:153], v[166:169], v[134:137]
	v_mfma_f32_16x16x32_bf16 v[126:129], v[158:161], v[166:169], v[126:129]
	v_mfma_f32_16x16x32_bf16 v[106:109], v[150:153], v[174:177], v[106:109]
	v_mfma_f32_16x16x32_bf16 v[102:105], v[158:161], v[174:177], v[102:105]
	v_mfma_f32_16x16x32_bf16 v[86:89], v[150:153], v[182:185], v[86:89]
	v_mfma_f32_16x16x32_bf16 v[82:85], v[158:161], v[182:185], v[82:85]
	v_mfma_f32_16x16x32_bf16 v[70:73], v[150:153], v[206:209], v[70:73]
	v_mfma_f32_16x16x32_bf16 v[66:69], v[158:161], v[206:209], v[66:69]
	s_setprio 0
	s_barrier
	s_add_i32 s64, s57, s40
	v_lshl_add_u64 v[210:211], s[36:37], 0, v[188:189]
	s_mov_b32 m0, s64
	ds_read_b128 v[162:165], v227 offset:16384
	ds_read_b128 v[166:169], v227 offset:17408
	ds_read_b128 v[170:173], v227 offset:18432
	ds_read_b128 v[174:177], v227 offset:19456
	ds_read_b128 v[178:181], v227 offset:20480
	ds_read_b128 v[182:185], v227 offset:21504
	ds_read_b128 v[202:205], v227 offset:22528
	ds_read_b128 v[206:209], v227 offset:23552
	global_load_lds_dwordx4 v[210:211], off
	s_add_i32 m0, s64, 0x2000
	s_add_u32 s64, s36, 0x40000
	v_lshl_add_u64 v[212:213], s[36:37], 0, v[192:193]
	s_addc_u32 s65, s37, 0
	s_add_i32 s66, s58, s40
	global_load_lds_dwordx4 v[212:213], off
	v_lshl_add_u64 v[214:215], s[64:65], 0, v[188:189]
	s_mov_b32 m0, s66
	v_lshl_add_u64 v[216:217], s[38:39], 0, v[190:191]
	global_load_lds_dwordx4 v[214:215], off
	v_lshl_add_u64 v[214:215], s[64:65], 0, v[192:193]
	s_add_i32 m0, s66, 0x2000
	s_nop 0
	global_load_lds_dwordx4 v[214:215], off
	v_lshl_add_u64 v[214:215], s[38:39], 0, v[186:187]
	s_mov_b32 m0, s41
	s_nop 0
	global_load_lds_dwordx4 v[214:215], off
	s_mov_b32 m0, s44
	s_nop 0
	global_load_lds_dwordx4 v[216:217], off
	s_waitcnt vmcnt(8)
	s_waitcnt lgkmcnt(0)
	s_barrier
; #define PG8_STAGE_A(b, h, ptr, NX) do { if constexpr (Sched::GATHER) { unsigned gs_[2]; gs_[0] = ((NX) && last_) ? gN[h][0] : gA[h][0]; gs_[1] = ((NX) && last_) ? gN[h][1] : gA[h][1]; PG8_STAGE(PG8_SA(b, h), ptr, gs_); } \
;         else PG8_STAGE(PG8_SA(b, h), (ptr) + ((h) ? hstep : (size_t)0), voffA); } while (0)
; #define PG8_LDA(dst, b, h) do { _Pragma("unroll") for (int m = 0; m < 4; ++m) _Pragma("unroll") for (int k = 0; k < 2; ++k) dst[m][k] = *(const PG8_LAS bf16x8*)(lds + PG8_SA(b, h) + aoff + m * 2048 + k * 1024); } while (0)
; #define PG8_LDB(dst, b, h) do { _Pragma("unroll") for (int n = 0; n < 2; ++n) _Pragma("unroll") for (int k = 0; k < 2; ++k) dst[n][k] = *(const PG8_LAS bf16x8*)(lds + PG8_SB(b, h) + boff + n * 2048 + k * 1024); } while (0)
; #define PG8_MMA(ai, bj, At, Bt) do { __builtin_amdgcn_s_setprio(1); _Pragma("unroll") for (int m = 0; m < 4; ++m) _Pragma("unroll") for (int n = 0; n < 2; ++n) _Pragma("unroll") for (int k = 0; k < 2; ++k) \
;         acc[ai][bj][m][n] = __builtin_amdgcn_mfma_f32_16x16x32_bf16(Bt[n][k], At[m][k], acc[ai][bj][m][n], 0, 0, 0); __builtin_amdgcn_s_setprio(0); } while (0)
; #define PG8_WAIT_V(n) asm volatile("s_waitcnt vmcnt(" #n ")" ::: "memory")
; #define PG8_WAIT_L(n) asm volatile("s_waitcnt lgkmcnt(" #n ")" ::: "memory")
; #define PG8_BAR __builtin_amdgcn_s_barrier()
; #define PG8_SCHED __builtin_amdgcn_sched_barrier(0)
; template <class Epi, class Sched, bool ALIGN_EPI = false, bool SP2 = false>
; __device__ __forceinline__ void gemm_phase(PG8_LAS unsigned char* lds, const Gemm g, const Sched& S, const Epi& E, const bool skip_epi = false) {
;     ...
;             PG8_WAIT_V(8); PG8_WAIT_L(0); PG8_BAR; PG8_MMA(1, 0, At, B0); PG8_MMA(1, 1, At, B1); PG8_BAR; PG8_SCHED;
;             PG8_LDB(B0, 1, 0); PG8_LDB(B1, 1, 1); PG8_SCHED; PG8_LDA(At, 1, 0); PG8_STAGE_A(0, 1, a2, true);
;             PG8_WAIT_V(8); PG8_WAIT_L(0); PG8_BAR; PG8_MMA(0, 0, At, B0); PG8_MMA(0, 1, At, B1); PG8_BAR; PG8_SCHED;
	s_setprio 1
	s_waitcnt lgkmcnt(0)
	v_mfma_f32_16x16x32_bf16 v[62:65], v[98:101], v[162:165], 0
	v_mfma_f32_16x16x32_bf16 v[58:61], v[122:125], v[162:165], 0
	v_mfma_f32_16x16x32_bf16 v[46:49], v[98:101], v[170:173], 0
	v_mfma_f32_16x16x32_bf16 v[42:45], v[122:125], v[170:173], 0
	v_mfma_f32_16x16x32_bf16 v[30:33], v[98:101], v[178:181], 0
	v_mfma_f32_16x16x32_bf16 v[26:29], v[122:125], v[178:181], 0
	v_mfma_f32_16x16x32_bf16 v[14:17], v[98:101], v[202:205], 0
	v_mfma_f32_16x16x32_bf16 v[10:13], v[122:125], v[202:205], 0
	v_mfma_f32_16x16x32_bf16 v[62:65], v[110:113], v[166:169], v[62:65]
	v_mfma_f32_16x16x32_bf16 v[58:61], v[130:133], v[166:169], v[58:61]
	v_mfma_f32_16x16x32_bf16 v[46:49], v[110:113], v[174:177], v[46:49]
	v_mfma_f32_16x16x32_bf16 v[42:45], v[130:133], v[174:177], v[42:45]
	v_mfma_f32_16x16x32_bf16 v[30:33], v[110:113], v[182:185], v[30:33]
	v_mfma_f32_16x16x32_bf16 v[26:29], v[130:133], v[182:185], v[26:29]
	v_mfma_f32_16x16x32_bf16 v[14:17], v[110:113], v[206:209], v[14:17]
	v_mfma_f32_16x16x32_bf16 v[10:13], v[130:133], v[206:209], v[10:13]
	s_setprio 0
	s_setprio 1
	v_mfma_f32_16x16x32_bf16 v[54:57], v[146:149], v[162:165], 0
	v_mfma_f32_16x16x32_bf16 v[50:53], v[154:157], v[162:165], 0
	v_mfma_f32_16x16x32_bf16 v[38:41], v[146:149], v[170:173], 0
	v_mfma_f32_16x16x32_bf16 v[34:37], v[154:157], v[170:173], 0
	v_mfma_f32_16x16x32_bf16 v[22:25], v[146:149], v[178:181], 0
	v_mfma_f32_16x16x32_bf16 v[18:21], v[154:157], v[178:181], 0
	v_mfma_f32_16x16x32_bf16 v[6:9], v[146:149], v[202:205], 0
	v_mfma_f32_16x16x32_bf16 v[2:5], v[154:157], v[202:205], 0
	v_mfma_f32_16x16x32_bf16 v[54:57], v[150:153], v[166:169], v[54:57]
	v_mfma_f32_16x16x32_bf16 v[50:53], v[158:161], v[166:169], v[50:53]
	v_mfma_f32_16x16x32_bf16 v[38:41], v[150:153], v[174:177], v[38:41]
	v_mfma_f32_16x16x32_bf16 v[34:37], v[158:161], v[174:177], v[34:37]
	v_mfma_f32_16x16x32_bf16 v[22:25], v[150:153], v[182:185], v[22:25]
	v_mfma_f32_16x16x32_bf16 v[18:21], v[158:161], v[182:185], v[18:21]
	v_mfma_f32_16x16x32_bf16 v[6:9], v[150:153], v[206:209], v[6:9]
	v_mfma_f32_16x16x32_bf16 v[2:5], v[158:161], v[206:209], v[2:5]
	s_setprio 0
	s_barrier
	s_add_i32 s64, 0, 0x18000
	s_add_i32 s65, 0, 0x1c000
	v_add_u32_e32 v130, s64, v220
	v_add_u32_e32 v158, s65, v220
	ds_read_b128 v[98:101], v130
	ds_read_b128 v[110:113], v130 offset:1024
	ds_read_b128 v[122:125], v130 offset:2048
	ds_read_b128 v[130:133], v130 offset:3072
	ds_read_b128 v[146:149], v158
	ds_read_b128 v[150:153], v158 offset:1024
	ds_read_b128 v[154:157], v158 offset:2048
	ds_read_b128 v[158:161], v158 offset:3072
	s_add_u32 s38, s38, 0x40000
	s_addc_u32 s39, s39, 0
	s_mov_b32 m0, s45
	v_lshl_add_u64 v[218:219], s[38:39], 0, v[186:187]
	ds_read_b128 v[162:165], v227 offset:32768
	ds_read_b128 v[166:169], v227 offset:33792
	ds_read_b128 v[170:173], v227 offset:34816
	ds_read_b128 v[174:177], v227 offset:35840
	ds_read_b128 v[178:181], v227 offset:36864
	ds_read_b128 v[182:185], v227 offset:37888
	ds_read_b128 v[202:205], v227 offset:38912
	ds_read_b128 v[206:209], v227 offset:39936
	global_load_lds_dwordx4 v[218:219], off
	v_lshl_add_u64 v[218:219], s[38:39], 0, v[190:191]
	s_mov_b32 m0, s48
	s_nop 0
	global_load_lds_dwordx4 v[218:219], off
	s_waitcnt vmcnt(8)
	s_waitcnt lgkmcnt(0)
	s_barrier
	s_setprio 1
	s_waitcnt lgkmcnt(0)
	v_mfma_f32_16x16x32_bf16 v[142:145], v[98:101], v[162:165], v[142:145]
	v_mfma_f32_16x16x32_bf16 v[138:141], v[122:125], v[162:165], v[138:141]
	v_mfma_f32_16x16x32_bf16 v[118:121], v[98:101], v[170:173], v[118:121]
	v_mfma_f32_16x16x32_bf16 v[114:117], v[122:125], v[170:173], v[114:117]
	v_mfma_f32_16x16x32_bf16 v[94:97], v[98:101], v[178:181], v[94:97]
	v_mfma_f32_16x16x32_bf16 v[90:93], v[122:125], v[178:181], v[90:93]
	v_mfma_f32_16x16x32_bf16 v[78:81], v[98:101], v[202:205], v[78:81]
	v_mfma_f32_16x16x32_bf16 v[74:77], v[122:125], v[202:205], v[74:77]
	v_mfma_f32_16x16x32_bf16 v[142:145], v[110:113], v[166:169], v[142:145]
	v_mfma_f32_16x16x32_bf16 v[138:141], v[130:133], v[166:169], v[138:141]
	v_mfma_f32_16x16x32_bf16 v[118:121], v[110:113], v[174:177], v[118:121]
	v_mfma_f32_16x16x32_bf16 v[114:117], v[130:133], v[174:177], v[114:117]
	v_mfma_f32_16x16x32_bf16 v[94:97], v[110:113], v[182:185], v[94:97]
	v_mfma_f32_16x16x32_bf16 v[90:93], v[130:133], v[182:185], v[90:93]
	v_mfma_f32_16x16x32_bf16 v[78:81], v[110:113], v[206:209], v[78:81]
	v_mfma_f32_16x16x32_bf16 v[74:77], v[130:133], v[206:209], v[74:77]
	s_setprio 0
	s_setprio 1
	v_mfma_f32_16x16x32_bf16 v[134:137], v[146:149], v[162:165], v[134:137]
	v_mfma_f32_16x16x32_bf16 v[126:129], v[154:157], v[162:165], v[126:129]
	v_mfma_f32_16x16x32_bf16 v[106:109], v[146:149], v[170:173], v[106:109]
	v_mfma_f32_16x16x32_bf16 v[102:105], v[154:157], v[170:173], v[102:105]
	v_mfma_f32_16x16x32_bf16 v[86:89], v[146:149], v[178:181], v[86:89]
	v_mfma_f32_16x16x32_bf16 v[82:85], v[154:157], v[178:181], v[82:85]
	v_mfma_f32_16x16x32_bf16 v[70:73], v[146:149], v[202:205], v[70:73]
	v_mfma_f32_16x16x32_bf16 v[66:69], v[154:157], v[202:205], v[66:69]
	v_mfma_f32_16x16x32_bf16 v[134:137], v[150:153], v[166:169], v[134:137]
	v_mfma_f32_16x16x32_bf16 v[126:129], v[158:161], v[166:169], v[126:129]
	v_mfma_f32_16x16x32_bf16 v[106:109], v[150:153], v[174:177], v[106:109]
	v_mfma_f32_16x16x32_bf16 v[102:105], v[158:161], v[174:177], v[102:105]
	v_mfma_f32_16x16x32_bf16 v[86:89], v[150:153], v[182:185], v[86:89]
	v_mfma_f32_16x16x32_bf16 v[82:85], v[158:161], v[182:185], v[82:85]
	v_mfma_f32_16x16x32_bf16 v[70:73], v[150:153], v[206:209], v[70:73]
	v_mfma_f32_16x16x32_bf16 v[66:69], v[158:161], v[206:209], v[66:69]
	s_setprio 0
	s_barrier
; #define PG8_STAGE_A(b, h, ptr, NX) do { if constexpr (Sched::GATHER) { unsigned gs_[2]; gs_[0] = ((NX) && last_) ? gN[h][0] : gA[h][0]; gs_[1] = ((NX) && last_) ? gN[h][1] : gA[h][1]; PG8_STAGE(PG8_SA(b, h), ptr, gs_); } \
;         else PG8_STAGE(PG8_SA(b, h), (ptr) + ((h) ? hstep : (size_t)0), voffA); } while (0)
; #define PG8_STAGE(bufoff, gbase, voff) do { _Pragma("unroll") for (int _i = 0; _i < 2; ++_i) \
;         __builtin_amdgcn_global_load_lds((const unsigned*)((const char*)(gbase) + (voff)[_i]), (PG8_LAS unsigned*)(lds + (bufoff) + ldsw + _i * 8192), 16, 0, 0); } while (0)
; #define PG8_LDA(dst, b, h) do { _Pragma("unroll") for (int m = 0; m < 4; ++m) _Pragma("unroll") for (int k = 0; k < 2; ++k) dst[m][k] = *(const PG8_LAS bf16x8*)(lds + PG8_SA(b, h) + aoff + m * 2048 + k * 1024); } while (0)
; #define PG8_MMA(ai, bj, At, Bt) do { __builtin_amdgcn_s_setprio(1); _Pragma("unroll") for (int m = 0; m < 4; ++m) _Pragma("unroll") for (int n = 0; n < 2; ++n) _Pragma("unroll") for (int k = 0; k < 2; ++k) \
;         acc[ai][bj][m][n] = __builtin_amdgcn_mfma_f32_16x16x32_bf16(Bt[n][k], At[m][k], acc[ai][bj][m][n], 0, 0, 0); __builtin_amdgcn_s_setprio(0); } while (0)
; #define PG8_WAIT_V(n) asm volatile("s_waitcnt vmcnt(" #n ")" ::: "memory")
; #define PG8_WAIT_L(n) asm volatile("s_waitcnt lgkmcnt(" #n ")" ::: "memory")
; #define PG8_BAR __builtin_amdgcn_s_barrier()
; #define PG8_SCHED __builtin_amdgcn_sched_barrier(0)
; template <class Epi, class Sched, bool ALIGN_EPI = false, bool SP2 = false>
; __device__ __forceinline__ void gemm_phase(PG8_LAS unsigned char* lds, const Gemm g, const Sched& S, const Epi& E, const bool skip_epi = false) {
;     ...
;         for (int t = 0; t < nt; t += 2) {
;             const bool last = (t == nt - 2); last_ = last && has_next;
;     ...
;             PG8_LDA(At, 1, 1); PG8_STAGE(PG8_SB(1, 0), b3, voffB); PG8_STAGE(PG8_SB(1, 1), b3 + hstep, voffB); PG8_STAGE_A(1, 0, a3, true);
;             PG8_WAIT_V(8); PG8_WAIT_L(0); PG8_BAR; PG8_MMA(1, 0, At, B0); PG8_MMA(1, 1, At, B1); PG8_BAR; PG8_SCHED;
	s_add_i32 s38, s64, s40
	v_lshl_add_u64 v[210:211], v[210:211], 0, s[12:13]
	s_mov_b32 m0, s38
	ds_read_b128 v[162:165], v227 offset:49152
	ds_read_b128 v[166:169], v227 offset:50176
	ds_read_b128 v[170:173], v227 offset:51200
	ds_read_b128 v[174:177], v227 offset:52224
	ds_read_b128 v[178:181], v227 offset:53248
	ds_read_b128 v[182:185], v227 offset:54272
	ds_read_b128 v[202:205], v227 offset:55296
	ds_read_b128 v[206:209], v227 offset:56320
	global_load_lds_dwordx4 v[210:211], off
	s_add_i32 m0, s38, 0x2000
	s_add_u32 s36, s36, 0x40080
	v_lshl_add_u64 v[210:211], v[212:213], 0, s[12:13]
	s_addc_u32 s37, s37, 0
	s_add_i32 s38, s65, s40
	global_load_lds_dwordx4 v[210:211], off
	v_lshl_add_u64 v[210:211], s[36:37], 0, v[188:189]
	s_mov_b32 m0, s38
	s_nop 0
	global_load_lds_dwordx4 v[210:211], off
	v_lshl_add_u64 v[210:211], s[36:37], 0, v[192:193]
	s_add_i32 m0, s38, 0x2000
	s_nop 0
	global_load_lds_dwordx4 v[210:211], off
	v_lshl_add_u64 v[210:211], v[214:215], 0, s[12:13]
	s_mov_b32 m0, s53
	s_nop 0
	global_load_lds_dwordx4 v[210:211], off
	v_lshl_add_u64 v[210:211], v[216:217], 0, s[12:13]
	s_mov_b32 m0, s54
	s_nop 0
	global_load_lds_dwordx4 v[210:211], off
	s_waitcnt vmcnt(8)
	s_waitcnt lgkmcnt(0)
	s_barrier
	s_setprio 1
	s_waitcnt lgkmcnt(0)
	v_mfma_f32_16x16x32_bf16 v[62:65], v[98:101], v[162:165], v[62:65]
	v_mfma_f32_16x16x32_bf16 v[58:61], v[122:125], v[162:165], v[58:61]
	v_mfma_f32_16x16x32_bf16 v[46:49], v[98:101], v[170:173], v[46:49]
	v_mfma_f32_16x16x32_bf16 v[42:45], v[122:125], v[170:173], v[42:45]
	v_mfma_f32_16x16x32_bf16 v[30:33], v[98:101], v[178:181], v[30:33]
	v_mfma_f32_16x16x32_bf16 v[26:29], v[122:125], v[178:181], v[26:29]
	v_mfma_f32_16x16x32_bf16 v[14:17], v[98:101], v[202:205], v[14:17]
	v_mfma_f32_16x16x32_bf16 v[10:13], v[122:125], v[202:205], v[10:13]
	v_mfma_f32_16x16x32_bf16 v[62:65], v[110:113], v[166:169], v[62:65]
	v_mfma_f32_16x16x32_bf16 v[58:61], v[130:133], v[166:169], v[58:61]
	v_mfma_f32_16x16x32_bf16 v[46:49], v[110:113], v[174:177], v[46:49]
	v_mfma_f32_16x16x32_bf16 v[42:45], v[130:133], v[174:177], v[42:45]
	v_mfma_f32_16x16x32_bf16 v[30:33], v[110:113], v[182:185], v[30:33]
	v_mfma_f32_16x16x32_bf16 v[26:29], v[130:133], v[182:185], v[26:29]
	v_mfma_f32_16x16x32_bf16 v[14:17], v[110:113], v[206:209], v[14:17]
	v_mfma_f32_16x16x32_bf16 v[10:13], v[130:133], v[206:209], v[10:13]
	s_setprio 0
	s_setprio 1
	v_mfma_f32_16x16x32_bf16 v[54:57], v[146:149], v[162:165], v[54:57]
	v_mfma_f32_16x16x32_bf16 v[50:53], v[154:157], v[162:165], v[50:53]
	v_mfma_f32_16x16x32_bf16 v[38:41], v[146:149], v[170:173], v[38:41]
	v_mfma_f32_16x16x32_bf16 v[34:37], v[154:157], v[170:173], v[34:37]
	v_mfma_f32_16x16x32_bf16 v[22:25], v[146:149], v[178:181], v[22:25]
	v_mfma_f32_16x16x32_bf16 v[18:21], v[154:157], v[178:181], v[18:21]
	v_mfma_f32_16x16x32_bf16 v[6:9], v[146:149], v[202:205], v[6:9]
	v_mfma_f32_16x16x32_bf16 v[2:5], v[154:157], v[202:205], v[2:5]
	v_mfma_f32_16x16x32_bf16 v[54:57], v[150:153], v[166:169], v[54:57]
	v_mfma_f32_16x16x32_bf16 v[50:53], v[158:161], v[166:169], v[50:53]
	v_mfma_f32_16x16x32_bf16 v[38:41], v[150:153], v[174:177], v[38:41]
	v_mfma_f32_16x16x32_bf16 v[34:37], v[158:161], v[174:177], v[34:37]
	v_mfma_f32_16x16x32_bf16 v[22:25], v[150:153], v[182:185], v[22:25]
	v_mfma_f32_16x16x32_bf16 v[18:21], v[158:161], v[182:185], v[18:21]
	v_mfma_f32_16x16x32_bf16 v[6:9], v[150:153], v[206:209], v[6:9]
	v_mfma_f32_16x16x32_bf16 v[2:5], v[158:161], v[206:209], v[2:5]
	s_setprio 0
	s_barrier
	s_add_i32 s63, s63, 2
	s_add_u32 s34, s34, 0x100
	s_addc_u32 s35, s35, 0
	s_add_u32 s61, s61, 0x100
	s_addc_u32 s62, s62, 0
	s_cmp_gt_u32 s63, 13

; #define PG8_GIDX(G_, PM_) do { if constexpr (Sched::GATHER) { _Pragma("unroll") for (int h_ = 0; h_ < 2; ++h_) _Pragma("unroll") for (int i_ = 0; i_ < 2; ++i_) { int R_, C_; stage_rc(tid * 16 + i_ * 8192, R_, C_); \
;         const int src_ = S.rowsrc[(PM_) * BM + h_ * HALF + R_]; G_[h_][i_] = (unsigned)(src_ * K + C_) * 2u; } } } while (0)
; #define PG8_STAGE_A(b, h, ptr, NX) do { if constexpr (Sched::GATHER) { unsigned gs_[2]; gs_[0] = ((NX) && last_) ? gN[h][0] : gA[h][0]; gs_[1] = ((NX) && last_) ? gN[h][1] : gA[h][1]; PG8_STAGE(PG8_SA(b, h), ptr, gs_); } \
;         else PG8_STAGE(PG8_SA(b, h), (ptr) + ((h) ? hstep : (size_t)0), voffA); } while (0)
; #define PG8_LDA(dst, b, h) do { _Pragma("unroll") for (int m = 0; m < 4; ++m) _Pragma("unroll") for (int k = 0; k < 2; ++k) dst[m][k] = *(const PG8_LAS bf16x8*)(lds + PG8_SA(b, h) + aoff + m * 2048 + k * 1024); } while (0)
; template <class Epi, class Sched, bool ALIGN_EPI = false, bool SP2 = false>
; __device__ __forceinline__ void gemm_phase(PG8_LAS unsigned char* lds, const Gemm g, const Sched& S, const Epi& E, const bool skip_epi = false) {
;     ...
;         const bool has_next = S.next(ui + 1, nxt);
;         if (has_next) PG8_GIDX(gN, nxt.pm);
;         const char* nA = has_next ? (const char*)g.A + (size_t)nxt.pm * pmstepA + nxt.ko : cA; const char* nB = has_next ? (const char*)g.Bt + (size_t)nxt.pn * tstep + nxt.ko : cB;
;         for (int t = 0; t < nt; t += 2) {
;             const bool last = (t == nt - 2); last_ = last && has_next;
;             const char* a1 = cA + (size_t)(t + 1) * kstep;
;             const char* a2 = last ? nA : cA + (size_t)(t + 2) * kstep; const char* b2 = last ? nB : cB + (size_t)(t + 2) * kstep;
;             const char* a3 = a2 + kstep; const char* b3 = b2 + kstep;
;             if (last && has_next) S.a_ready(nxt);
;             if constexpr (SP2) {
;             PG8_LDB(B0, 0, 0); PG8_LDB(B1, 0, 1); PG8_SCHED; PG8_LDA(At, 0, 0); PG8_STAGE_A(1, 1, a1, false);
;             PG8_WAIT_V(8); PG8_WAIT_L(0); PG8_BAR; PG8_MMA(0, 0, At, B0); PG8_MMA(0, 1, At, B1); PG8_BAR; PG8_SCHED;
;             PG8_LDA(At, 0, 1); PG8_STAGE(PG8_SB(0, 0), b2, voffB); PG8_STAGE(PG8_SB(0, 1), b2 + hstep, voffB); PG8_STAGE_A(0, 0, a2, true);
;             PG8_WAIT_V(8); PG8_WAIT_L(0); PG8_BAR; PG8_MMA(1, 0, At, B0); PG8_MMA(1, 1, At, B1); PG8_BAR; PG8_SCHED;
.Lg5_zero:
.LBB0_1727:
	s_mov_b32 s29, s41
	s_mov_b32 s31, s40
	v_mov_b32_e32 v143, v133
	v_mov_b32_e32 v141, v133
	s_add_u32 s61, s40, 0x100
	v_lshl_add_u64 v[146:147], s[24:25], 0, v[140:141]
	v_lshl_add_u64 v[148:149], s[24:25], 0, v[142:143]
	s_addc_u32 s62, s41, 0
	s_mov_b32 s63, -2
	s_mov_b64 s[40:41], 0
	ds_read_b128 v[166:169], v158
	ds_read_b128 v[170:173], v158 offset:1024
	ds_read_b128 v[174:177], v158 offset:2048
	ds_read_b128 v[178:181], v158 offset:3072
	ds_read_b128 v[182:185], v159
	ds_read_b128 v[186:189], v159 offset:1024
	ds_read_b128 v[190:193], v159 offset:2048
	ds_read_b128 v[194:197], v159 offset:3072
	s_add_u32 s42, s78, s40
	s_addc_u32 s43, s79, s41
	s_add_u32 s44, s42, 0x1aa00100
	s_addc_u32 s45, s43, 0
	s_add_u32 s66, s61, s40
	s_addc_u32 s67, s62, s41
	s_cmpk_eq_i32 s40, 0x700
	s_cselect_b64 s[64:65], -1, 0
	s_and_b64 s[42:43], s[64:65], exec
	s_cselect_b32 s45, s87, s45
	s_cselect_b32 s44, s86, s44
	s_cselect_b32 s42, s31, s66
	s_cselect_b32 s43, s29, s67
	s_and_b64 vcc, s[6:7], s[64:65]
	v_lshl_add_u64 v[226:227], v[148:149], 0, s[40:41]
	s_add_i32 m0, s37, 0xc000
	ds_read_b128 v[198:201], v160
	ds_read_b128 v[202:205], v160 offset:1024
	ds_read_b128 v[206:209], v160 offset:2048
	ds_read_b128 v[210:213], v160 offset:3072
	ds_read_b128 v[214:217], v160 offset:4096
	ds_read_b128 v[218:221], v160 offset:5120
	ds_read_b128 v[222:225], v160 offset:6144
	ds_read_b128 v[230:233], v160 offset:7168
	global_load_lds_dwordx4 v[226:227], off
	v_lshl_add_u64 v[226:227], v[146:147], 0, s[40:41]
	s_add_i32 m0, s37, 0xe000
	s_nop 0
	global_load_lds_dwordx4 v[226:227], off
	s_waitcnt vmcnt(8)
	s_waitcnt lgkmcnt(0)
	s_barrier
	s_setprio 1
	s_waitcnt lgkmcnt(0)
	v_mfma_f32_16x16x32_bf16 v[126:129], v[166:169], v[198:201], 0
	v_mfma_f32_16x16x32_bf16 v[122:125], v[174:177], v[198:201], 0
	v_mfma_f32_16x16x32_bf16 v[110:113], v[166:169], v[206:209], 0
	v_mfma_f32_16x16x32_bf16 v[106:109], v[174:177], v[206:209], 0
	v_mfma_f32_16x16x32_bf16 v[94:97], v[166:169], v[214:217], 0
	v_mfma_f32_16x16x32_bf16 v[90:93], v[174:177], v[214:217], 0
	v_mfma_f32_16x16x32_bf16 v[78:81], v[166:169], v[222:225], 0
	v_mfma_f32_16x16x32_bf16 v[74:77], v[174:177], v[222:225], 0
	v_mfma_f32_16x16x32_bf16 v[126:129], v[170:173], v[202:205], v[126:129]
	v_mfma_f32_16x16x32_bf16 v[122:125], v[178:181], v[202:205], v[122:125]
	v_mfma_f32_16x16x32_bf16 v[110:113], v[170:173], v[210:213], v[110:113]
	v_mfma_f32_16x16x32_bf16 v[106:109], v[178:181], v[210:213], v[106:109]
	v_mfma_f32_16x16x32_bf16 v[94:97], v[170:173], v[218:221], v[94:97]
	v_mfma_f32_16x16x32_bf16 v[90:93], v[178:181], v[218:221], v[90:93]
	v_mfma_f32_16x16x32_bf16 v[78:81], v[170:173], v[230:233], v[78:81]
	v_mfma_f32_16x16x32_bf16 v[74:77], v[178:181], v[230:233], v[74:77]
	s_setprio 0
	s_setprio 1
	v_mfma_f32_16x16x32_bf16 v[118:121], v[182:185], v[198:201], 0
	v_mfma_f32_16x16x32_bf16 v[114:117], v[190:193], v[198:201], 0
	v_mfma_f32_16x16x32_bf16 v[102:105], v[182:185], v[206:209], 0
	v_mfma_f32_16x16x32_bf16 v[98:101], v[190:193], v[206:209], 0
	v_mfma_f32_16x16x32_bf16 v[86:89], v[182:185], v[214:217], 0
	v_mfma_f32_16x16x32_bf16 v[82:85], v[190:193], v[214:217], 0
	v_mfma_f32_16x16x32_bf16 v[70:73], v[182:185], v[222:225], 0
	v_mfma_f32_16x16x32_bf16 v[66:69], v[190:193], v[222:225], 0
	v_mfma_f32_16x16x32_bf16 v[118:121], v[186:189], v[202:205], v[118:121]
	v_mfma_f32_16x16x32_bf16 v[114:117], v[194:197], v[202:205], v[114:117]
	v_mfma_f32_16x16x32_bf16 v[102:105], v[186:189], v[210:213], v[102:105]
	v_mfma_f32_16x16x32_bf16 v[98:101], v[194:197], v[210:213], v[98:101]
	v_mfma_f32_16x16x32_bf16 v[86:89], v[186:189], v[218:221], v[86:89]
	v_mfma_f32_16x16x32_bf16 v[82:85], v[194:197], v[218:221], v[82:85]
	v_mfma_f32_16x16x32_bf16 v[70:73], v[186:189], v[230:233], v[70:73]
	v_mfma_f32_16x16x32_bf16 v[66:69], v[194:197], v[230:233], v[66:69]
	s_setprio 0
	s_barrier
	s_add_i32 s64, s58, s50
	v_lshl_add_u64 v[226:227], s[42:43], 0, v[134:135]
	s_mov_b32 m0, s64
	ds_read_b128 v[198:201], v160 offset:16384
	ds_read_b128 v[202:205], v160 offset:17408
	ds_read_b128 v[206:209], v160 offset:18432
	ds_read_b128 v[210:213], v160 offset:19456
	ds_read_b128 v[214:217], v160 offset:20480
	ds_read_b128 v[218:221], v160 offset:21504
	ds_read_b128 v[222:225], v160 offset:22528
	ds_read_b128 v[230:233], v160 offset:23552
	global_load_lds_dwordx4 v[226:227], off
	s_add_i32 m0, s64, 0x2000
	s_add_u32 s64, s42, 0x40000
	v_lshl_add_u64 v[234:235], s[42:43], 0, v[136:137]
	s_addc_u32 s65, s43, 0
	s_add_i32 s66, s59, s50
	global_load_lds_dwordx4 v[234:235], off
	v_lshl_add_u64 v[236:237], s[64:65], 0, v[134:135]
	s_mov_b32 m0, s66
	v_cndmask_b32_e32 v132, v130, v164, vcc
	global_load_lds_dwordx4 v[236:237], off
	v_lshl_add_u64 v[236:237], s[64:65], 0, v[136:137]
	s_add_i32 m0, s66, 0x2000
	v_lshl_add_u64 v[238:239], s[44:45], 0, v[132:133]
	global_load_lds_dwordx4 v[236:237], off
	s_mov_b32 m0, s37
	v_cndmask_b32_e32 v236, v144, v163, vcc
	global_load_lds_dwordx4 v132, s[44:45]
	s_mov_b32 m0, s39
	v_mov_b32_e32 v237, v133
	global_load_lds_dwordx4 v236, s[44:45]
	s_waitcnt vmcnt(8)
	s_waitcnt lgkmcnt(0)
	v_lshl_add_u64 v[236:237], s[44:45], 0, v[236:237]
	s_barrier
; #define PG8_STAGE_A(b, h, ptr, NX) do { if constexpr (Sched::GATHER) { unsigned gs_[2]; gs_[0] = ((NX) && last_) ? gN[h][0] : gA[h][0]; gs_[1] = ((NX) && last_) ? gN[h][1] : gA[h][1]; PG8_STAGE(PG8_SA(b, h), ptr, gs_); } \
;         else PG8_STAGE(PG8_SA(b, h), (ptr) + ((h) ? hstep : (size_t)0), voffA); } while (0)
; #define PG8_LDA(dst, b, h) do { _Pragma("unroll") for (int m = 0; m < 4; ++m) _Pragma("unroll") for (int k = 0; k < 2; ++k) dst[m][k] = *(const PG8_LAS bf16x8*)(lds + PG8_SA(b, h) + aoff + m * 2048 + k * 1024); } while (0)
; #define PG8_LDB(dst, b, h) do { _Pragma("unroll") for (int n = 0; n < 2; ++n) _Pragma("unroll") for (int k = 0; k < 2; ++k) dst[n][k] = *(const PG8_LAS bf16x8*)(lds + PG8_SB(b, h) + boff + n * 2048 + k * 1024); } while (0)
; #define PG8_MMA(ai, bj, At, Bt) do { __builtin_amdgcn_s_setprio(1); _Pragma("unroll") for (int m = 0; m < 4; ++m) _Pragma("unroll") for (int n = 0; n < 2; ++n) _Pragma("unroll") for (int k = 0; k < 2; ++k) \
;         acc[ai][bj][m][n] = __builtin_amdgcn_mfma_f32_16x16x32_bf16(Bt[n][k], At[m][k], acc[ai][bj][m][n], 0, 0, 0); __builtin_amdgcn_s_setprio(0); } while (0)
; #define PG8_WAIT_V(n) asm volatile("s_waitcnt vmcnt(" #n ")" ::: "memory")
; #define PG8_WAIT_L(n) asm volatile("s_waitcnt lgkmcnt(" #n ")" ::: "memory")
; #define PG8_BAR __builtin_amdgcn_s_barrier()
; #define PG8_SCHED __builtin_amdgcn_sched_barrier(0)
; template <class Epi, class Sched, bool ALIGN_EPI = false, bool SP2 = false>
; __device__ __forceinline__ void gemm_phase(PG8_LAS unsigned char* lds, const Gemm g, const Sched& S, const Epi& E, const bool skip_epi = false) {
;     ...
;             PG8_WAIT_V(8); PG8_WAIT_L(0); PG8_BAR; PG8_MMA(1, 0, At, B0); PG8_MMA(1, 1, At, B1); PG8_BAR; PG8_SCHED;
;             PG8_LDB(B0, 1, 0); PG8_LDB(B1, 1, 1); PG8_SCHED; PG8_LDA(At, 1, 0); PG8_STAGE_A(0, 1, a2, true);
;             PG8_WAIT_V(8); PG8_WAIT_L(0); PG8_BAR; PG8_MMA(0, 0, At, B0); PG8_MMA(0, 1, At, B1); PG8_BAR; PG8_SCHED;
	s_setprio 1
	s_waitcnt lgkmcnt(0)
	v_mfma_f32_16x16x32_bf16 v[62:65], v[166:169], v[198:201], 0
	v_mfma_f32_16x16x32_bf16 v[58:61], v[174:177], v[198:201], 0
	v_mfma_f32_16x16x32_bf16 v[38:41], v[166:169], v[206:209], 0
	v_mfma_f32_16x16x32_bf16 v[34:37], v[174:177], v[206:209], 0
	v_mfma_f32_16x16x32_bf16 v[22:25], v[166:169], v[214:217], 0
	v_mfma_f32_16x16x32_bf16 v[18:21], v[174:177], v[214:217], 0
	v_mfma_f32_16x16x32_bf16 v[6:9], v[166:169], v[222:225], 0
	v_mfma_f32_16x16x32_bf16 v[2:5], v[174:177], v[222:225], 0
	v_mfma_f32_16x16x32_bf16 v[62:65], v[170:173], v[202:205], v[62:65]
	v_mfma_f32_16x16x32_bf16 v[58:61], v[178:181], v[202:205], v[58:61]
	v_mfma_f32_16x16x32_bf16 v[38:41], v[170:173], v[210:213], v[38:41]
	v_mfma_f32_16x16x32_bf16 v[34:37], v[178:181], v[210:213], v[34:37]
	v_mfma_f32_16x16x32_bf16 v[22:25], v[170:173], v[218:221], v[22:25]
	v_mfma_f32_16x16x32_bf16 v[18:21], v[178:181], v[218:221], v[18:21]
	v_mfma_f32_16x16x32_bf16 v[6:9], v[170:173], v[230:233], v[6:9]
	v_mfma_f32_16x16x32_bf16 v[2:5], v[178:181], v[230:233], v[2:5]
	s_setprio 0
	s_setprio 1
	v_mfma_f32_16x16x32_bf16 v[50:53], v[182:185], v[198:201], 0
	v_mfma_f32_16x16x32_bf16 v[42:45], v[190:193], v[198:201], 0
	v_mfma_f32_16x16x32_bf16 v[54:57], v[182:185], v[206:209], 0
	v_mfma_f32_16x16x32_bf16 v[46:49], v[190:193], v[206:209], 0
	v_mfma_f32_16x16x32_bf16 v[30:33], v[182:185], v[214:217], 0
	v_mfma_f32_16x16x32_bf16 v[26:29], v[190:193], v[214:217], 0
	v_mfma_f32_16x16x32_bf16 v[14:17], v[182:185], v[222:225], 0
	v_mfma_f32_16x16x32_bf16 v[10:13], v[190:193], v[222:225], 0
	v_mfma_f32_16x16x32_bf16 v[50:53], v[186:189], v[202:205], v[50:53]
	v_mfma_f32_16x16x32_bf16 v[42:45], v[194:197], v[202:205], v[42:45]
	v_mfma_f32_16x16x32_bf16 v[54:57], v[186:189], v[210:213], v[54:57]
	v_mfma_f32_16x16x32_bf16 v[46:49], v[194:197], v[210:213], v[46:49]
	v_mfma_f32_16x16x32_bf16 v[30:33], v[186:189], v[218:221], v[30:33]
	v_mfma_f32_16x16x32_bf16 v[26:29], v[194:197], v[218:221], v[26:29]
	v_mfma_f32_16x16x32_bf16 v[14:17], v[186:189], v[230:233], v[14:17]
	v_mfma_f32_16x16x32_bf16 v[10:13], v[194:197], v[230:233], v[10:13]
	s_setprio 0
	s_barrier
	s_add_i32 s64, 0, 0x18000
	v_add_u32_e32 v132, s64, v154
	s_add_i32 s65, 0, 0x1c000
	ds_read_b128 v[166:169], v132
	ds_read_b128 v[170:173], v132 offset:1024
	ds_read_b128 v[174:177], v132 offset:2048
	ds_read_b128 v[178:181], v132 offset:3072
	v_add_u32_e32 v132, s65, v154
	ds_read_b128 v[182:185], v132
	ds_read_b128 v[186:189], v132 offset:1024
	ds_read_b128 v[190:193], v132 offset:2048
	ds_read_b128 v[194:197], v132 offset:3072
	s_mov_b32 m0, s51
	v_cndmask_b32_e32 v132, v142, v162, vcc
	ds_read_b128 v[198:201], v160 offset:32768
	ds_read_b128 v[202:205], v160 offset:33792
	ds_read_b128 v[206:209], v160 offset:34816
	ds_read_b128 v[210:213], v160 offset:35840
	ds_read_b128 v[214:217], v160 offset:36864
	ds_read_b128 v[218:221], v160 offset:37888
	ds_read_b128 v[222:225], v160 offset:38912
	ds_read_b128 v[230:233], v160 offset:39936
	v_cndmask_b32_e32 v141, v140, v161, vcc
	global_load_lds_dwordx4 v132, s[44:45]
	s_mov_b32 m0, s52
	s_nop 0
	global_load_lds_dwordx4 v141, s[44:45]
	s_waitcnt vmcnt(8)
	s_waitcnt lgkmcnt(0)
	s_barrier
	s_setprio 1
	s_waitcnt lgkmcnt(0)
	v_mfma_f32_16x16x32_bf16 v[126:129], v[166:169], v[198:201], v[126:129]
	v_mfma_f32_16x16x32_bf16 v[122:125], v[174:177], v[198:201], v[122:125]
	v_mfma_f32_16x16x32_bf16 v[110:113], v[166:169], v[206:209], v[110:113]
	v_mfma_f32_16x16x32_bf16 v[106:109], v[174:177], v[206:209], v[106:109]
	v_mfma_f32_16x16x32_bf16 v[94:97], v[166:169], v[214:217], v[94:97]
	v_mfma_f32_16x16x32_bf16 v[90:93], v[174:177], v[214:217], v[90:93]
	v_mfma_f32_16x16x32_bf16 v[78:81], v[166:169], v[222:225], v[78:81]
	v_mfma_f32_16x16x32_bf16 v[74:77], v[174:177], v[222:225], v[74:77]
	v_mfma_f32_16x16x32_bf16 v[126:129], v[170:173], v[202:205], v[126:129]
	v_mfma_f32_16x16x32_bf16 v[122:125], v[178:181], v[202:205], v[122:125]
	v_mfma_f32_16x16x32_bf16 v[110:113], v[170:173], v[210:213], v[110:113]
	v_mfma_f32_16x16x32_bf16 v[106:109], v[178:181], v[210:213], v[106:109]
	v_mfma_f32_16x16x32_bf16 v[94:97], v[170:173], v[218:221], v[94:97]
	v_mfma_f32_16x16x32_bf16 v[90:93], v[178:181], v[218:221], v[90:93]
	v_mfma_f32_16x16x32_bf16 v[78:81], v[170:173], v[230:233], v[78:81]
	v_mfma_f32_16x16x32_bf16 v[74:77], v[178:181], v[230:233], v[74:77]
	s_setprio 0
	s_setprio 1
	v_mfma_f32_16x16x32_bf16 v[118:121], v[182:185], v[198:201], v[118:121]
	v_mfma_f32_16x16x32_bf16 v[114:117], v[190:193], v[198:201], v[114:117]
	v_mfma_f32_16x16x32_bf16 v[102:105], v[182:185], v[206:209], v[102:105]
	v_mfma_f32_16x16x32_bf16 v[98:101], v[190:193], v[206:209], v[98:101]
	v_mfma_f32_16x16x32_bf16 v[86:89], v[182:185], v[214:217], v[86:89]
	v_mfma_f32_16x16x32_bf16 v[82:85], v[190:193], v[214:217], v[82:85]
	v_mfma_f32_16x16x32_bf16 v[70:73], v[182:185], v[222:225], v[70:73]
	v_mfma_f32_16x16x32_bf16 v[66:69], v[190:193], v[222:225], v[66:69]
	v_mfma_f32_16x16x32_bf16 v[118:121], v[186:189], v[202:205], v[118:121]
	v_mfma_f32_16x16x32_bf16 v[114:117], v[194:197], v[202:205], v[114:117]
	v_mfma_f32_16x16x32_bf16 v[102:105], v[186:189], v[210:213], v[102:105]
	v_mfma_f32_16x16x32_bf16 v[98:101], v[194:197], v[210:213], v[98:101]
	v_mfma_f32_16x16x32_bf16 v[86:89], v[186:189], v[218:221], v[86:89]
	v_mfma_f32_16x16x32_bf16 v[82:85], v[194:197], v[218:221], v[82:85]
	v_mfma_f32_16x16x32_bf16 v[70:73], v[186:189], v[230:233], v[70:73]
	v_mfma_f32_16x16x32_bf16 v[66:69], v[194:197], v[230:233], v[66:69]
	s_setprio 0
	s_barrier
; #define PG8_STAGE_A(b, h, ptr, NX) do { if constexpr (Sched::GATHER) { unsigned gs_[2]; gs_[0] = ((NX) && last_) ? gN[h][0] : gA[h][0]; gs_[1] = ((NX) && last_) ? gN[h][1] : gA[h][1]; PG8_STAGE(PG8_SA(b, h), ptr, gs_); } \
;         else PG8_STAGE(PG8_SA(b, h), (ptr) + ((h) ? hstep : (size_t)0), voffA); } while (0)
; #define PG8_STAGE(bufoff, gbase, voff) do { _Pragma("unroll") for (int _i = 0; _i < 2; ++_i) \
;         __builtin_amdgcn_global_load_lds((const unsigned*)((const char*)(gbase) + (voff)[_i]), (PG8_LAS unsigned*)(lds + (bufoff) + ldsw + _i * 8192), 16, 0, 0); } while (0)
; #define PG8_LDA(dst, b, h) do { _Pragma("unroll") for (int m = 0; m < 4; ++m) _Pragma("unroll") for (int k = 0; k < 2; ++k) dst[m][k] = *(const PG8_LAS bf16x8*)(lds + PG8_SA(b, h) + aoff + m * 2048 + k * 1024); } while (0)
; #define PG8_MMA(ai, bj, At, Bt) do { __builtin_amdgcn_s_setprio(1); _Pragma("unroll") for (int m = 0; m < 4; ++m) _Pragma("unroll") for (int n = 0; n < 2; ++n) _Pragma("unroll") for (int k = 0; k < 2; ++k) \
;         acc[ai][bj][m][n] = __builtin_amdgcn_mfma_f32_16x16x32_bf16(Bt[n][k], At[m][k], acc[ai][bj][m][n], 0, 0, 0); __builtin_amdgcn_s_setprio(0); } while (0)
; #define PG8_WAIT_V(n) asm volatile("s_waitcnt vmcnt(" #n ")" ::: "memory")
; #define PG8_WAIT_L(n) asm volatile("s_waitcnt lgkmcnt(" #n ")" ::: "memory")
; #define PG8_BAR __builtin_amdgcn_s_barrier()
; #define PG8_SCHED __builtin_amdgcn_sched_barrier(0)
;     __device__ bool next(int i, Unit& u) const {
;     ...
;         const int nig = GP * NT, grp = wgid / nig, fm = grp * GP, gsz = (npan - fm) < GP ? (npan - fm) : GP; const int rr = wgid % nig;
;         const int p = fm + rr % gsz; u.pm = p; u.pn = panel_e[p] * NT + rr / gsz; u.ko = 0; return true;
; template <class Epi, class Sched, bool ALIGN_EPI = false, bool SP2 = false>
; __device__ __forceinline__ void gemm_phase(PG8_LAS unsigned char* lds, const Gemm g, const Sched& S, const Epi& E, const bool skip_epi = false) {
;     ...
;             PG8_LDA(At, 1, 1); PG8_STAGE(PG8_SB(1, 0), b3, voffB); PG8_STAGE(PG8_SB(1, 1), b3 + hstep, voffB); PG8_STAGE_A(1, 0, a3, true);
;             PG8_WAIT_V(8); PG8_WAIT_L(0); PG8_BAR; PG8_MMA(1, 0, At, B0); PG8_MMA(1, 1, At, B1); PG8_BAR; PG8_SCHED;
	s_add_i32 s44, s64, s50
	v_lshl_add_u64 v[226:227], v[226:227], 0, s[22:23]
	s_mov_b32 m0, s44
	ds_read_b128 v[198:201], v160 offset:49152
	ds_read_b128 v[202:205], v160 offset:50176
	ds_read_b128 v[206:209], v160 offset:51200
	ds_read_b128 v[210:213], v160 offset:52224
	ds_read_b128 v[214:217], v160 offset:53248
	ds_read_b128 v[218:221], v160 offset:54272
	ds_read_b128 v[222:225], v160 offset:55296
	ds_read_b128 v[230:233], v160 offset:56320
	global_load_lds_dwordx4 v[226:227], off
	s_add_i32 m0, s44, 0x2000
	s_add_u32 s42, s42, 0x40080
	v_lshl_add_u64 v[226:227], v[234:235], 0, s[22:23]
	s_addc_u32 s43, s43, 0
	s_add_i32 s44, s65, s50
	global_load_lds_dwordx4 v[226:227], off
	v_lshl_add_u64 v[226:227], s[42:43], 0, v[134:135]
	s_mov_b32 m0, s44
	s_nop 0
	global_load_lds_dwordx4 v[226:227], off
	v_lshl_add_u64 v[226:227], s[42:43], 0, v[136:137]
	s_add_i32 m0, s44, 0x2000
	s_nop 0
	global_load_lds_dwordx4 v[226:227], off
	v_lshl_add_u64 v[226:227], v[238:239], 0, s[22:23]
	s_mov_b32 m0, s55
	s_nop 0
	global_load_lds_dwordx4 v[226:227], off
	v_lshl_add_u64 v[226:227], v[236:237], 0, s[22:23]
	s_mov_b32 m0, s56
	s_nop 0
	global_load_lds_dwordx4 v[226:227], off
	s_waitcnt vmcnt(8)
	s_waitcnt lgkmcnt(0)
	s_barrier
	s_setprio 1
	s_waitcnt lgkmcnt(0)
	v_mfma_f32_16x16x32_bf16 v[62:65], v[166:169], v[198:201], v[62:65]
	v_mfma_f32_16x16x32_bf16 v[58:61], v[174:177], v[198:201], v[58:61]
	v_mfma_f32_16x16x32_bf16 v[38:41], v[166:169], v[206:209], v[38:41]
	v_mfma_f32_16x16x32_bf16 v[34:37], v[174:177], v[206:209], v[34:37]
	v_mfma_f32_16x16x32_bf16 v[22:25], v[166:169], v[214:217], v[22:25]
	v_mfma_f32_16x16x32_bf16 v[18:21], v[174:177], v[214:217], v[18:21]
	v_mfma_f32_16x16x32_bf16 v[6:9], v[166:169], v[222:225], v[6:9]
	v_mfma_f32_16x16x32_bf16 v[2:5], v[174:177], v[222:225], v[2:5]
	v_mfma_f32_16x16x32_bf16 v[62:65], v[170:173], v[202:205], v[62:65]
	v_mfma_f32_16x16x32_bf16 v[58:61], v[178:181], v[202:205], v[58:61]
	v_mfma_f32_16x16x32_bf16 v[38:41], v[170:173], v[210:213], v[38:41]
	v_mfma_f32_16x16x32_bf16 v[34:37], v[178:181], v[210:213], v[34:37]
	v_mfma_f32_16x16x32_bf16 v[22:25], v[170:173], v[218:221], v[22:25]
	v_mfma_f32_16x16x32_bf16 v[18:21], v[178:181], v[218:221], v[18:21]
	v_mfma_f32_16x16x32_bf16 v[6:9], v[170:173], v[230:233], v[6:9]
	v_mfma_f32_16x16x32_bf16 v[2:5], v[178:181], v[230:233], v[2:5]
	s_setprio 0
	s_setprio 1
	v_mfma_f32_16x16x32_bf16 v[50:53], v[182:185], v[198:201], v[50:53]
	v_mfma_f32_16x16x32_bf16 v[42:45], v[190:193], v[198:201], v[42:45]
	v_mfma_f32_16x16x32_bf16 v[54:57], v[182:185], v[206:209], v[54:57]
	v_mfma_f32_16x16x32_bf16 v[46:49], v[190:193], v[206:209], v[46:49]
	v_mfma_f32_16x16x32_bf16 v[30:33], v[182:185], v[214:217], v[30:33]
	v_mfma_f32_16x16x32_bf16 v[26:29], v[190:193], v[214:217], v[26:29]
	v_mfma_f32_16x16x32_bf16 v[14:17], v[182:185], v[222:225], v[14:17]
	v_mfma_f32_16x16x32_bf16 v[10:13], v[190:193], v[222:225], v[10:13]
	v_mfma_f32_16x16x32_bf16 v[50:53], v[186:189], v[202:205], v[50:53]
	v_mfma_f32_16x16x32_bf16 v[42:45], v[194:197], v[202:205], v[42:45]
	v_mfma_f32_16x16x32_bf16 v[54:57], v[186:189], v[210:213], v[54:57]
	v_mfma_f32_16x16x32_bf16 v[46:49], v[194:197], v[210:213], v[46:49]
	v_mfma_f32_16x16x32_bf16 v[30:33], v[186:189], v[218:221], v[30:33]
	v_mfma_f32_16x16x32_bf16 v[26:29], v[194:197], v[218:221], v[26:29]
	v_mfma_f32_16x16x32_bf16 v[14:17], v[186:189], v[230:233], v[14:17]
	v_mfma_f32_16x16x32_bf16 v[10:13], v[194:197], v[230:233], v[10:13]
	s_setprio 0
	s_barrier
	s_add_i32 s63, s63, 2
	s_add_u32 s40, s40, 0x100
	s_addc_u32 s41, s41, 0
	s_cmp_gt_u32 s63, 13
	s_andn2_b64 vcc, exec, s[6:7]
	s_cbranch_vccnz .Lg5_nonext
	s_waitcnt vmcnt(8)
	v_readfirstlane_b32 s34, v250
	v_lshl_add_u32 v164, v229, 11, v152
	v_lshl_add_u32 v163, v251, 11, v153
	v_lshl_add_u32 v162, v252, 11, v152
	v_lshl_add_u32 v161, v253, 11, v153
	s_mul_i32 s34, s34, 28
	s_add_i32 s30, s34, s30
	s_ashr_i32 s31, s30, 31
	s_lshl_b64 s[34:35], s[30:31], 19
	v_readlane_b32 s42, v254, 29
	v_readlane_b32 s43, v254, 30
	s_add_u32 s34, s42, s34
	s_addc_u32 s35, s43, s35
	s_mov_b32 s29, s35
	s_mov_b32 s31, s34
.Lg5_nonext:
.LBB0_1728:
	ds_read_b128 v[166:169], v158
	ds_read_b128 v[170:173], v158 offset:1024
	ds_read_b128 v[174:177], v158 offset:2048
	ds_read_b128 v[178:181], v158 offset:3072
	ds_read_b128 v[182:185], v159
	ds_read_b128 v[186:189], v159 offset:1024
	ds_read_b128 v[190:193], v159 offset:2048
	ds_read_b128 v[194:197], v159 offset:3072
	s_add_u32 s42, s78, s40
	s_addc_u32 s43, s79, s41
	s_add_u32 s44, s42, 0x1aa00100
	s_addc_u32 s45, s43, 0
	s_add_u32 s66, s61, s40
	s_addc_u32 s67, s62, s41
	s_cmpk_eq_i32 s40, 0x700
	s_cselect_b64 s[64:65], -1, 0
	s_and_b64 s[42:43], s[64:65], exec
	s_cselect_b32 s45, s87, s45
	s_cselect_b32 s44, s86, s44
	s_cselect_b32 s42, s31, s66
	s_cselect_b32 s43, s29, s67
	s_and_b64 vcc, s[6:7], s[64:65]
	v_lshl_add_u64 v[226:227], v[148:149], 0, s[40:41]
	s_add_i32 m0, s37, 0xc000
	ds_read_b128 v[198:201], v160
	ds_read_b128 v[202:205], v160 offset:1024
	ds_read_b128 v[206:209], v160 offset:2048
	ds_read_b128 v[210:213], v160 offset:3072
	ds_read_b128 v[214:217], v160 offset:4096
	ds_read_b128 v[218:221], v160 offset:5120
	ds_read_b128 v[222:225], v160 offset:6144
	ds_read_b128 v[230:233], v160 offset:7168
	global_load_lds_dwordx4 v[226:227], off
	v_lshl_add_u64 v[226:227], v[146:147], 0, s[40:41]
	s_add_i32 m0, s37, 0xe000
	s_nop 0
	global_load_lds_dwordx4 v[226:227], off
	s_waitcnt vmcnt(8)
	s_waitcnt lgkmcnt(0)
	s_barrier
; #define PG8_STAGE_A(b, h, ptr, NX) do { if constexpr (Sched::GATHER) { unsigned gs_[2]; gs_[0] = ((NX) && last_) ? gN[h][0] : gA[h][0]; gs_[1] = ((NX) && last_) ? gN[h][1] : gA[h][1]; PG8_STAGE(PG8_SA(b, h), ptr, gs_); } \
;         else PG8_STAGE(PG8_SA(b, h), (ptr) + ((h) ? hstep : (size_t)0), voffA); } while (0)
; #define PG8_STAGE(bufoff, gbase, voff) do { _Pragma("unroll") for (int _i = 0; _i < 2; ++_i) \
;         __builtin_amdgcn_global_load_lds((const unsigned*)((const char*)(gbase) + (voff)[_i]), (PG8_LAS unsigned*)(lds + (bufoff) + ldsw + _i * 8192), 16, 0, 0); } while (0)
; #define PG8_LDA(dst, b, h) do { _Pragma("unroll") for (int m = 0; m < 4; ++m) _Pragma("unroll") for (int k = 0; k < 2; ++k) dst[m][k] = *(const PG8_LAS bf16x8*)(lds + PG8_SA(b, h) + aoff + m * 2048 + k * 1024); } while (0)
; #define PG8_LDB(dst, b, h) do { _Pragma("unroll") for (int n = 0; n < 2; ++n) _Pragma("unroll") for (int k = 0; k < 2; ++k) dst[n][k] = *(const PG8_LAS bf16x8*)(lds + PG8_SB(b, h) + boff + n * 2048 + k * 1024); } while (0)
; #define PG8_MMA(ai, bj, At, Bt) do { __builtin_amdgcn_s_setprio(1); _Pragma("unroll") for (int m = 0; m < 4; ++m) _Pragma("unroll") for (int n = 0; n < 2; ++n) _Pragma("unroll") for (int k = 0; k < 2; ++k) \
;         acc[ai][bj][m][n] = __builtin_amdgcn_mfma_f32_16x16x32_bf16(Bt[n][k], At[m][k], acc[ai][bj][m][n], 0, 0, 0); __builtin_amdgcn_s_setprio(0); } while (0)
; #define PG8_WAIT_V(n) asm volatile("s_waitcnt vmcnt(" #n ")" ::: "memory")
; #define PG8_WAIT_L(n) asm volatile("s_waitcnt lgkmcnt(" #n ")" ::: "memory")
; #define PG8_BAR __builtin_amdgcn_s_barrier()
; #define PG8_SCHED __builtin_amdgcn_sched_barrier(0)
; template <class Epi, class Sched, bool ALIGN_EPI = false, bool SP2 = false>
; __device__ __forceinline__ void gemm_phase(PG8_LAS unsigned char* lds, const Gemm g, const Sched& S, const Epi& E, const bool skip_epi = false) {
;     ...
;             PG8_LDB(B0, 0, 0); PG8_LDB(B1, 0, 1); PG8_SCHED; PG8_LDA(At, 0, 0); PG8_STAGE_A(1, 1, a1, false);
;             PG8_WAIT_V(8); PG8_WAIT_L(0); PG8_BAR; PG8_MMA(0, 0, At, B0); PG8_MMA(0, 1, At, B1); PG8_BAR; PG8_SCHED;
;             PG8_LDA(At, 0, 1); PG8_STAGE(PG8_SB(0, 0), b2, voffB); PG8_STAGE(PG8_SB(0, 1), b2 + hstep, voffB); PG8_STAGE_A(0, 0, a2, true);
;             PG8_WAIT_V(8); PG8_WAIT_L(0); PG8_BAR; PG8_MMA(1, 0, At, B0); PG8_MMA(1, 1, At, B1); PG8_BAR; PG8_SCHED;
	s_setprio 1
	s_waitcnt lgkmcnt(0)
	v_mfma_f32_16x16x32_bf16 v[126:129], v[166:169], v[198:201], v[126:129]
	v_mfma_f32_16x16x32_bf16 v[122:125], v[174:177], v[198:201], v[122:125]
	v_mfma_f32_16x16x32_bf16 v[110:113], v[166:169], v[206:209], v[110:113]
	v_mfma_f32_16x16x32_bf16 v[106:109], v[174:177], v[206:209], v[106:109]
	v_mfma_f32_16x16x32_bf16 v[94:97], v[166:169], v[214:217], v[94:97]
	v_mfma_f32_16x16x32_bf16 v[90:93], v[174:177], v[214:217], v[90:93]
	v_mfma_f32_16x16x32_bf16 v[78:81], v[166:169], v[222:225], v[78:81]
	v_mfma_f32_16x16x32_bf16 v[74:77], v[174:177], v[222:225], v[74:77]
	v_mfma_f32_16x16x32_bf16 v[126:129], v[170:173], v[202:205], v[126:129]
	v_mfma_f32_16x16x32_bf16 v[122:125], v[178:181], v[202:205], v[122:125]
	v_mfma_f32_16x16x32_bf16 v[110:113], v[170:173], v[210:213], v[110:113]
	v_mfma_f32_16x16x32_bf16 v[106:109], v[178:181], v[210:213], v[106:109]
	v_mfma_f32_16x16x32_bf16 v[94:97], v[170:173], v[218:221], v[94:97]
	v_mfma_f32_16x16x32_bf16 v[90:93], v[178:181], v[218:221], v[90:93]
	v_mfma_f32_16x16x32_bf16 v[78:81], v[170:173], v[230:233], v[78:81]
	v_mfma_f32_16x16x32_bf16 v[74:77], v[178:181], v[230:233], v[74:77]
	s_setprio 0
	s_setprio 1
	v_mfma_f32_16x16x32_bf16 v[118:121], v[182:185], v[198:201], v[118:121]
	v_mfma_f32_16x16x32_bf16 v[114:117], v[190:193], v[198:201], v[114:117]
	v_mfma_f32_16x16x32_bf16 v[102:105], v[182:185], v[206:209], v[102:105]
	v_mfma_f32_16x16x32_bf16 v[98:101], v[190:193], v[206:209], v[98:101]
	v_mfma_f32_16x16x32_bf16 v[86:89], v[182:185], v[214:217], v[86:89]
	v_mfma_f32_16x16x32_bf16 v[82:85], v[190:193], v[214:217], v[82:85]
	v_mfma_f32_16x16x32_bf16 v[70:73], v[182:185], v[222:225], v[70:73]
	v_mfma_f32_16x16x32_bf16 v[66:69], v[190:193], v[222:225], v[66:69]
	v_mfma_f32_16x16x32_bf16 v[118:121], v[186:189], v[202:205], v[118:121]
	v_mfma_f32_16x16x32_bf16 v[114:117], v[194:197], v[202:205], v[114:117]
	v_mfma_f32_16x16x32_bf16 v[102:105], v[186:189], v[210:213], v[102:105]
	v_mfma_f32_16x16x32_bf16 v[98:101], v[194:197], v[210:213], v[98:101]
	v_mfma_f32_16x16x32_bf16 v[86:89], v[186:189], v[218:221], v[86:89]
	v_mfma_f32_16x16x32_bf16 v[82:85], v[194:197], v[218:221], v[82:85]
	v_mfma_f32_16x16x32_bf16 v[70:73], v[186:189], v[230:233], v[70:73]
	v_mfma_f32_16x16x32_bf16 v[66:69], v[194:197], v[230:233], v[66:69]
	s_setprio 0
	s_barrier
	s_add_i32 s64, s58, s50
	v_lshl_add_u64 v[226:227], s[42:43], 0, v[134:135]
	s_mov_b32 m0, s64
	ds_read_b128 v[198:201], v160 offset:16384
	ds_read_b128 v[202:205], v160 offset:17408
	ds_read_b128 v[206:209], v160 offset:18432
	ds_read_b128 v[210:213], v160 offset:19456
	ds_read_b128 v[214:217], v160 offset:20480
	ds_read_b128 v[218:221], v160 offset:21504
	ds_read_b128 v[222:225], v160 offset:22528
	ds_read_b128 v[230:233], v160 offset:23552
	global_load_lds_dwordx4 v[226:227], off
	s_add_i32 m0, s64, 0x2000
	s_add_u32 s64, s42, 0x40000
	v_lshl_add_u64 v[234:235], s[42:43], 0, v[136:137]
	s_addc_u32 s65, s43, 0
	s_add_i32 s66, s59, s50
	global_load_lds_dwordx4 v[234:235], off
	v_lshl_add_u64 v[236:237], s[64:65], 0, v[134:135]
	s_mov_b32 m0, s66
	v_cndmask_b32_e32 v132, v130, v164, vcc
	global_load_lds_dwordx4 v[236:237], off
	v_lshl_add_u64 v[236:237], s[64:65], 0, v[136:137]
	s_add_i32 m0, s66, 0x2000
	v_lshl_add_u64 v[238:239], s[44:45], 0, v[132:133]
	global_load_lds_dwordx4 v[236:237], off
	s_mov_b32 m0, s37
	v_cndmask_b32_e32 v236, v144, v163, vcc
	global_load_lds_dwordx4 v132, s[44:45]
	s_mov_b32 m0, s39
	v_mov_b32_e32 v237, v133
	global_load_lds_dwordx4 v236, s[44:45]
	s_waitcnt vmcnt(8)
	s_waitcnt lgkmcnt(0)
	v_lshl_add_u64 v[236:237], s[44:45], 0, v[236:237]
	s_barrier
	s_setprio 1
	s_waitcnt lgkmcnt(0)
	v_mfma_f32_16x16x32_bf16 v[62:65], v[166:169], v[198:201], v[62:65]
	v_mfma_f32_16x16x32_bf16 v[58:61], v[174:177], v[198:201], v[58:61]
	v_mfma_f32_16x16x32_bf16 v[38:41], v[166:169], v[206:209], v[38:41]
	v_mfma_f32_16x16x32_bf16 v[34:37], v[174:177], v[206:209], v[34:37]
	v_mfma_f32_16x16x32_bf16 v[22:25], v[166:169], v[214:217], v[22:25]
	v_mfma_f32_16x16x32_bf16 v[18:21], v[174:177], v[214:217], v[18:21]
	v_mfma_f32_16x16x32_bf16 v[6:9], v[166:169], v[222:225], v[6:9]
	v_mfma_f32_16x16x32_bf16 v[2:5], v[174:177], v[222:225], v[2:5]
	v_mfma_f32_16x16x32_bf16 v[62:65], v[170:173], v[202:205], v[62:65]
	v_mfma_f32_16x16x32_bf16 v[58:61], v[178:181], v[202:205], v[58:61]
	v_mfma_f32_16x16x32_bf16 v[38:41], v[170:173], v[210:213], v[38:41]
	v_mfma_f32_16x16x32_bf16 v[34:37], v[178:181], v[210:213], v[34:37]
	v_mfma_f32_16x16x32_bf16 v[22:25], v[170:173], v[218:221], v[22:25]
	v_mfma_f32_16x16x32_bf16 v[18:21], v[178:181], v[218:221], v[18:21]
	v_mfma_f32_16x16x32_bf16 v[6:9], v[170:173], v[230:233], v[6:9]
	v_mfma_f32_16x16x32_bf16 v[2:5], v[178:181], v[230:233], v[2:5]
	s_setprio 0
	s_setprio 1
	v_mfma_f32_16x16x32_bf16 v[50:53], v[182:185], v[198:201], v[50:53]
	v_mfma_f32_16x16x32_bf16 v[42:45], v[190:193], v[198:201], v[42:45]
	v_mfma_f32_16x16x32_bf16 v[54:57], v[182:185], v[206:209], v[54:57]
	v_mfma_f32_16x16x32_bf16 v[46:49], v[190:193], v[206:209], v[46:49]
	v_mfma_f32_16x16x32_bf16 v[30:33], v[182:185], v[214:217], v[30:33]
	v_mfma_f32_16x16x32_bf16 v[26:29], v[190:193], v[214:217], v[26:29]
	v_mfma_f32_16x16x32_bf16 v[14:17], v[182:185], v[222:225], v[14:17]
	v_mfma_f32_16x16x32_bf16 v[10:13], v[190:193], v[222:225], v[10:13]
	v_mfma_f32_16x16x32_bf16 v[50:53], v[186:189], v[202:205], v[50:53]
	v_mfma_f32_16x16x32_bf16 v[42:45], v[194:197], v[202:205], v[42:45]
	v_mfma_f32_16x16x32_bf16 v[54:57], v[186:189], v[210:213], v[54:57]
	v_mfma_f32_16x16x32_bf16 v[46:49], v[194:197], v[210:213], v[46:49]
	v_mfma_f32_16x16x32_bf16 v[30:33], v[186:189], v[218:221], v[30:33]
	v_mfma_f32_16x16x32_bf16 v[26:29], v[194:197], v[218:221], v[26:29]
	v_mfma_f32_16x16x32_bf16 v[14:17], v[186:189], v[230:233], v[14:17]
	v_mfma_f32_16x16x32_bf16 v[10:13], v[194:197], v[230:233], v[10:13]
	s_setprio 0
	s_barrier
; #define PG8_STAGE_A(b, h, ptr, NX) do { if constexpr (Sched::GATHER) { unsigned gs_[2]; gs_[0] = ((NX) && last_) ? gN[h][0] : gA[h][0]; gs_[1] = ((NX) && last_) ? gN[h][1] : gA[h][1]; PG8_STAGE(PG8_SA(b, h), ptr, gs_); } \
;         else PG8_STAGE(PG8_SA(b, h), (ptr) + ((h) ? hstep : (size_t)0), voffA); } while (0)
; #define PG8_LDA(dst, b, h) do { _Pragma("unroll") for (int m = 0; m < 4; ++m) _Pragma("unroll") for (int k = 0; k < 2; ++k) dst[m][k] = *(const PG8_LAS bf16x8*)(lds + PG8_SA(b, h) + aoff + m * 2048 + k * 1024); } while (0)
; #define PG8_LDB(dst, b, h) do { _Pragma("unroll") for (int n = 0; n < 2; ++n) _Pragma("unroll") for (int k = 0; k < 2; ++k) dst[n][k] = *(const PG8_LAS bf16x8*)(lds + PG8_SB(b, h) + boff + n * 2048 + k * 1024); } while (0)
; #define PG8_MMA(ai, bj, At, Bt) do { __builtin_amdgcn_s_setprio(1); _Pragma("unroll") for (int m = 0; m < 4; ++m) _Pragma("unroll") for (int n = 0; n < 2; ++n) _Pragma("unroll") for (int k = 0; k < 2; ++k) \
;         acc[ai][bj][m][n] = __builtin_amdgcn_mfma_f32_16x16x32_bf16(Bt[n][k], At[m][k], acc[ai][bj][m][n], 0, 0, 0); __builtin_amdgcn_s_setprio(0); } while (0)
; #define PG8_WAIT_V(n) asm volatile("s_waitcnt vmcnt(" #n ")" ::: "memory")
; #define PG8_WAIT_L(n) asm volatile("s_waitcnt lgkmcnt(" #n ")" ::: "memory")
; #define PG8_BAR __builtin_amdgcn_s_barrier()
; #define PG8_SCHED __builtin_amdgcn_sched_barrier(0)
; template <class Epi, class Sched, bool ALIGN_EPI = false, bool SP2 = false>
; __device__ __forceinline__ void gemm_phase(PG8_LAS unsigned char* lds, const Gemm g, const Sched& S, const Epi& E, const bool skip_epi = false) {
;     ...
;             PG8_LDB(B0, 1, 0); PG8_LDB(B1, 1, 1); PG8_SCHED; PG8_LDA(At, 1, 0); PG8_STAGE_A(0, 1, a2, true);
;             PG8_WAIT_V(8); PG8_WAIT_L(0); PG8_BAR; PG8_MMA(0, 0, At, B0); PG8_MMA(0, 1, At, B1); PG8_BAR; PG8_SCHED;
	s_add_i32 s64, 0, 0x18000
	v_add_u32_e32 v132, s64, v154
	s_add_i32 s65, 0, 0x1c000
	ds_read_b128 v[166:169], v132
	ds_read_b128 v[170:173], v132 offset:1024
	ds_read_b128 v[174:177], v132 offset:2048
	ds_read_b128 v[178:181], v132 offset:3072
	v_add_u32_e32 v132, s65, v154
	ds_read_b128 v[182:185], v132
	ds_read_b128 v[186:189], v132 offset:1024
	ds_read_b128 v[190:193], v132 offset:2048
	ds_read_b128 v[194:197], v132 offset:3072
	s_mov_b32 m0, s51
	v_cndmask_b32_e32 v132, v142, v162, vcc
	ds_read_b128 v[198:201], v160 offset:32768
	ds_read_b128 v[202:205], v160 offset:33792
	ds_read_b128 v[206:209], v160 offset:34816
	ds_read_b128 v[210:213], v160 offset:35840
	ds_read_b128 v[214:217], v160 offset:36864
	ds_read_b128 v[218:221], v160 offset:37888
	ds_read_b128 v[222:225], v160 offset:38912
	ds_read_b128 v[230:233], v160 offset:39936
	v_cndmask_b32_e32 v141, v140, v161, vcc
	global_load_lds_dwordx4 v132, s[44:45]
	s_mov_b32 m0, s52
	s_nop 0
	global_load_lds_dwordx4 v141, s[44:45]
	s_waitcnt vmcnt(8)
	s_waitcnt lgkmcnt(0)
	s_barrier
	s_setprio 1
	s_waitcnt lgkmcnt(0)
	v_mfma_f32_16x16x32_bf16 v[126:129], v[166:169], v[198:201], v[126:129]
	v_mfma_f32_16x16x32_bf16 v[122:125], v[174:177], v[198:201], v[122:125]
	v_mfma_f32_16x16x32_bf16 v[110:113], v[166:169], v[206:209], v[110:113]
	v_mfma_f32_16x16x32_bf16 v[106:109], v[174:177], v[206:209], v[106:109]
	v_mfma_f32_16x16x32_bf16 v[94:97], v[166:169], v[214:217], v[94:97]
	v_mfma_f32_16x16x32_bf16 v[90:93], v[174:177], v[214:217], v[90:93]
	v_mfma_f32_16x16x32_bf16 v[78:81], v[166:169], v[222:225], v[78:81]
	v_mfma_f32_16x16x32_bf16 v[74:77], v[174:177], v[222:225], v[74:77]
	v_mfma_f32_16x16x32_bf16 v[126:129], v[170:173], v[202:205], v[126:129]
	v_mfma_f32_16x16x32_bf16 v[122:125], v[178:181], v[202:205], v[122:125]
	v_mfma_f32_16x16x32_bf16 v[110:113], v[170:173], v[210:213], v[110:113]
	v_mfma_f32_16x16x32_bf16 v[106:109], v[178:181], v[210:213], v[106:109]
	v_mfma_f32_16x16x32_bf16 v[94:97], v[170:173], v[218:221], v[94:97]
	v_mfma_f32_16x16x32_bf16 v[90:93], v[178:181], v[218:221], v[90:93]
	v_mfma_f32_16x16x32_bf16 v[78:81], v[170:173], v[230:233], v[78:81]
	v_mfma_f32_16x16x32_bf16 v[74:77], v[178:181], v[230:233], v[74:77]
	s_setprio 0
	s_setprio 1
	v_mfma_f32_16x16x32_bf16 v[118:121], v[182:185], v[198:201], v[118:121]
	v_mfma_f32_16x16x32_bf16 v[114:117], v[190:193], v[198:201], v[114:117]
	v_mfma_f32_16x16x32_bf16 v[102:105], v[182:185], v[206:209], v[102:105]
	v_mfma_f32_16x16x32_bf16 v[98:101], v[190:193], v[206:209], v[98:101]
	v_mfma_f32_16x16x32_bf16 v[86:89], v[182:185], v[214:217], v[86:89]
	v_mfma_f32_16x16x32_bf16 v[82:85], v[190:193], v[214:217], v[82:85]
	v_mfma_f32_16x16x32_bf16 v[70:73], v[182:185], v[222:225], v[70:73]
	v_mfma_f32_16x16x32_bf16 v[66:69], v[190:193], v[222:225], v[66:69]
	v_mfma_f32_16x16x32_bf16 v[118:121], v[186:189], v[202:205], v[118:121]
	v_mfma_f32_16x16x32_bf16 v[114:117], v[194:197], v[202:205], v[114:117]
	v_mfma_f32_16x16x32_bf16 v[102:105], v[186:189], v[210:213], v[102:105]
	v_mfma_f32_16x16x32_bf16 v[98:101], v[194:197], v[210:213], v[98:101]
	v_mfma_f32_16x16x32_bf16 v[86:89], v[186:189], v[218:221], v[86:89]
	v_mfma_f32_16x16x32_bf16 v[82:85], v[194:197], v[218:221], v[82:85]
	v_mfma_f32_16x16x32_bf16 v[70:73], v[186:189], v[230:233], v[70:73]
	v_mfma_f32_16x16x32_bf16 v[66:69], v[194:197], v[230:233], v[66:69]
	s_setprio 0
	s_barrier
; #define PG8_STAGE_A(b, h, ptr, NX) do { if constexpr (Sched::GATHER) { unsigned gs_[2]; gs_[0] = ((NX) && last_) ? gN[h][0] : gA[h][0]; gs_[1] = ((NX) && last_) ? gN[h][1] : gA[h][1]; PG8_STAGE(PG8_SA(b, h), ptr, gs_); } \
;         else PG8_STAGE(PG8_SA(b, h), (ptr) + ((h) ? hstep : (size_t)0), voffA); } while (0)
; #define PG8_STAGE(bufoff, gbase, voff) do { _Pragma("unroll") for (int _i = 0; _i < 2; ++_i) \
;         __builtin_amdgcn_global_load_lds((const unsigned*)((const char*)(gbase) + (voff)[_i]), (PG8_LAS unsigned*)(lds + (bufoff) + ldsw + _i * 8192), 16, 0, 0); } while (0)
; #define PG8_LDA(dst, b, h) do { _Pragma("unroll") for (int m = 0; m < 4; ++m) _Pragma("unroll") for (int k = 0; k < 2; ++k) dst[m][k] = *(const PG8_LAS bf16x8*)(lds + PG8_SA(b, h) + aoff + m * 2048 + k * 1024); } while (0)
; #define PG8_MMA(ai, bj, At, Bt) do { __builtin_amdgcn_s_setprio(1); _Pragma("unroll") for (int m = 0; m < 4; ++m) _Pragma("unroll") for (int n = 0; n < 2; ++n) _Pragma("unroll") for (int k = 0; k < 2; ++k) \
;         acc[ai][bj][m][n] = __builtin_amdgcn_mfma_f32_16x16x32_bf16(Bt[n][k], At[m][k], acc[ai][bj][m][n], 0, 0, 0); __builtin_amdgcn_s_setprio(0); } while (0)
; #define PG8_WAIT_V(n) asm volatile("s_waitcnt vmcnt(" #n ")" ::: "memory")
; #define PG8_WAIT_L(n) asm volatile("s_waitcnt lgkmcnt(" #n ")" ::: "memory")
; #define PG8_BAR __builtin_amdgcn_s_barrier()
; #define PG8_SCHED __builtin_amdgcn_sched_barrier(0)
; template <class Epi, class Sched, bool ALIGN_EPI = false, bool SP2 = false>
; __device__ __forceinline__ void gemm_phase(PG8_LAS unsigned char* lds, const Gemm g, const Sched& S, const Epi& E, const bool skip_epi = false) {
;     ...
;         for (int t = 0; t < nt; t += 2) {
;             const bool last = (t == nt - 2); last_ = last && has_next;
;     ...
;             PG8_LDA(At, 1, 1); PG8_STAGE(PG8_SB(1, 0), b3, voffB); PG8_STAGE(PG8_SB(1, 1), b3 + hstep, voffB); PG8_STAGE_A(1, 0, a3, true);
;             PG8_WAIT_V(8); PG8_WAIT_L(0); PG8_BAR; PG8_MMA(1, 0, At, B0); PG8_MMA(1, 1, At, B1); PG8_BAR; PG8_SCHED;
	s_add_i32 s44, s64, s50
	v_lshl_add_u64 v[226:227], v[226:227], 0, s[22:23]
	s_mov_b32 m0, s44
	ds_read_b128 v[198:201], v160 offset:49152
	ds_read_b128 v[202:205], v160 offset:50176
	ds_read_b128 v[206:209], v160 offset:51200
	ds_read_b128 v[210:213], v160 offset:52224
	ds_read_b128 v[214:217], v160 offset:53248
	ds_read_b128 v[218:221], v160 offset:54272
	ds_read_b128 v[222:225], v160 offset:55296
	ds_read_b128 v[230:233], v160 offset:56320
	global_load_lds_dwordx4 v[226:227], off
	s_add_i32 m0, s44, 0x2000
	s_add_u32 s42, s42, 0x40080
	v_lshl_add_u64 v[226:227], v[234:235], 0, s[22:23]
	s_addc_u32 s43, s43, 0
	s_add_i32 s44, s65, s50
	global_load_lds_dwordx4 v[226:227], off
	v_lshl_add_u64 v[226:227], s[42:43], 0, v[134:135]
	s_mov_b32 m0, s44
	s_nop 0
	global_load_lds_dwordx4 v[226:227], off
	v_lshl_add_u64 v[226:227], s[42:43], 0, v[136:137]
	s_add_i32 m0, s44, 0x2000
	s_nop 0
	global_load_lds_dwordx4 v[226:227], off
	v_lshl_add_u64 v[226:227], v[238:239], 0, s[22:23]
	s_mov_b32 m0, s55
	s_nop 0
	global_load_lds_dwordx4 v[226:227], off
	v_lshl_add_u64 v[226:227], v[236:237], 0, s[22:23]
	s_mov_b32 m0, s56
	s_nop 0
	global_load_lds_dwordx4 v[226:227], off
	s_waitcnt vmcnt(8)
	s_waitcnt lgkmcnt(0)
	s_barrier
	s_setprio 1
	s_waitcnt lgkmcnt(0)
	v_mfma_f32_16x16x32_bf16 v[62:65], v[166:169], v[198:201], v[62:65]
	v_mfma_f32_16x16x32_bf16 v[58:61], v[174:177], v[198:201], v[58:61]
	v_mfma_f32_16x16x32_bf16 v[38:41], v[166:169], v[206:209], v[38:41]
	v_mfma_f32_16x16x32_bf16 v[34:37], v[174:177], v[206:209], v[34:37]
	v_mfma_f32_16x16x32_bf16 v[22:25], v[166:169], v[214:217], v[22:25]
	v_mfma_f32_16x16x32_bf16 v[18:21], v[174:177], v[214:217], v[18:21]
	v_mfma_f32_16x16x32_bf16 v[6:9], v[166:169], v[222:225], v[6:9]
	v_mfma_f32_16x16x32_bf16 v[2:5], v[174:177], v[222:225], v[2:5]
	v_mfma_f32_16x16x32_bf16 v[62:65], v[170:173], v[202:205], v[62:65]
	v_mfma_f32_16x16x32_bf16 v[58:61], v[178:181], v[202:205], v[58:61]
	v_mfma_f32_16x16x32_bf16 v[38:41], v[170:173], v[210:213], v[38:41]
	v_mfma_f32_16x16x32_bf16 v[34:37], v[178:181], v[210:213], v[34:37]
	v_mfma_f32_16x16x32_bf16 v[22:25], v[170:173], v[218:221], v[22:25]
	v_mfma_f32_16x16x32_bf16 v[18:21], v[178:181], v[218:221], v[18:21]
	v_mfma_f32_16x16x32_bf16 v[6:9], v[170:173], v[230:233], v[6:9]
	v_mfma_f32_16x16x32_bf16 v[2:5], v[178:181], v[230:233], v[2:5]
	s_setprio 0
	s_setprio 1
	v_mfma_f32_16x16x32_bf16 v[50:53], v[182:185], v[198:201], v[50:53]
	v_mfma_f32_16x16x32_bf16 v[42:45], v[190:193], v[198:201], v[42:45]
	v_mfma_f32_16x16x32_bf16 v[54:57], v[182:185], v[206:209], v[54:57]
	v_mfma_f32_16x16x32_bf16 v[46:49], v[190:193], v[206:209], v[46:49]
	v_mfma_f32_16x16x32_bf16 v[30:33], v[182:185], v[214:217], v[30:33]
	v_mfma_f32_16x16x32_bf16 v[26:29], v[190:193], v[214:217], v[26:29]
	v_mfma_f32_16x16x32_bf16 v[14:17], v[182:185], v[222:225], v[14:17]
	v_mfma_f32_16x16x32_bf16 v[10:13], v[190:193], v[222:225], v[10:13]
	v_mfma_f32_16x16x32_bf16 v[50:53], v[186:189], v[202:205], v[50:53]
	v_mfma_f32_16x16x32_bf16 v[42:45], v[194:197], v[202:205], v[42:45]
	v_mfma_f32_16x16x32_bf16 v[54:57], v[186:189], v[210:213], v[54:57]
	v_mfma_f32_16x16x32_bf16 v[46:49], v[194:197], v[210:213], v[46:49]
	v_mfma_f32_16x16x32_bf16 v[30:33], v[186:189], v[218:221], v[30:33]
	v_mfma_f32_16x16x32_bf16 v[26:29], v[194:197], v[218:221], v[26:29]
	v_mfma_f32_16x16x32_bf16 v[14:17], v[186:189], v[230:233], v[14:17]
	v_mfma_f32_16x16x32_bf16 v[10:13], v[194:197], v[230:233], v[10:13]
	s_setprio 0
	s_barrier
	s_add_i32 s63, s63, 2
	s_add_u32 s40, s40, 0x100
	s_addc_u32 s41, s41, 0
	s_cmp_gt_u32 s63, 13
	s_cbranch_scc0 .LBB0_1728
	s_and_b64 vcc, exec, s[26:27]
	s_cbranch_vccz .LBB0_1731
	s_barrier

; #define PG8_STAGE_A(b, h, ptr, NX) do { if constexpr (Sched::GATHER) { unsigned gs_[2]; gs_[0] = ((NX) && last_) ? gN[h][0] : gA[h][0]; gs_[1] = ((NX) && last_) ? gN[h][1] : gA[h][1]; PG8_STAGE(PG8_SA(b, h), ptr, gs_); } \
;         else PG8_STAGE(PG8_SA(b, h), (ptr) + ((h) ? hstep : (size_t)0), voffA); } while (0)
; #define PG8_STAGE(bufoff, gbase, voff) do { _Pragma("unroll") for (int _i = 0; _i < 2; ++_i) \
;         __builtin_amdgcn_global_load_lds((const unsigned*)((const char*)(gbase) + (voff)[_i]), (PG8_LAS unsigned*)(lds + (bufoff) + ldsw + _i * 8192), 16, 0, 0); } while (0)
; #define PG8_LDA(dst, b, h) do { _Pragma("unroll") for (int m = 0; m < 4; ++m) _Pragma("unroll") for (int k = 0; k < 2; ++k) dst[m][k] = *(const PG8_LAS bf16x8*)(lds + PG8_SA(b, h) + aoff + m * 2048 + k * 1024); } while (0)
; #define PG8_LDB(dst, b, h) do { _Pragma("unroll") for (int n = 0; n < 2; ++n) _Pragma("unroll") for (int k = 0; k < 2; ++k) dst[n][k] = *(const PG8_LAS bf16x8*)(lds + PG8_SB(b, h) + boff + n * 2048 + k * 1024); } while (0)
; #define PG8_MMA(ai, bj, At, Bt) do { __builtin_amdgcn_s_setprio(1); _Pragma("unroll") for (int m = 0; m < 4; ++m) _Pragma("unroll") for (int n = 0; n < 2; ++n) _Pragma("unroll") for (int k = 0; k < 2; ++k) \
;         acc[ai][bj][m][n] = __builtin_amdgcn_mfma_f32_16x16x32_bf16(Bt[n][k], At[m][k], acc[ai][bj][m][n], 0, 0, 0); __builtin_amdgcn_s_setprio(0); } while (0)
; #define PG8_WAIT_V(n) asm volatile("s_waitcnt vmcnt(" #n ")" ::: "memory")
; #define PG8_WAIT_L(n) asm volatile("s_waitcnt lgkmcnt(" #n ")" ::: "memory")
; #define PG8_BAR __builtin_amdgcn_s_barrier()
; #define PG8_SCHED __builtin_amdgcn_sched_barrier(0)
; template <class Epi, class Sched, bool ALIGN_EPI = false, bool SP2 = false>
; __device__ __forceinline__ void gemm_phase(PG8_LAS unsigned char* lds, const Gemm g, const Sched& S, const Epi& E, const bool skip_epi = false) {
;     ...
;             PG8_LDB(B0, 0, 0); PG8_LDB(B1, 0, 1); PG8_SCHED; PG8_LDA(At, 0, 0); PG8_STAGE_A(1, 1, a1, false);
;             PG8_WAIT_V(8); PG8_WAIT_L(0); PG8_BAR; PG8_MMA(0, 0, At, B0); PG8_MMA(0, 1, At, B1); PG8_BAR; PG8_SCHED;
;             PG8_LDA(At, 0, 1); PG8_STAGE(PG8_SB(0, 0), b2, voffB); PG8_STAGE(PG8_SB(0, 1), b2 + hstep, voffB); PG8_STAGE_A(0, 0, a2, true);
.LBB0_1822:
	s_add_u32 s67, s40, 0x100
	s_addc_u32 s68, s41, 0
	s_mov_b32 s69, -2
	ds_read_b128 v[160:163], v157
	ds_read_b128 v[164:167], v157 offset:1024
	ds_read_b128 v[168:171], v157 offset:2048
	ds_read_b128 v[172:175], v157 offset:3072
	ds_read_b128 v[176:179], v158
	ds_read_b128 v[180:183], v158 offset:1024
	ds_read_b128 v[184:187], v158 offset:2048
	ds_read_b128 v[188:191], v158 offset:3072
	s_add_u32 s40, s38, 0x100
	s_addc_u32 s41, s39, 0
	s_cmp_eq_u32 s69, 52
	s_cselect_b32 s45, s7, s41
	s_cselect_b32 s44, s6, s40
	s_cselect_b32 s43, s35, s68
	s_cselect_b32 s42, s34, s67
	v_lshl_add_u64 v[152:153], s[38:39], 0, v[140:141]
	s_add_i32 m0, s37, 0xc000
	ds_read_b128 v[192:195], v159
	ds_read_b128 v[196:199], v159 offset:1024
	ds_read_b128 v[200:203], v159 offset:2048
	ds_read_b128 v[204:207], v159 offset:3072
	ds_read_b128 v[208:211], v159 offset:4096
	ds_read_b128 v[212:215], v159 offset:5120
	ds_read_b128 v[216:219], v159 offset:6144
	ds_read_b128 v[220:223], v159 offset:7168
	global_load_lds_dwordx4 v[152:153], off
	v_lshl_add_u64 v[152:153], s[38:39], 0, v[142:143]
	s_add_i32 m0, s37, 0xe000
	s_nop 0
	global_load_lds_dwordx4 v[152:153], off
	s_waitcnt vmcnt(8)
	s_waitcnt lgkmcnt(0)
	s_barrier
	s_setprio 1
	s_waitcnt lgkmcnt(0)
	v_mfma_f32_16x16x32_bf16 v[126:129], v[160:163], v[192:195], 0
	v_mfma_f32_16x16x32_bf16 v[122:125], v[168:171], v[192:195], 0
	v_mfma_f32_16x16x32_bf16 v[118:121], v[160:163], v[200:203], 0
	v_mfma_f32_16x16x32_bf16 v[114:117], v[168:171], v[200:203], 0
	v_mfma_f32_16x16x32_bf16 v[106:109], v[160:163], v[208:211], 0
	v_mfma_f32_16x16x32_bf16 v[98:101], v[168:171], v[208:211], 0
	v_mfma_f32_16x16x32_bf16 v[78:81], v[160:163], v[216:219], 0
	v_mfma_f32_16x16x32_bf16 v[74:77], v[168:171], v[216:219], 0
	v_mfma_f32_16x16x32_bf16 v[126:129], v[164:167], v[196:199], v[126:129]
	v_mfma_f32_16x16x32_bf16 v[122:125], v[172:175], v[196:199], v[122:125]
	v_mfma_f32_16x16x32_bf16 v[118:121], v[164:167], v[204:207], v[118:121]
	v_mfma_f32_16x16x32_bf16 v[114:117], v[172:175], v[204:207], v[114:117]
	v_mfma_f32_16x16x32_bf16 v[106:109], v[164:167], v[212:215], v[106:109]
	v_mfma_f32_16x16x32_bf16 v[98:101], v[172:175], v[212:215], v[98:101]
	v_mfma_f32_16x16x32_bf16 v[78:81], v[164:167], v[220:223], v[78:81]
	v_mfma_f32_16x16x32_bf16 v[74:77], v[172:175], v[220:223], v[74:77]
	s_setprio 0
	s_setprio 1
	v_mfma_f32_16x16x32_bf16 v[110:113], v[176:179], v[192:195], 0
	v_mfma_f32_16x16x32_bf16 v[102:105], v[184:187], v[192:195], 0
	v_mfma_f32_16x16x32_bf16 v[94:97], v[176:179], v[200:203], 0
	v_mfma_f32_16x16x32_bf16 v[90:93], v[184:187], v[200:203], 0
	v_mfma_f32_16x16x32_bf16 v[86:89], v[176:179], v[208:211], 0
	v_mfma_f32_16x16x32_bf16 v[82:85], v[184:187], v[208:211], 0
	v_mfma_f32_16x16x32_bf16 v[70:73], v[176:179], v[216:219], 0
	v_mfma_f32_16x16x32_bf16 v[66:69], v[184:187], v[216:219], 0
	v_mfma_f32_16x16x32_bf16 v[110:113], v[180:183], v[196:199], v[110:113]
	v_mfma_f32_16x16x32_bf16 v[102:105], v[188:191], v[196:199], v[102:105]
	v_mfma_f32_16x16x32_bf16 v[94:97], v[180:183], v[204:207], v[94:97]
	v_mfma_f32_16x16x32_bf16 v[90:93], v[188:191], v[204:207], v[90:93]
	v_mfma_f32_16x16x32_bf16 v[86:89], v[180:183], v[212:215], v[86:89]
	v_mfma_f32_16x16x32_bf16 v[82:85], v[188:191], v[212:215], v[82:85]
	v_mfma_f32_16x16x32_bf16 v[70:73], v[180:183], v[220:223], v[70:73]
	v_mfma_f32_16x16x32_bf16 v[66:69], v[188:191], v[220:223], v[66:69]
	s_setprio 0
	s_barrier
	s_add_i32 s38, s60, s51
	v_lshl_add_u64 v[152:153], s[42:43], 0, v[134:135]
	s_mov_b32 m0, s38
	ds_read_b128 v[192:195], v159 offset:16384
	ds_read_b128 v[196:199], v159 offset:17408
	ds_read_b128 v[200:203], v159 offset:18432
	ds_read_b128 v[204:207], v159 offset:19456
	ds_read_b128 v[208:211], v159 offset:20480
	ds_read_b128 v[212:215], v159 offset:21504
	ds_read_b128 v[216:219], v159 offset:22528
	ds_read_b128 v[220:223], v159 offset:23552
	global_load_lds_dwordx4 v[152:153], off
	s_add_i32 m0, s38, 0x2000
	s_add_u32 s38, s42, 0xe0000
	v_lshl_add_u64 v[224:225], s[42:43], 0, v[138:139]
	s_addc_u32 s39, s43, 0
	s_add_i32 s70, s61, s51
	global_load_lds_dwordx4 v[224:225], off
	v_lshl_add_u64 v[226:227], s[38:39], 0, v[134:135]
	s_mov_b32 m0, s70
	v_lshl_add_u64 v[230:231], s[44:45], 0, v[136:137]
	global_load_lds_dwordx4 v[226:227], off
	v_lshl_add_u64 v[226:227], s[38:39], 0, v[138:139]
	s_add_i32 m0, s70, 0x2000
	s_nop 0
	global_load_lds_dwordx4 v[226:227], off
	v_lshl_add_u64 v[226:227], s[44:45], 0, v[132:133]
	s_mov_b32 m0, s37
	s_nop 0
	global_load_lds_dwordx4 v[226:227], off
	s_mov_b32 m0, s52
	s_nop 0
	global_load_lds_dwordx4 v[230:231], off
	s_waitcnt vmcnt(8)
	s_waitcnt lgkmcnt(0)
	s_barrier
; #define PG8_STAGE_A(b, h, ptr, NX) do { if constexpr (Sched::GATHER) { unsigned gs_[2]; gs_[0] = ((NX) && last_) ? gN[h][0] : gA[h][0]; gs_[1] = ((NX) && last_) ? gN[h][1] : gA[h][1]; PG8_STAGE(PG8_SA(b, h), ptr, gs_); } \
;         else PG8_STAGE(PG8_SA(b, h), (ptr) + ((h) ? hstep : (size_t)0), voffA); } while (0)
; #define PG8_LDA(dst, b, h) do { _Pragma("unroll") for (int m = 0; m < 4; ++m) _Pragma("unroll") for (int k = 0; k < 2; ++k) dst[m][k] = *(const PG8_LAS bf16x8*)(lds + PG8_SA(b, h) + aoff + m * 2048 + k * 1024); } while (0)
; #define PG8_LDB(dst, b, h) do { _Pragma("unroll") for (int n = 0; n < 2; ++n) _Pragma("unroll") for (int k = 0; k < 2; ++k) dst[n][k] = *(const PG8_LAS bf16x8*)(lds + PG8_SB(b, h) + boff + n * 2048 + k * 1024); } while (0)
; #define PG8_MMA(ai, bj, At, Bt) do { __builtin_amdgcn_s_setprio(1); _Pragma("unroll") for (int m = 0; m < 4; ++m) _Pragma("unroll") for (int n = 0; n < 2; ++n) _Pragma("unroll") for (int k = 0; k < 2; ++k) \
;         acc[ai][bj][m][n] = __builtin_amdgcn_mfma_f32_16x16x32_bf16(Bt[n][k], At[m][k], acc[ai][bj][m][n], 0, 0, 0); __builtin_amdgcn_s_setprio(0); } while (0)
; #define PG8_WAIT_V(n) asm volatile("s_waitcnt vmcnt(" #n ")" ::: "memory")
; #define PG8_WAIT_L(n) asm volatile("s_waitcnt lgkmcnt(" #n ")" ::: "memory")
; #define PG8_BAR __builtin_amdgcn_s_barrier()
; #define PG8_SCHED __builtin_amdgcn_sched_barrier(0)
; template <class Epi, class Sched, bool ALIGN_EPI = false, bool SP2 = false>
; __device__ __forceinline__ void gemm_phase(PG8_LAS unsigned char* lds, const Gemm g, const Sched& S, const Epi& E, const bool skip_epi = false) {
;     ...
;             PG8_WAIT_V(8); PG8_WAIT_L(0); PG8_BAR; PG8_MMA(1, 0, At, B0); PG8_MMA(1, 1, At, B1); PG8_BAR; PG8_SCHED;
;             PG8_LDB(B0, 1, 0); PG8_LDB(B1, 1, 1); PG8_SCHED; PG8_LDA(At, 1, 0); PG8_STAGE_A(0, 1, a2, true);
;             PG8_WAIT_V(8); PG8_WAIT_L(0); PG8_BAR; PG8_MMA(0, 0, At, B0); PG8_MMA(0, 1, At, B1); PG8_BAR; PG8_SCHED;
	s_setprio 1
	s_waitcnt lgkmcnt(0)
	v_mfma_f32_16x16x32_bf16 v[62:65], v[160:163], v[192:195], 0
	v_mfma_f32_16x16x32_bf16 v[58:61], v[168:171], v[192:195], 0
	v_mfma_f32_16x16x32_bf16 v[50:53], v[160:163], v[200:203], 0
	v_mfma_f32_16x16x32_bf16 v[42:45], v[168:171], v[200:203], 0
	v_mfma_f32_16x16x32_bf16 v[34:37], v[160:163], v[208:211], 0
	v_mfma_f32_16x16x32_bf16 v[26:29], v[168:171], v[208:211], 0
	v_mfma_f32_16x16x32_bf16 v[18:21], v[160:163], v[216:219], 0
	v_mfma_f32_16x16x32_bf16 v[10:13], v[168:171], v[216:219], 0
	v_mfma_f32_16x16x32_bf16 v[62:65], v[164:167], v[196:199], v[62:65]
	v_mfma_f32_16x16x32_bf16 v[58:61], v[172:175], v[196:199], v[58:61]
	v_mfma_f32_16x16x32_bf16 v[50:53], v[164:167], v[204:207], v[50:53]
	v_mfma_f32_16x16x32_bf16 v[42:45], v[172:175], v[204:207], v[42:45]
	v_mfma_f32_16x16x32_bf16 v[34:37], v[164:167], v[212:215], v[34:37]
	v_mfma_f32_16x16x32_bf16 v[26:29], v[172:175], v[212:215], v[26:29]
	v_mfma_f32_16x16x32_bf16 v[18:21], v[164:167], v[220:223], v[18:21]
	v_mfma_f32_16x16x32_bf16 v[10:13], v[172:175], v[220:223], v[10:13]
	s_setprio 0
	s_setprio 1
	v_mfma_f32_16x16x32_bf16 v[54:57], v[176:179], v[192:195], 0
	v_mfma_f32_16x16x32_bf16 v[46:49], v[184:187], v[192:195], 0
	v_mfma_f32_16x16x32_bf16 v[38:41], v[176:179], v[200:203], 0
	v_mfma_f32_16x16x32_bf16 v[30:33], v[184:187], v[200:203], 0
	v_mfma_f32_16x16x32_bf16 v[22:25], v[176:179], v[208:211], 0
	v_mfma_f32_16x16x32_bf16 v[14:17], v[184:187], v[208:211], 0
	v_mfma_f32_16x16x32_bf16 v[6:9], v[176:179], v[216:219], 0
	v_mfma_f32_16x16x32_bf16 v[2:5], v[184:187], v[216:219], 0
	v_mfma_f32_16x16x32_bf16 v[54:57], v[180:183], v[196:199], v[54:57]
	v_mfma_f32_16x16x32_bf16 v[46:49], v[188:191], v[196:199], v[46:49]
	v_mfma_f32_16x16x32_bf16 v[38:41], v[180:183], v[204:207], v[38:41]
	v_mfma_f32_16x16x32_bf16 v[30:33], v[188:191], v[204:207], v[30:33]
	v_mfma_f32_16x16x32_bf16 v[22:25], v[180:183], v[212:215], v[22:25]
	v_mfma_f32_16x16x32_bf16 v[14:17], v[188:191], v[212:215], v[14:17]
	v_mfma_f32_16x16x32_bf16 v[6:9], v[180:183], v[220:223], v[6:9]
	v_mfma_f32_16x16x32_bf16 v[2:5], v[188:191], v[220:223], v[2:5]
	s_setprio 0
	s_barrier
	s_add_i32 s70, 0, 0x18000
	v_add_u32_e32 v130, s70, v147
	s_add_i32 s71, 0, 0x1c000
	ds_read_b128 v[160:163], v130
	ds_read_b128 v[164:167], v130 offset:1024
	ds_read_b128 v[168:171], v130 offset:2048
	ds_read_b128 v[172:175], v130 offset:3072
	v_add_u32_e32 v130, s71, v147
	ds_read_b128 v[176:179], v130
	ds_read_b128 v[180:183], v130 offset:1024
	ds_read_b128 v[184:187], v130 offset:2048
	ds_read_b128 v[188:191], v130 offset:3072
	s_add_u32 s38, s44, 0xe0000
	s_addc_u32 s39, s45, 0
	s_mov_b32 m0, s53
	v_lshl_add_u64 v[232:233], s[38:39], 0, v[132:133]
	ds_read_b128 v[192:195], v159 offset:32768
	ds_read_b128 v[196:199], v159 offset:33792
	ds_read_b128 v[200:203], v159 offset:34816
	ds_read_b128 v[204:207], v159 offset:35840
	ds_read_b128 v[208:211], v159 offset:36864
	ds_read_b128 v[212:215], v159 offset:37888
	ds_read_b128 v[216:219], v159 offset:38912
	ds_read_b128 v[220:223], v159 offset:39936
	global_load_lds_dwordx4 v[232:233], off
	v_lshl_add_u64 v[232:233], s[38:39], 0, v[136:137]
	s_mov_b32 m0, s54
	s_nop 0
	global_load_lds_dwordx4 v[232:233], off
	s_waitcnt vmcnt(8)
	s_waitcnt lgkmcnt(0)
	s_barrier
	s_setprio 1
	s_waitcnt lgkmcnt(0)
	v_mfma_f32_16x16x32_bf16 v[126:129], v[160:163], v[192:195], v[126:129]
	v_mfma_f32_16x16x32_bf16 v[122:125], v[168:171], v[192:195], v[122:125]
	v_mfma_f32_16x16x32_bf16 v[118:121], v[160:163], v[200:203], v[118:121]
	v_mfma_f32_16x16x32_bf16 v[114:117], v[168:171], v[200:203], v[114:117]
	v_mfma_f32_16x16x32_bf16 v[106:109], v[160:163], v[208:211], v[106:109]
	v_mfma_f32_16x16x32_bf16 v[98:101], v[168:171], v[208:211], v[98:101]
	v_mfma_f32_16x16x32_bf16 v[78:81], v[160:163], v[216:219], v[78:81]
	v_mfma_f32_16x16x32_bf16 v[74:77], v[168:171], v[216:219], v[74:77]
	v_mfma_f32_16x16x32_bf16 v[126:129], v[164:167], v[196:199], v[126:129]
	v_mfma_f32_16x16x32_bf16 v[122:125], v[172:175], v[196:199], v[122:125]
	v_mfma_f32_16x16x32_bf16 v[118:121], v[164:167], v[204:207], v[118:121]
	v_mfma_f32_16x16x32_bf16 v[114:117], v[172:175], v[204:207], v[114:117]
	v_mfma_f32_16x16x32_bf16 v[106:109], v[164:167], v[212:215], v[106:109]
	v_mfma_f32_16x16x32_bf16 v[98:101], v[172:175], v[212:215], v[98:101]
	v_mfma_f32_16x16x32_bf16 v[78:81], v[164:167], v[220:223], v[78:81]
	v_mfma_f32_16x16x32_bf16 v[74:77], v[172:175], v[220:223], v[74:77]
	s_setprio 0
	s_setprio 1
	v_mfma_f32_16x16x32_bf16 v[110:113], v[176:179], v[192:195], v[110:113]
	v_mfma_f32_16x16x32_bf16 v[102:105], v[184:187], v[192:195], v[102:105]
	v_mfma_f32_16x16x32_bf16 v[94:97], v[176:179], v[200:203], v[94:97]
	v_mfma_f32_16x16x32_bf16 v[90:93], v[184:187], v[200:203], v[90:93]
	v_mfma_f32_16x16x32_bf16 v[86:89], v[176:179], v[208:211], v[86:89]
	v_mfma_f32_16x16x32_bf16 v[82:85], v[184:187], v[208:211], v[82:85]
	v_mfma_f32_16x16x32_bf16 v[70:73], v[176:179], v[216:219], v[70:73]
	v_mfma_f32_16x16x32_bf16 v[66:69], v[184:187], v[216:219], v[66:69]
	v_mfma_f32_16x16x32_bf16 v[110:113], v[180:183], v[196:199], v[110:113]
	v_mfma_f32_16x16x32_bf16 v[102:105], v[188:191], v[196:199], v[102:105]
	v_mfma_f32_16x16x32_bf16 v[94:97], v[180:183], v[204:207], v[94:97]
	v_mfma_f32_16x16x32_bf16 v[90:93], v[188:191], v[204:207], v[90:93]
	v_mfma_f32_16x16x32_bf16 v[86:89], v[180:183], v[212:215], v[86:89]
	v_mfma_f32_16x16x32_bf16 v[82:85], v[188:191], v[212:215], v[82:85]
	v_mfma_f32_16x16x32_bf16 v[70:73], v[180:183], v[220:223], v[70:73]
	v_mfma_f32_16x16x32_bf16 v[66:69], v[188:191], v[220:223], v[66:69]
	s_setprio 0
	s_barrier
; #define PG8_STAGE_A(b, h, ptr, NX) do { if constexpr (Sched::GATHER) { unsigned gs_[2]; gs_[0] = ((NX) && last_) ? gN[h][0] : gA[h][0]; gs_[1] = ((NX) && last_) ? gN[h][1] : gA[h][1]; PG8_STAGE(PG8_SA(b, h), ptr, gs_); } \
;         else PG8_STAGE(PG8_SA(b, h), (ptr) + ((h) ? hstep : (size_t)0), voffA); } while (0)
; #define PG8_STAGE(bufoff, gbase, voff) do { _Pragma("unroll") for (int _i = 0; _i < 2; ++_i) \
;         __builtin_amdgcn_global_load_lds((const unsigned*)((const char*)(gbase) + (voff)[_i]), (PG8_LAS unsigned*)(lds + (bufoff) + ldsw + _i * 8192), 16, 0, 0); } while (0)
; #define PG8_LDA(dst, b, h) do { _Pragma("unroll") for (int m = 0; m < 4; ++m) _Pragma("unroll") for (int k = 0; k < 2; ++k) dst[m][k] = *(const PG8_LAS bf16x8*)(lds + PG8_SA(b, h) + aoff + m * 2048 + k * 1024); } while (0)
; #define PG8_MMA(ai, bj, At, Bt) do { __builtin_amdgcn_s_setprio(1); _Pragma("unroll") for (int m = 0; m < 4; ++m) _Pragma("unroll") for (int n = 0; n < 2; ++n) _Pragma("unroll") for (int k = 0; k < 2; ++k) \
;         acc[ai][bj][m][n] = __builtin_amdgcn_mfma_f32_16x16x32_bf16(Bt[n][k], At[m][k], acc[ai][bj][m][n], 0, 0, 0); __builtin_amdgcn_s_setprio(0); } while (0)
; #define PG8_WAIT_V(n) asm volatile("s_waitcnt vmcnt(" #n ")" ::: "memory")
; #define PG8_WAIT_L(n) asm volatile("s_waitcnt lgkmcnt(" #n ")" ::: "memory")
; #define PG8_BAR __builtin_amdgcn_s_barrier()
; #define PG8_SCHED __builtin_amdgcn_sched_barrier(0)
; template <class Epi, class Sched, bool ALIGN_EPI = false, bool SP2 = false>
; __device__ __forceinline__ void gemm_phase(PG8_LAS unsigned char* lds, const Gemm g, const Sched& S, const Epi& E, const bool skip_epi = false) {
;     ...
;             PG8_LDA(At, 1, 1); PG8_STAGE(PG8_SB(1, 0), b3, voffB); PG8_STAGE(PG8_SB(1, 1), b3 + hstep, voffB); PG8_STAGE_A(1, 0, a3, true);
;             PG8_WAIT_V(8); PG8_WAIT_L(0); PG8_BAR; PG8_MMA(1, 0, At, B0); PG8_MMA(1, 1, At, B1); PG8_BAR; PG8_SCHED;
	s_add_i32 s38, s70, s51
	v_lshl_add_u64 v[152:153], v[152:153], 0, s[18:19]
	s_mov_b32 m0, s38
	ds_read_b128 v[192:195], v159 offset:49152
	ds_read_b128 v[196:199], v159 offset:50176
	ds_read_b128 v[200:203], v159 offset:51200
	ds_read_b128 v[204:207], v159 offset:52224
	ds_read_b128 v[208:211], v159 offset:53248
	ds_read_b128 v[212:215], v159 offset:54272
	ds_read_b128 v[216:219], v159 offset:55296
	ds_read_b128 v[220:223], v159 offset:56320
	global_load_lds_dwordx4 v[152:153], off
	s_add_i32 m0, s38, 0x2000
	s_add_u32 s38, s42, 0xe0080
	v_lshl_add_u64 v[152:153], v[224:225], 0, s[18:19]
	s_addc_u32 s39, s43, 0
	s_add_i32 s42, s71, s51
	global_load_lds_dwordx4 v[152:153], off
	v_lshl_add_u64 v[152:153], s[38:39], 0, v[134:135]
	s_mov_b32 m0, s42
	s_nop 0
	global_load_lds_dwordx4 v[152:153], off
	v_lshl_add_u64 v[152:153], s[38:39], 0, v[138:139]
	s_add_i32 m0, s42, 0x2000
	s_nop 0
	global_load_lds_dwordx4 v[152:153], off
	v_lshl_add_u64 v[152:153], v[226:227], 0, s[18:19]
	s_mov_b32 m0, s57
	s_nop 0
	global_load_lds_dwordx4 v[152:153], off
	v_lshl_add_u64 v[152:153], v[230:231], 0, s[18:19]
	s_mov_b32 m0, s58
	s_nop 0
	global_load_lds_dwordx4 v[152:153], off
	s_waitcnt vmcnt(8)
	s_waitcnt lgkmcnt(0)
	s_barrier
	s_setprio 1
	s_waitcnt lgkmcnt(0)
	v_mfma_f32_16x16x32_bf16 v[62:65], v[160:163], v[192:195], v[62:65]
	v_mfma_f32_16x16x32_bf16 v[58:61], v[168:171], v[192:195], v[58:61]
	v_mfma_f32_16x16x32_bf16 v[50:53], v[160:163], v[200:203], v[50:53]
	v_mfma_f32_16x16x32_bf16 v[42:45], v[168:171], v[200:203], v[42:45]
	v_mfma_f32_16x16x32_bf16 v[34:37], v[160:163], v[208:211], v[34:37]
	v_mfma_f32_16x16x32_bf16 v[26:29], v[168:171], v[208:211], v[26:29]
	v_mfma_f32_16x16x32_bf16 v[18:21], v[160:163], v[216:219], v[18:21]
	v_mfma_f32_16x16x32_bf16 v[10:13], v[168:171], v[216:219], v[10:13]
	v_mfma_f32_16x16x32_bf16 v[62:65], v[164:167], v[196:199], v[62:65]
	v_mfma_f32_16x16x32_bf16 v[58:61], v[172:175], v[196:199], v[58:61]
	v_mfma_f32_16x16x32_bf16 v[50:53], v[164:167], v[204:207], v[50:53]
	v_mfma_f32_16x16x32_bf16 v[42:45], v[172:175], v[204:207], v[42:45]
	v_mfma_f32_16x16x32_bf16 v[34:37], v[164:167], v[212:215], v[34:37]
	v_mfma_f32_16x16x32_bf16 v[26:29], v[172:175], v[212:215], v[26:29]
	v_mfma_f32_16x16x32_bf16 v[18:21], v[164:167], v[220:223], v[18:21]
	v_mfma_f32_16x16x32_bf16 v[10:13], v[172:175], v[220:223], v[10:13]
	s_setprio 0
	s_setprio 1
	v_mfma_f32_16x16x32_bf16 v[54:57], v[176:179], v[192:195], v[54:57]
	v_mfma_f32_16x16x32_bf16 v[46:49], v[184:187], v[192:195], v[46:49]
	v_mfma_f32_16x16x32_bf16 v[38:41], v[176:179], v[200:203], v[38:41]
	v_mfma_f32_16x16x32_bf16 v[30:33], v[184:187], v[200:203], v[30:33]
	v_mfma_f32_16x16x32_bf16 v[22:25], v[176:179], v[208:211], v[22:25]
	v_mfma_f32_16x16x32_bf16 v[14:17], v[184:187], v[208:211], v[14:17]
	v_mfma_f32_16x16x32_bf16 v[6:9], v[176:179], v[216:219], v[6:9]
	v_mfma_f32_16x16x32_bf16 v[2:5], v[184:187], v[216:219], v[2:5]
	v_mfma_f32_16x16x32_bf16 v[54:57], v[180:183], v[196:199], v[54:57]
	v_mfma_f32_16x16x32_bf16 v[46:49], v[188:191], v[196:199], v[46:49]
	v_mfma_f32_16x16x32_bf16 v[38:41], v[180:183], v[204:207], v[38:41]
	v_mfma_f32_16x16x32_bf16 v[30:33], v[188:191], v[204:207], v[30:33]
	v_mfma_f32_16x16x32_bf16 v[22:25], v[180:183], v[212:215], v[22:25]
	v_mfma_f32_16x16x32_bf16 v[14:17], v[188:191], v[212:215], v[14:17]
	v_mfma_f32_16x16x32_bf16 v[6:9], v[180:183], v[220:223], v[6:9]
	v_mfma_f32_16x16x32_bf16 v[2:5], v[188:191], v[220:223], v[2:5]
	s_setprio 0
	s_barrier
	s_add_i32 s69, s69, 2
	s_add_u32 s67, s67, 0x100
	s_addc_u32 s68, s68, 0
	s_cmp_gt_u32 s69, 53
	s_mov_b64 s[38:39], s[40:41]

; #define PG8_STAGE_A(b, h, ptr, NX) do { if constexpr (Sched::GATHER) { unsigned gs_[2]; gs_[0] = ((NX) && last_) ? gN[h][0] : gA[h][0]; gs_[1] = ((NX) && last_) ? gN[h][1] : gA[h][1]; PG8_STAGE(PG8_SA(b, h), ptr, gs_); } \
;         else PG8_STAGE(PG8_SA(b, h), (ptr) + ((h) ? hstep : (size_t)0), voffA); } while (0)
; #define PG8_STAGE(bufoff, gbase, voff) do { _Pragma("unroll") for (int _i = 0; _i < 2; ++_i) \
;         __builtin_amdgcn_global_load_lds((const unsigned*)((const char*)(gbase) + (voff)[_i]), (PG8_LAS unsigned*)(lds + (bufoff) + ldsw + _i * 8192), 16, 0, 0); } while (0)
; #define PG8_LDA(dst, b, h) do { _Pragma("unroll") for (int m = 0; m < 4; ++m) _Pragma("unroll") for (int k = 0; k < 2; ++k) dst[m][k] = *(const PG8_LAS bf16x8*)(lds + PG8_SA(b, h) + aoff + m * 2048 + k * 1024); } while (0)
; #define PG8_LDB(dst, b, h) do { _Pragma("unroll") for (int n = 0; n < 2; ++n) _Pragma("unroll") for (int k = 0; k < 2; ++k) dst[n][k] = *(const PG8_LAS bf16x8*)(lds + PG8_SB(b, h) + boff + n * 2048 + k * 1024); } while (0)
; #define PG8_MMA(ai, bj, At, Bt) do { __builtin_amdgcn_s_setprio(1); _Pragma("unroll") for (int m = 0; m < 4; ++m) _Pragma("unroll") for (int n = 0; n < 2; ++n) _Pragma("unroll") for (int k = 0; k < 2; ++k) \
;         acc[ai][bj][m][n] = __builtin_amdgcn_mfma_f32_16x16x32_bf16(Bt[n][k], At[m][k], acc[ai][bj][m][n], 0, 0, 0); __builtin_amdgcn_s_setprio(0); } while (0)
; #define PG8_WAIT_V(n) asm volatile("s_waitcnt vmcnt(" #n ")" ::: "memory")
; #define PG8_WAIT_L(n) asm volatile("s_waitcnt lgkmcnt(" #n ")" ::: "memory")
; #define PG8_BAR __builtin_amdgcn_s_barrier()
; #define PG8_SCHED __builtin_amdgcn_sched_barrier(0)
; template <class Epi, class Sched, bool ALIGN_EPI = false, bool SP2 = false>
; __device__ __forceinline__ void gemm_phase(PG8_LAS unsigned char* lds, const Gemm g, const Sched& S, const Epi& E, const bool skip_epi = false) {
;     ...
;             PG8_LDB(B0, 0, 0); PG8_LDB(B1, 0, 1); PG8_SCHED; PG8_LDA(At, 0, 0); PG8_STAGE_A(1, 1, a1, false);
;             PG8_WAIT_V(8); PG8_WAIT_L(0); PG8_BAR; PG8_MMA(0, 0, At, B0); PG8_MMA(0, 1, At, B1); PG8_BAR; PG8_SCHED;
;             PG8_LDA(At, 0, 1); PG8_STAGE(PG8_SB(0, 0), b2, voffB); PG8_STAGE(PG8_SB(0, 1), b2 + hstep, voffB); PG8_STAGE_A(0, 0, a2, true);
.LBB0_1843:
	s_add_u32 s54, s30, 0x100
	s_addc_u32 s55, s31, 0
	s_mov_b32 s56, -2
	ds_read_b128 v[142:145], v150
	ds_read_b128 v[154:157], v150 offset:1024
	ds_read_b128 v[158:161], v150 offset:2048
	ds_read_b128 v[162:165], v150 offset:3072
	ds_read_b128 v[166:169], v151
	ds_read_b128 v[170:173], v151 offset:1024
	ds_read_b128 v[174:177], v151 offset:2048
	ds_read_b128 v[178:181], v151 offset:3072
	s_add_u32 s30, s28, 0x100
	s_addc_u32 s31, s29, 0
	s_cmp_eq_u32 s56, 10
	s_cselect_b32 s37, s7, s31
	s_cselect_b32 s36, s6, s30
	s_cselect_b32 s35, s25, s55
	s_cselect_b32 s34, s24, s54
	v_lshl_add_u64 v[214:215], s[28:29], 0, v[136:137]
	s_add_i32 m0, s38, 0xc000
	ds_read_b128 v[182:185], v152
	ds_read_b128 v[186:189], v152 offset:1024
	ds_read_b128 v[190:193], v152 offset:2048
	ds_read_b128 v[194:197], v152 offset:3072
	ds_read_b128 v[198:201], v152 offset:4096
	ds_read_b128 v[202:205], v152 offset:5120
	ds_read_b128 v[206:209], v152 offset:6144
	ds_read_b128 v[210:213], v152 offset:7168
	global_load_lds_dwordx4 v[214:215], off
	v_lshl_add_u64 v[214:215], s[28:29], 0, v[138:139]
	s_add_i32 m0, s38, 0xe000
	s_nop 0
	global_load_lds_dwordx4 v[214:215], off
	s_waitcnt vmcnt(8)
	s_waitcnt lgkmcnt(0)
	s_barrier
	s_setprio 1
	s_waitcnt lgkmcnt(0)
	v_mfma_f32_16x16x32_bf16 v[126:129], v[142:145], v[182:185], 0
	v_mfma_f32_16x16x32_bf16 v[122:125], v[158:161], v[182:185], 0
	v_mfma_f32_16x16x32_bf16 v[110:113], v[142:145], v[190:193], 0
	v_mfma_f32_16x16x32_bf16 v[106:109], v[158:161], v[190:193], 0
	v_mfma_f32_16x16x32_bf16 v[94:97], v[142:145], v[198:201], 0
	v_mfma_f32_16x16x32_bf16 v[90:93], v[158:161], v[198:201], 0
	v_mfma_f32_16x16x32_bf16 v[78:81], v[142:145], v[206:209], 0
	v_mfma_f32_16x16x32_bf16 v[74:77], v[158:161], v[206:209], 0
	v_mfma_f32_16x16x32_bf16 v[126:129], v[154:157], v[186:189], v[126:129]
	v_mfma_f32_16x16x32_bf16 v[122:125], v[162:165], v[186:189], v[122:125]
	v_mfma_f32_16x16x32_bf16 v[110:113], v[154:157], v[194:197], v[110:113]
	v_mfma_f32_16x16x32_bf16 v[106:109], v[162:165], v[194:197], v[106:109]
	v_mfma_f32_16x16x32_bf16 v[94:97], v[154:157], v[202:205], v[94:97]
	v_mfma_f32_16x16x32_bf16 v[90:93], v[162:165], v[202:205], v[90:93]
	v_mfma_f32_16x16x32_bf16 v[78:81], v[154:157], v[210:213], v[78:81]
	v_mfma_f32_16x16x32_bf16 v[74:77], v[162:165], v[210:213], v[74:77]
	s_setprio 0
	s_setprio 1
	v_mfma_f32_16x16x32_bf16 v[118:121], v[166:169], v[182:185], 0
	v_mfma_f32_16x16x32_bf16 v[114:117], v[174:177], v[182:185], 0
	v_mfma_f32_16x16x32_bf16 v[102:105], v[166:169], v[190:193], 0
	v_mfma_f32_16x16x32_bf16 v[98:101], v[174:177], v[190:193], 0
	v_mfma_f32_16x16x32_bf16 v[86:89], v[166:169], v[198:201], 0
	v_mfma_f32_16x16x32_bf16 v[82:85], v[174:177], v[198:201], 0
	v_mfma_f32_16x16x32_bf16 v[70:73], v[166:169], v[206:209], 0
	v_mfma_f32_16x16x32_bf16 v[66:69], v[174:177], v[206:209], 0
	v_mfma_f32_16x16x32_bf16 v[118:121], v[170:173], v[186:189], v[118:121]
	v_mfma_f32_16x16x32_bf16 v[114:117], v[178:181], v[186:189], v[114:117]
	v_mfma_f32_16x16x32_bf16 v[102:105], v[170:173], v[194:197], v[102:105]
	v_mfma_f32_16x16x32_bf16 v[98:101], v[178:181], v[194:197], v[98:101]
	v_mfma_f32_16x16x32_bf16 v[86:89], v[170:173], v[202:205], v[86:89]
	v_mfma_f32_16x16x32_bf16 v[82:85], v[178:181], v[202:205], v[82:85]
	v_mfma_f32_16x16x32_bf16 v[70:73], v[170:173], v[210:213], v[70:73]
	v_mfma_f32_16x16x32_bf16 v[66:69], v[178:181], v[210:213], v[66:69]
	s_setprio 0
	s_barrier
	s_add_i32 s28, s50, s3
	v_lshl_add_u64 v[214:215], s[34:35], 0, v[132:133]
	s_mov_b32 m0, s28
	ds_read_b128 v[182:185], v152 offset:16384
	ds_read_b128 v[186:189], v152 offset:17408
	ds_read_b128 v[190:193], v152 offset:18432
	ds_read_b128 v[194:197], v152 offset:19456
	ds_read_b128 v[198:201], v152 offset:20480
	ds_read_b128 v[202:205], v152 offset:21504
	ds_read_b128 v[206:209], v152 offset:22528
	ds_read_b128 v[210:213], v152 offset:23552
	global_load_lds_dwordx4 v[214:215], off
	s_add_i32 m0, s28, 0x2000
	s_add_u32 s28, s34, 0xe0000
	v_lshl_add_u64 v[216:217], s[34:35], 0, v[134:135]
	s_addc_u32 s29, s35, 0
	s_add_i32 s57, s51, s3
	global_load_lds_dwordx4 v[216:217], off
	v_lshl_add_u64 v[218:219], s[28:29], 0, v[132:133]
	s_mov_b32 m0, s57
	v_lshl_add_u64 v[220:221], s[36:37], 0, v[134:135]
	global_load_lds_dwordx4 v[218:219], off
	v_lshl_add_u64 v[218:219], s[28:29], 0, v[134:135]
	s_add_i32 m0, s57, 0x2000
	s_nop 0
	global_load_lds_dwordx4 v[218:219], off
	v_lshl_add_u64 v[218:219], s[36:37], 0, v[132:133]
	s_mov_b32 m0, s38
	s_nop 0
	global_load_lds_dwordx4 v[218:219], off
	s_mov_b32 m0, s39
	s_nop 0
	global_load_lds_dwordx4 v[220:221], off
	s_waitcnt vmcnt(8)
	s_waitcnt lgkmcnt(0)
	s_barrier
; #define PG8_STAGE_A(b, h, ptr, NX) do { if constexpr (Sched::GATHER) { unsigned gs_[2]; gs_[0] = ((NX) && last_) ? gN[h][0] : gA[h][0]; gs_[1] = ((NX) && last_) ? gN[h][1] : gA[h][1]; PG8_STAGE(PG8_SA(b, h), ptr, gs_); } \
;         else PG8_STAGE(PG8_SA(b, h), (ptr) + ((h) ? hstep : (size_t)0), voffA); } while (0)
; #define PG8_LDA(dst, b, h) do { _Pragma("unroll") for (int m = 0; m < 4; ++m) _Pragma("unroll") for (int k = 0; k < 2; ++k) dst[m][k] = *(const PG8_LAS bf16x8*)(lds + PG8_SA(b, h) + aoff + m * 2048 + k * 1024); } while (0)
; #define PG8_LDB(dst, b, h) do { _Pragma("unroll") for (int n = 0; n < 2; ++n) _Pragma("unroll") for (int k = 0; k < 2; ++k) dst[n][k] = *(const PG8_LAS bf16x8*)(lds + PG8_SB(b, h) + boff + n * 2048 + k * 1024); } while (0)
; #define PG8_MMA(ai, bj, At, Bt) do { __builtin_amdgcn_s_setprio(1); _Pragma("unroll") for (int m = 0; m < 4; ++m) _Pragma("unroll") for (int n = 0; n < 2; ++n) _Pragma("unroll") for (int k = 0; k < 2; ++k) \
;         acc[ai][bj][m][n] = __builtin_amdgcn_mfma_f32_16x16x32_bf16(Bt[n][k], At[m][k], acc[ai][bj][m][n], 0, 0, 0); __builtin_amdgcn_s_setprio(0); } while (0)
; #define PG8_WAIT_V(n) asm volatile("s_waitcnt vmcnt(" #n ")" ::: "memory")
; #define PG8_WAIT_L(n) asm volatile("s_waitcnt lgkmcnt(" #n ")" ::: "memory")
; #define PG8_BAR __builtin_amdgcn_s_barrier()
; #define PG8_SCHED __builtin_amdgcn_sched_barrier(0)
; template <class Epi, class Sched, bool ALIGN_EPI = false, bool SP2 = false>
; __device__ __forceinline__ void gemm_phase(PG8_LAS unsigned char* lds, const Gemm g, const Sched& S, const Epi& E, const bool skip_epi = false) {
;     ...
;             PG8_WAIT_V(8); PG8_WAIT_L(0); PG8_BAR; PG8_MMA(1, 0, At, B0); PG8_MMA(1, 1, At, B1); PG8_BAR; PG8_SCHED;
;             PG8_LDB(B0, 1, 0); PG8_LDB(B1, 1, 1); PG8_SCHED; PG8_LDA(At, 1, 0); PG8_STAGE_A(0, 1, a2, true);
;             PG8_WAIT_V(8); PG8_WAIT_L(0); PG8_BAR; PG8_MMA(0, 0, At, B0); PG8_MMA(0, 1, At, B1); PG8_BAR; PG8_SCHED;
	s_setprio 1
	s_waitcnt lgkmcnt(0)
	v_mfma_f32_16x16x32_bf16 v[62:65], v[142:145], v[182:185], 0
	v_mfma_f32_16x16x32_bf16 v[58:61], v[158:161], v[182:185], 0
	v_mfma_f32_16x16x32_bf16 v[46:49], v[142:145], v[190:193], 0
	v_mfma_f32_16x16x32_bf16 v[42:45], v[158:161], v[190:193], 0
	v_mfma_f32_16x16x32_bf16 v[30:33], v[142:145], v[198:201], 0
	v_mfma_f32_16x16x32_bf16 v[26:29], v[158:161], v[198:201], 0
	v_mfma_f32_16x16x32_bf16 v[14:17], v[142:145], v[206:209], 0
	v_mfma_f32_16x16x32_bf16 v[10:13], v[158:161], v[206:209], 0
	v_mfma_f32_16x16x32_bf16 v[62:65], v[154:157], v[186:189], v[62:65]
	v_mfma_f32_16x16x32_bf16 v[58:61], v[162:165], v[186:189], v[58:61]
	v_mfma_f32_16x16x32_bf16 v[46:49], v[154:157], v[194:197], v[46:49]
	v_mfma_f32_16x16x32_bf16 v[42:45], v[162:165], v[194:197], v[42:45]
	v_mfma_f32_16x16x32_bf16 v[30:33], v[154:157], v[202:205], v[30:33]
	v_mfma_f32_16x16x32_bf16 v[26:29], v[162:165], v[202:205], v[26:29]
	v_mfma_f32_16x16x32_bf16 v[14:17], v[154:157], v[210:213], v[14:17]
	v_mfma_f32_16x16x32_bf16 v[10:13], v[162:165], v[210:213], v[10:13]
	s_setprio 0
	s_setprio 1
	v_mfma_f32_16x16x32_bf16 v[54:57], v[166:169], v[182:185], 0
	v_mfma_f32_16x16x32_bf16 v[50:53], v[174:177], v[182:185], 0
	v_mfma_f32_16x16x32_bf16 v[38:41], v[166:169], v[190:193], 0
	v_mfma_f32_16x16x32_bf16 v[34:37], v[174:177], v[190:193], 0
	v_mfma_f32_16x16x32_bf16 v[22:25], v[166:169], v[198:201], 0
	v_mfma_f32_16x16x32_bf16 v[18:21], v[174:177], v[198:201], 0
	v_mfma_f32_16x16x32_bf16 v[6:9], v[166:169], v[206:209], 0
	v_mfma_f32_16x16x32_bf16 v[2:5], v[174:177], v[206:209], 0
	v_mfma_f32_16x16x32_bf16 v[54:57], v[170:173], v[186:189], v[54:57]
	v_mfma_f32_16x16x32_bf16 v[50:53], v[178:181], v[186:189], v[50:53]
	v_mfma_f32_16x16x32_bf16 v[38:41], v[170:173], v[194:197], v[38:41]
	v_mfma_f32_16x16x32_bf16 v[34:37], v[178:181], v[194:197], v[34:37]
	v_mfma_f32_16x16x32_bf16 v[22:25], v[170:173], v[202:205], v[22:25]
	v_mfma_f32_16x16x32_bf16 v[18:21], v[178:181], v[202:205], v[18:21]
	v_mfma_f32_16x16x32_bf16 v[6:9], v[170:173], v[210:213], v[6:9]
	v_mfma_f32_16x16x32_bf16 v[2:5], v[178:181], v[210:213], v[2:5]
	s_setprio 0
	s_barrier
	s_add_i32 s57, 0, 0x18000
	v_add_u32_e32 v130, s57, v146
	s_add_i32 s58, 0, 0x1c000
	ds_read_b128 v[142:145], v130
	ds_read_b128 v[154:157], v130 offset:1024
	ds_read_b128 v[158:161], v130 offset:2048
	ds_read_b128 v[162:165], v130 offset:3072
	v_add_u32_e32 v130, s58, v146
	ds_read_b128 v[166:169], v130
	ds_read_b128 v[170:173], v130 offset:1024
	ds_read_b128 v[174:177], v130 offset:2048
	ds_read_b128 v[178:181], v130 offset:3072
	s_add_u32 s28, s36, 0xe0000
	s_addc_u32 s29, s37, 0
	s_mov_b32 m0, s40
	v_lshl_add_u64 v[222:223], s[28:29], 0, v[132:133]
	ds_read_b128 v[182:185], v152 offset:32768
	ds_read_b128 v[186:189], v152 offset:33792
	ds_read_b128 v[190:193], v152 offset:34816
	ds_read_b128 v[194:197], v152 offset:35840
	ds_read_b128 v[198:201], v152 offset:36864
	ds_read_b128 v[202:205], v152 offset:37888
	ds_read_b128 v[206:209], v152 offset:38912
	ds_read_b128 v[210:213], v152 offset:39936
	global_load_lds_dwordx4 v[222:223], off
	v_lshl_add_u64 v[222:223], s[28:29], 0, v[134:135]
	s_mov_b32 m0, s41
	s_nop 0
	global_load_lds_dwordx4 v[222:223], off
	s_waitcnt vmcnt(8)
	s_waitcnt lgkmcnt(0)
	s_barrier
	s_setprio 1
	s_waitcnt lgkmcnt(0)
	v_mfma_f32_16x16x32_bf16 v[126:129], v[142:145], v[182:185], v[126:129]
	v_mfma_f32_16x16x32_bf16 v[122:125], v[158:161], v[182:185], v[122:125]
	v_mfma_f32_16x16x32_bf16 v[110:113], v[142:145], v[190:193], v[110:113]
	v_mfma_f32_16x16x32_bf16 v[106:109], v[158:161], v[190:193], v[106:109]
	v_mfma_f32_16x16x32_bf16 v[94:97], v[142:145], v[198:201], v[94:97]
	v_mfma_f32_16x16x32_bf16 v[90:93], v[158:161], v[198:201], v[90:93]
	v_mfma_f32_16x16x32_bf16 v[78:81], v[142:145], v[206:209], v[78:81]
	v_mfma_f32_16x16x32_bf16 v[74:77], v[158:161], v[206:209], v[74:77]
	v_mfma_f32_16x16x32_bf16 v[126:129], v[154:157], v[186:189], v[126:129]
	v_mfma_f32_16x16x32_bf16 v[122:125], v[162:165], v[186:189], v[122:125]
	v_mfma_f32_16x16x32_bf16 v[110:113], v[154:157], v[194:197], v[110:113]
	v_mfma_f32_16x16x32_bf16 v[106:109], v[162:165], v[194:197], v[106:109]
	v_mfma_f32_16x16x32_bf16 v[94:97], v[154:157], v[202:205], v[94:97]
	v_mfma_f32_16x16x32_bf16 v[90:93], v[162:165], v[202:205], v[90:93]
	v_mfma_f32_16x16x32_bf16 v[78:81], v[154:157], v[210:213], v[78:81]
	v_mfma_f32_16x16x32_bf16 v[74:77], v[162:165], v[210:213], v[74:77]
	s_setprio 0
	s_setprio 1
	v_mfma_f32_16x16x32_bf16 v[118:121], v[166:169], v[182:185], v[118:121]
	v_mfma_f32_16x16x32_bf16 v[114:117], v[174:177], v[182:185], v[114:117]
	v_mfma_f32_16x16x32_bf16 v[102:105], v[166:169], v[190:193], v[102:105]
	v_mfma_f32_16x16x32_bf16 v[98:101], v[174:177], v[190:193], v[98:101]
	v_mfma_f32_16x16x32_bf16 v[86:89], v[166:169], v[198:201], v[86:89]
	v_mfma_f32_16x16x32_bf16 v[82:85], v[174:177], v[198:201], v[82:85]
	v_mfma_f32_16x16x32_bf16 v[70:73], v[166:169], v[206:209], v[70:73]
	v_mfma_f32_16x16x32_bf16 v[66:69], v[174:177], v[206:209], v[66:69]
	v_mfma_f32_16x16x32_bf16 v[118:121], v[170:173], v[186:189], v[118:121]
	v_mfma_f32_16x16x32_bf16 v[114:117], v[178:181], v[186:189], v[114:117]
	v_mfma_f32_16x16x32_bf16 v[102:105], v[170:173], v[194:197], v[102:105]
	v_mfma_f32_16x16x32_bf16 v[98:101], v[178:181], v[194:197], v[98:101]
	v_mfma_f32_16x16x32_bf16 v[86:89], v[170:173], v[202:205], v[86:89]
	v_mfma_f32_16x16x32_bf16 v[82:85], v[178:181], v[202:205], v[82:85]
	v_mfma_f32_16x16x32_bf16 v[70:73], v[170:173], v[210:213], v[70:73]
	v_mfma_f32_16x16x32_bf16 v[66:69], v[178:181], v[210:213], v[66:69]
	s_setprio 0
	s_barrier
; #define PG8_STAGE_A(b, h, ptr, NX) do { if constexpr (Sched::GATHER) { unsigned gs_[2]; gs_[0] = ((NX) && last_) ? gN[h][0] : gA[h][0]; gs_[1] = ((NX) && last_) ? gN[h][1] : gA[h][1]; PG8_STAGE(PG8_SA(b, h), ptr, gs_); } \
;         else PG8_STAGE(PG8_SA(b, h), (ptr) + ((h) ? hstep : (size_t)0), voffA); } while (0)
; #define PG8_STAGE(bufoff, gbase, voff) do { _Pragma("unroll") for (int _i = 0; _i < 2; ++_i) \
;         __builtin_amdgcn_global_load_lds((const unsigned*)((const char*)(gbase) + (voff)[_i]), (PG8_LAS unsigned*)(lds + (bufoff) + ldsw + _i * 8192), 16, 0, 0); } while (0)
; #define PG8_LDA(dst, b, h) do { _Pragma("unroll") for (int m = 0; m < 4; ++m) _Pragma("unroll") for (int k = 0; k < 2; ++k) dst[m][k] = *(const PG8_LAS bf16x8*)(lds + PG8_SA(b, h) + aoff + m * 2048 + k * 1024); } while (0)
; #define PG8_MMA(ai, bj, At, Bt) do { __builtin_amdgcn_s_setprio(1); _Pragma("unroll") for (int m = 0; m < 4; ++m) _Pragma("unroll") for (int n = 0; n < 2; ++n) _Pragma("unroll") for (int k = 0; k < 2; ++k) \
;         acc[ai][bj][m][n] = __builtin_amdgcn_mfma_f32_16x16x32_bf16(Bt[n][k], At[m][k], acc[ai][bj][m][n], 0, 0, 0); __builtin_amdgcn_s_setprio(0); } while (0)
; #define PG8_WAIT_V(n) asm volatile("s_waitcnt vmcnt(" #n ")" ::: "memory")
; #define PG8_WAIT_L(n) asm volatile("s_waitcnt lgkmcnt(" #n ")" ::: "memory")
; #define PG8_BAR __builtin_amdgcn_s_barrier()
; #define PG8_SCHED __builtin_amdgcn_sched_barrier(0)
; template <class Epi, class Sched, bool ALIGN_EPI = false, bool SP2 = false>
; __device__ __forceinline__ void gemm_phase(PG8_LAS unsigned char* lds, const Gemm g, const Sched& S, const Epi& E, const bool skip_epi = false) {
;     ...
;             PG8_LDA(At, 1, 1); PG8_STAGE(PG8_SB(1, 0), b3, voffB); PG8_STAGE(PG8_SB(1, 1), b3 + hstep, voffB); PG8_STAGE_A(1, 0, a3, true);
;             PG8_WAIT_V(8); PG8_WAIT_L(0); PG8_BAR; PG8_MMA(1, 0, At, B0); PG8_MMA(1, 1, At, B1); PG8_BAR; PG8_SCHED;
	s_add_i32 s28, s57, s3
	v_lshl_add_u64 v[214:215], v[214:215], 0, s[18:19]
	s_mov_b32 m0, s28
	ds_read_b128 v[182:185], v152 offset:49152
	ds_read_b128 v[186:189], v152 offset:50176
	ds_read_b128 v[190:193], v152 offset:51200
	ds_read_b128 v[194:197], v152 offset:52224
	ds_read_b128 v[198:201], v152 offset:53248
	ds_read_b128 v[202:205], v152 offset:54272
	ds_read_b128 v[206:209], v152 offset:55296
	ds_read_b128 v[210:213], v152 offset:56320
	global_load_lds_dwordx4 v[214:215], off
	s_add_i32 m0, s28, 0x2000
	s_add_u32 s28, s34, 0xe0080
	v_lshl_add_u64 v[214:215], v[216:217], 0, s[18:19]
	s_addc_u32 s29, s35, 0
	s_add_i32 s34, s58, s3
	global_load_lds_dwordx4 v[214:215], off
	v_lshl_add_u64 v[214:215], s[28:29], 0, v[132:133]
	s_mov_b32 m0, s34
	s_nop 0
	global_load_lds_dwordx4 v[214:215], off
	v_lshl_add_u64 v[214:215], s[28:29], 0, v[134:135]
	s_add_i32 m0, s34, 0x2000
	s_nop 0
	global_load_lds_dwordx4 v[214:215], off
	v_lshl_add_u64 v[214:215], v[218:219], 0, s[18:19]
	s_mov_b32 m0, s46
	s_nop 0
	global_load_lds_dwordx4 v[214:215], off
	v_lshl_add_u64 v[214:215], v[220:221], 0, s[18:19]
	s_mov_b32 m0, s47
	s_nop 0
	global_load_lds_dwordx4 v[214:215], off
	s_waitcnt vmcnt(8)
	s_waitcnt lgkmcnt(0)
	s_barrier
	s_setprio 1
	s_waitcnt lgkmcnt(0)
	v_mfma_f32_16x16x32_bf16 v[62:65], v[142:145], v[182:185], v[62:65]
	v_mfma_f32_16x16x32_bf16 v[58:61], v[158:161], v[182:185], v[58:61]
	v_mfma_f32_16x16x32_bf16 v[46:49], v[142:145], v[190:193], v[46:49]
	v_mfma_f32_16x16x32_bf16 v[42:45], v[158:161], v[190:193], v[42:45]
	v_mfma_f32_16x16x32_bf16 v[30:33], v[142:145], v[198:201], v[30:33]
	v_mfma_f32_16x16x32_bf16 v[26:29], v[158:161], v[198:201], v[26:29]
	v_mfma_f32_16x16x32_bf16 v[14:17], v[142:145], v[206:209], v[14:17]
	v_mfma_f32_16x16x32_bf16 v[10:13], v[158:161], v[206:209], v[10:13]
	v_mfma_f32_16x16x32_bf16 v[62:65], v[154:157], v[186:189], v[62:65]
	v_mfma_f32_16x16x32_bf16 v[58:61], v[162:165], v[186:189], v[58:61]
	v_mfma_f32_16x16x32_bf16 v[46:49], v[154:157], v[194:197], v[46:49]
	v_mfma_f32_16x16x32_bf16 v[42:45], v[162:165], v[194:197], v[42:45]
	v_mfma_f32_16x16x32_bf16 v[30:33], v[154:157], v[202:205], v[30:33]
	v_mfma_f32_16x16x32_bf16 v[26:29], v[162:165], v[202:205], v[26:29]
	v_mfma_f32_16x16x32_bf16 v[14:17], v[154:157], v[210:213], v[14:17]
	v_mfma_f32_16x16x32_bf16 v[10:13], v[162:165], v[210:213], v[10:13]
	s_setprio 0
	s_setprio 1
	v_mfma_f32_16x16x32_bf16 v[54:57], v[166:169], v[182:185], v[54:57]
	v_mfma_f32_16x16x32_bf16 v[50:53], v[174:177], v[182:185], v[50:53]
	v_mfma_f32_16x16x32_bf16 v[38:41], v[166:169], v[190:193], v[38:41]
	v_mfma_f32_16x16x32_bf16 v[34:37], v[174:177], v[190:193], v[34:37]
	v_mfma_f32_16x16x32_bf16 v[22:25], v[166:169], v[198:201], v[22:25]
	v_mfma_f32_16x16x32_bf16 v[18:21], v[174:177], v[198:201], v[18:21]
	v_mfma_f32_16x16x32_bf16 v[6:9], v[166:169], v[206:209], v[6:9]
	v_mfma_f32_16x16x32_bf16 v[2:5], v[174:177], v[206:209], v[2:5]
	v_mfma_f32_16x16x32_bf16 v[54:57], v[170:173], v[186:189], v[54:57]
	v_mfma_f32_16x16x32_bf16 v[50:53], v[178:181], v[186:189], v[50:53]
	v_mfma_f32_16x16x32_bf16 v[38:41], v[170:173], v[194:197], v[38:41]
	v_mfma_f32_16x16x32_bf16 v[34:37], v[178:181], v[194:197], v[34:37]
	v_mfma_f32_16x16x32_bf16 v[22:25], v[170:173], v[202:205], v[22:25]
	v_mfma_f32_16x16x32_bf16 v[18:21], v[178:181], v[202:205], v[18:21]
	v_mfma_f32_16x16x32_bf16 v[6:9], v[170:173], v[210:213], v[6:9]
	v_mfma_f32_16x16x32_bf16 v[2:5], v[178:181], v[210:213], v[2:5]
	s_setprio 0
	s_barrier
	s_add_i32 s56, s56, 2
	s_add_u32 s54, s54, 0x100
	s_addc_u32 s55, s55, 0
	s_cmp_gt_u32 s56, 11
	s_mov_b64 s[28:29], s[30:31]
